# v27 + GEMM K-loops: per-phase vmcnt(10) waits (each LDS-DMA stage waited one phase before first read) instead of vmcnt(6) twice per iteration
# baseline (speedup 1.0000x reference)
.LBB0_351:
	s_add_i32 s10, s38, 0xfffc0080
	s_cmp_eq_u32 s40, 12
	s_cselect_b32 s43, s6, s10
	s_cselect_b32 s41, s7, s39
	s_add_i32 s10, 0, 0x10000
	v_add_u32_e32 v135, s10, v131
	v_add_u32_e32 v218, s10, v132
	ds_read_b128 v[136:139], v135
	ds_read_b128 v[144:147], v135 offset:2048
	ds_read_b128 v[140:143], v218
	ds_read_b128 v[148:151], v218 offset:2048
	s_or_b32 s42, s43, 0x80
	s_mov_b32 m0, s27
	ds_read_b128 v[152:155], v133
	ds_read_b128 v[168:171], v133 offset:2048
	ds_read_b128 v[156:159], v134
	ds_read_b128 v[172:175], v134 offset:2048
	ds_read_b128 v[176:179], v133 offset:4096
	ds_read_b128 v[184:187], v133 offset:6144
	ds_read_b128 v[180:183], v134 offset:4096
	ds_read_b128 v[188:191], v134 offset:6144
	buffer_load_dwordx4 v96, s[72:75], s38 offen lds
	s_mov_b32 m0, s28
	s_nop 0
	buffer_load_dwordx4 v130, s[72:75], s38 offen lds
	s_waitcnt lgkmcnt(8)
	s_waitcnt vmcnt(10)
	s_barrier
	s_waitcnt lgkmcnt(0)
	s_setprio 1
	s_waitcnt lgkmcnt(5)
	v_mfma_scale_f32_16x16x128_f8f6f4 v[126:129], v[136:143], v[152:159], v[126:129], v212, v212 op_sel_hi:[0,0,0]
	v_mfma_scale_f32_16x16x128_f8f6f4 v[122:125], v[144:151], v[152:159], v[122:125], v212, v212 op_sel_hi:[0,0,0]
	s_waitcnt lgkmcnt(4)
	v_mfma_scale_f32_16x16x128_f8f6f4 v[118:121], v[136:143], v[168:175], v[118:121], v212, v212 op_sel_hi:[0,0,0]
	v_mfma_scale_f32_16x16x128_f8f6f4 v[114:117], v[144:151], v[168:175], v[114:117], v212, v212 op_sel_hi:[0,0,0]
	s_waitcnt lgkmcnt(1)
	v_mfma_scale_f32_16x16x128_f8f6f4 v[160:163], v[136:143], v[176:183], v[102:105], v212, v212 op_sel_hi:[0,0,0]
	v_mfma_scale_f32_16x16x128_f8f6f4 v[192:195], v[144:151], v[176:183], v[98:101], v212, v212 op_sel_hi:[0,0,0]
	s_waitcnt lgkmcnt(0)
	v_mfma_scale_f32_16x16x128_f8f6f4 v[196:199], v[136:143], v[184:191], v[84:87], v212, v212 op_sel_hi:[0,0,0]
	v_mfma_scale_f32_16x16x128_f8f6f4 v[200:203], v[144:151], v[184:191], v[80:83], v212, v212 op_sel_hi:[0,0,0]
	s_setprio 0
	s_barrier
	s_mov_b32 s10, s74
	s_mov_b32 s11, s75
	s_mov_b32 m0, s13
	s_nop 1
	ds_read_b128 v[80:83], v135 offset:16384
	ds_read_b128 v[98:101], v135 offset:18432
	ds_read_b128 v[84:87], v218 offset:16384
	ds_read_b128 v[102:105], v218 offset:18432
	buffer_load_dwordx4 v96, s[8:11], s41 offen lds
	s_mov_b32 m0, s14
	s_nop 0
	buffer_load_dwordx4 v130, s[8:11], s41 offen lds
	s_waitcnt vmcnt(10)
	s_barrier
	s_waitcnt lgkmcnt(0)
	s_setprio 1
	s_waitcnt lgkmcnt(1)
	v_mfma_scale_f32_16x16x128_f8f6f4 v[204:207], v[80:87], v[152:159], v[110:113], v212, v212 op_sel_hi:[0,0,0]
	s_waitcnt lgkmcnt(0)
	v_mfma_scale_f32_16x16x128_f8f6f4 v[152:155], v[98:105], v[152:159], v[106:109], v212, v212 op_sel_hi:[0,0,0]
	v_mfma_scale_f32_16x16x128_f8f6f4 v[156:159], v[80:87], v[168:175], v[92:95], v212, v212 op_sel_hi:[0,0,0]
	v_mfma_scale_f32_16x16x128_f8f6f4 v[168:171], v[98:105], v[168:175], v[88:91], v212, v212 op_sel_hi:[0,0,0]
	v_mfma_scale_f32_16x16x128_f8f6f4 v[172:175], v[80:87], v[176:183], v[76:79], v212, v212 op_sel_hi:[0,0,0]
	v_mfma_scale_f32_16x16x128_f8f6f4 v[176:179], v[98:105], v[176:183], v[72:75], v212, v212 op_sel_hi:[0,0,0]
	v_mfma_scale_f32_16x16x128_f8f6f4 v[180:183], v[80:87], v[184:191], v[68:71], v212, v212 op_sel_hi:[0,0,0]
	v_mfma_scale_f32_16x16x128_f8f6f4 v[184:187], v[98:105], v[184:191], v[16:19], v212, v212 op_sel_hi:[0,0,0]
	s_setprio 0
	s_mov_b32 m0, s12
	s_barrier
	ds_read_b128 v[64:67], v133 offset:16384
	s_nop 0
	ds_read_b128 v[72:75], v133 offset:18432
	ds_read_b128 v[68:71], v134 offset:16384
	ds_read_b128 v[76:79], v134 offset:18432
	ds_read_b128 v[88:91], v133 offset:20480
	ds_read_b128 v[106:109], v133 offset:22528
	ds_read_b128 v[92:95], v134 offset:20480
	ds_read_b128 v[110:113], v134 offset:22528
	buffer_load_dwordx4 v96, s[72:75], s43 offen lds
	s_mov_b32 m0, s15
	s_nop 0
	buffer_load_dwordx4 v130, s[72:75], s43 offen lds
	s_barrier
	s_waitcnt lgkmcnt(0)
	s_setprio 1
	s_waitcnt lgkmcnt(5)
	v_mfma_scale_f32_16x16x128_f8f6f4 v[60:63], v[136:143], v[64:71], v[60:63], v212, v212 op_sel_hi:[0,0,0]
	v_mfma_scale_f32_16x16x128_f8f6f4 v[56:59], v[144:151], v[64:71], v[56:59], v212, v212 op_sel_hi:[0,0,0]
	s_waitcnt lgkmcnt(4)
	v_mfma_scale_f32_16x16x128_f8f6f4 v[52:55], v[136:143], v[72:79], v[52:55], v212, v212 op_sel_hi:[0,0,0]
	v_mfma_scale_f32_16x16x128_f8f6f4 v[228:231], v[144:151], v[72:79], v[44:47], v212, v212 op_sel_hi:[0,0,0]
	s_waitcnt lgkmcnt(1)
	v_mfma_scale_f32_16x16x128_f8f6f4 v[232:235], v[136:143], v[88:95], v[36:39], v212, v212 op_sel_hi:[0,0,0]
	v_mfma_scale_f32_16x16x128_f8f6f4 v[236:239], v[144:151], v[88:95], v[28:31], v212, v212 op_sel_hi:[0,0,0]
	s_waitcnt lgkmcnt(0)
	v_mfma_scale_f32_16x16x128_f8f6f4 v[240:243], v[136:143], v[106:113], v[20:23], v212, v212 op_sel_hi:[0,0,0]
	v_mfma_scale_f32_16x16x128_f8f6f4 v[244:247], v[144:151], v[106:113], v[12:15], v212, v212 op_sel_hi:[0,0,0]
	s_setprio 0
	s_barrier
	s_add_i32 s44, s41, 0x40000
	s_mov_b32 m0, s16
	s_nop 0
	buffer_load_dwordx4 v96, s[8:11], s44 offen lds
	s_mov_b32 m0, s17
	s_nop 0
	buffer_load_dwordx4 v130, s[8:11], s44 offen lds
	s_waitcnt vmcnt(10)
	s_barrier
	s_setprio 1
	v_mfma_scale_f32_16x16x128_f8f6f4 v[48:51], v[80:87], v[64:71], v[48:51], v212, v212 op_sel_hi:[0,0,0]
	v_mfma_scale_f32_16x16x128_f8f6f4 v[208:211], v[80:87], v[88:95], v[208:211], v212, v212 op_sel_hi:[0,0,0]
	v_mfma_scale_f32_16x16x128_f8f6f4 v[248:251], v[98:105], v[64:71], v[40:43], v212, v212 op_sel_hi:[0,0,0]
	v_mfma_scale_f32_16x16x128_f8f6f4 v[164:167], v[80:87], v[72:79], v[32:35], v212, v212 op_sel_hi:[0,0,0]
	v_mfma_scale_f32_16x16x128_f8f6f4 v[224:227], v[98:105], v[72:79], v[24:27], v212, v212 op_sel_hi:[0,0,0]
	v_mfma_scale_f32_16x16x128_f8f6f4 v[214:217], v[98:105], v[88:95], v[8:11], v212, v212 op_sel_hi:[0,0,0]
	v_mfma_scale_f32_16x16x128_f8f6f4 v[220:223], v[80:87], v[106:113], v[4:7], v212, v212 op_sel_hi:[0,0,0]
	v_mfma_scale_f32_16x16x128_f8f6f4 v[64:67], v[98:105], v[106:113], v[0:3], v212, v212 op_sel_hi:[0,0,0]
	s_setprio 0
	s_barrier
	s_nop 4
	ds_read_b128 v[0:3], v135 offset:32768
	ds_read_b128 v[8:11], v135 offset:34816
	ds_read_b128 v[4:7], v218 offset:32768
	ds_read_b128 v[12:15], v218 offset:34816
	s_add_i32 s43, s43, 0x40000
	s_mov_b32 m0, s18
	ds_read_b128 v[16:19], v133 offset:32768
	ds_read_b128 v[24:27], v133 offset:34816
	ds_read_b128 v[20:23], v134 offset:32768
	ds_read_b128 v[28:31], v134 offset:34816
	ds_read_b128 v[32:35], v133 offset:36864
	ds_read_b128 v[40:43], v133 offset:38912
	ds_read_b128 v[36:39], v134 offset:36864
	ds_read_b128 v[44:47], v134 offset:38912
	buffer_load_dwordx4 v96, s[72:75], s43 offen lds
	s_mov_b32 m0, s19
	s_nop 0
	buffer_load_dwordx4 v130, s[72:75], s43 offen lds
	s_waitcnt lgkmcnt(8)
	s_waitcnt vmcnt(10)
	s_barrier
	s_waitcnt lgkmcnt(0)
	s_setprio 1
	s_waitcnt lgkmcnt(5)
	v_mfma_scale_f32_16x16x128_f8f6f4 v[126:129], v[0:7], v[16:23], v[126:129], v212, v212 op_sel_hi:[0,0,0]
	v_mfma_scale_f32_16x16x128_f8f6f4 v[122:125], v[8:15], v[16:23], v[122:125], v212, v212 op_sel_hi:[0,0,0]
	s_waitcnt lgkmcnt(4)
	v_mfma_scale_f32_16x16x128_f8f6f4 v[118:121], v[0:7], v[24:31], v[118:121], v212, v212 op_sel_hi:[0,0,0]
	v_mfma_scale_f32_16x16x128_f8f6f4 v[114:117], v[8:15], v[24:31], v[114:117], v212, v212 op_sel_hi:[0,0,0]
	s_waitcnt lgkmcnt(1)
	v_mfma_scale_f32_16x16x128_f8f6f4 v[102:105], v[0:7], v[32:39], v[160:163], v212, v212 op_sel_hi:[0,0,0]
	v_mfma_scale_f32_16x16x128_f8f6f4 v[98:101], v[8:15], v[32:39], v[192:195], v212, v212 op_sel_hi:[0,0,0]
	s_waitcnt lgkmcnt(0)
	v_mfma_scale_f32_16x16x128_f8f6f4 v[84:87], v[0:7], v[40:47], v[196:199], v212, v212 op_sel_hi:[0,0,0]
	v_mfma_scale_f32_16x16x128_f8f6f4 v[80:83], v[8:15], v[40:47], v[200:203], v212, v212 op_sel_hi:[0,0,0]
	s_setprio 0
	s_barrier
	s_or_b32 s43, s41, 0x80
	s_mov_b32 m0, s22
	ds_read_b128 v[136:139], v135 offset:49152
	ds_read_b128 v[144:147], v135 offset:51200
	ds_read_b128 v[140:143], v218 offset:49152
	ds_read_b128 v[148:151], v218 offset:51200
	buffer_load_dwordx4 v96, s[8:11], s43 offen lds
	s_mov_b32 m0, s2
	s_nop 0
	buffer_load_dwordx4 v130, s[8:11], s43 offen lds
	s_waitcnt vmcnt(10)
	s_barrier
	s_waitcnt lgkmcnt(0)
	s_setprio 1
	s_waitcnt lgkmcnt(1)
	v_mfma_scale_f32_16x16x128_f8f6f4 v[110:113], v[136:143], v[16:23], v[204:207], v212, v212 op_sel_hi:[0,0,0]
	s_waitcnt lgkmcnt(0)
	v_mfma_scale_f32_16x16x128_f8f6f4 v[106:109], v[144:151], v[16:23], v[152:155], v212, v212 op_sel_hi:[0,0,0]
	v_mfma_scale_f32_16x16x128_f8f6f4 v[92:95], v[136:143], v[24:31], v[156:159], v212, v212 op_sel_hi:[0,0,0]
	v_mfma_scale_f32_16x16x128_f8f6f4 v[88:91], v[144:151], v[24:31], v[168:171], v212, v212 op_sel_hi:[0,0,0]
	v_mfma_scale_f32_16x16x128_f8f6f4 v[76:79], v[136:143], v[32:39], v[172:175], v212, v212 op_sel_hi:[0,0,0]
	v_mfma_scale_f32_16x16x128_f8f6f4 v[72:75], v[144:151], v[32:39], v[176:179], v212, v212 op_sel_hi:[0,0,0]
	v_mfma_scale_f32_16x16x128_f8f6f4 v[68:71], v[136:143], v[40:47], v[180:183], v212, v212 op_sel_hi:[0,0,0]
	v_mfma_scale_f32_16x16x128_f8f6f4 v[16:19], v[144:151], v[40:47], v[184:187], v212, v212 op_sel_hi:[0,0,0]
	s_setprio 0
	s_mov_b32 m0, s23
	s_barrier
	ds_read_b128 v[152:155], v133 offset:49152
	ds_read_b128 v[168:171], v133 offset:51200
	ds_read_b128 v[156:159], v134 offset:49152
	ds_read_b128 v[172:175], v134 offset:51200
	ds_read_b128 v[176:179], v133 offset:53248
	ds_read_b128 v[184:187], v133 offset:55296
	ds_read_b128 v[180:183], v134 offset:53248
	ds_read_b128 v[188:191], v134 offset:55296
	buffer_load_dwordx4 v96, s[72:75], s42 offen lds
	s_mov_b32 m0, s24
	s_nop 0
	buffer_load_dwordx4 v130, s[72:75], s42 offen lds
	s_barrier
	s_waitcnt lgkmcnt(0)
	s_setprio 1
	s_waitcnt lgkmcnt(5)
	v_mfma_scale_f32_16x16x128_f8f6f4 v[60:63], v[0:7], v[152:159], v[60:63], v212, v212 op_sel_hi:[0,0,0]
	v_mfma_scale_f32_16x16x128_f8f6f4 v[56:59], v[8:15], v[152:159], v[56:59], v212, v212 op_sel_hi:[0,0,0]
	s_waitcnt lgkmcnt(4)
	v_mfma_scale_f32_16x16x128_f8f6f4 v[52:55], v[0:7], v[168:175], v[52:55], v212, v212 op_sel_hi:[0,0,0]
	v_mfma_scale_f32_16x16x128_f8f6f4 v[44:47], v[8:15], v[168:175], v[228:231], v212, v212 op_sel_hi:[0,0,0]
	s_waitcnt lgkmcnt(1)
	v_mfma_scale_f32_16x16x128_f8f6f4 v[36:39], v[0:7], v[176:183], v[232:235], v212, v212 op_sel_hi:[0,0,0]
	v_mfma_scale_f32_16x16x128_f8f6f4 v[28:31], v[8:15], v[176:183], v[236:239], v212, v212 op_sel_hi:[0,0,0]
	s_waitcnt lgkmcnt(0)
	v_mfma_scale_f32_16x16x128_f8f6f4 v[20:23], v[0:7], v[184:191], v[240:243], v212, v212 op_sel_hi:[0,0,0]
	v_mfma_scale_f32_16x16x128_f8f6f4 v[12:15], v[8:15], v[184:191], v[244:247], v212, v212 op_sel_hi:[0,0,0]
	s_setprio 0
	s_barrier
	s_add_i32 s41, s41, 0x40080
	s_mov_b32 m0, s25
	s_nop 0
	buffer_load_dwordx4 v96, s[8:11], s41 offen lds
	s_mov_b32 m0, s26
	s_nop 0
	buffer_load_dwordx4 v130, s[8:11], s41 offen lds
	s_waitcnt vmcnt(10)
	s_barrier
	s_setprio 1
	v_mfma_scale_f32_16x16x128_f8f6f4 v[48:51], v[136:143], v[152:159], v[48:51], v212, v212 op_sel_hi:[0,0,0]
	v_mfma_scale_f32_16x16x128_f8f6f4 v[40:43], v[144:151], v[152:159], v[248:251], v212, v212 op_sel_hi:[0,0,0]
	v_mfma_scale_f32_16x16x128_f8f6f4 v[32:35], v[136:143], v[168:175], v[164:167], v212, v212 op_sel_hi:[0,0,0]
	v_mfma_scale_f32_16x16x128_f8f6f4 v[24:27], v[144:151], v[168:175], v[224:227], v212, v212 op_sel_hi:[0,0,0]
	v_mfma_scale_f32_16x16x128_f8f6f4 v[208:211], v[136:143], v[176:183], v[208:211], v212, v212 op_sel_hi:[0,0,0]
	v_mfma_scale_f32_16x16x128_f8f6f4 v[8:11], v[144:151], v[176:183], v[214:217], v212, v212 op_sel_hi:[0,0,0]
	v_mfma_scale_f32_16x16x128_f8f6f4 v[4:7], v[136:143], v[184:191], v[220:223], v212, v212 op_sel_hi:[0,0,0]
	v_mfma_scale_f32_16x16x128_f8f6f4 v[0:3], v[144:151], v[184:191], v[64:67], v212, v212 op_sel_hi:[0,0,0]
	s_setprio 0
	s_add_i32 s40, s40, 2
	s_addk_i32 s38, 0x100
	s_addk_i32 s39, 0x100
	s_cmp_gt_u32 s40, 13
	s_barrier
	s_cbranch_scc0 .LBB0_351
	s_getreg_b32 s6, hwreg(HW_REG_HW_ID, 0, 6)
	s_and_b32 s6, s6, 63
	s_lshl_b32 s6, s6, 2
	s_add_i32 s6, s6, 0
	s_add_i32 s6, s6, 0x20010
	v_mov_b32_e32 v64, s6
	ds_read_b32 v64, v64
	s_lshl_b32 s6, s37, 8
	s_mul_i32 s7, s37, 0x300000
	v_mbcnt_lo_u32_b32 v65, -1, 0
	v_mbcnt_hi_u32_b32 v65, -1, v65
	s_mul_hi_i32 s6, s6, 0x3000
	s_waitcnt lgkmcnt(0)
	v_readfirstlane_b32 s10, v64
	v_and_b32_e32 v66, 15, v65
	v_pk_mul_f32 v[18:19], v[18:19], s[78:79] op_sel_hi:[1,0]
	v_lshl_or_b32 v135, s10, 6, v65
	s_add_u32 s10, s20, s7
	s_addc_u32 s11, s21, s6
	s_lshl_b32 s6, s36, 8
	s_ashr_i32 s7, s6, 31
	s_lshl_b64 s[6:7], s[6:7], 1
	s_add_u32 s6, s10, s6
	v_lshrrev_b32_e32 v64, 2, v135
	s_mov_b32 s10, 0xfffc0
	v_and_or_b32 v136, v64, s10, v66
	v_pk_mul_f32 v[64:65], v[128:129], s[78:79] op_sel_hi:[1,0]
	v_pk_mul_f32 v[66:67], v[126:127], s[78:79] op_sel_hi:[1,0]
	v_pk_mul_f32 v[126:127], v[124:125], s[78:79] op_sel_hi:[1,0]
	v_pk_mul_f32 v[124:125], v[122:123], s[78:79] op_sel_hi:[1,0]
	v_cvt_pk_bf16_f32 v123, v64, v65
	v_mul_u32_u24_e32 v64, 0x3000, v136
	s_movk_i32 s10, 0xf0
	v_cvt_pk_bf16_f32 v122, v66, v67
	v_cvt_pk_bf16_f32 v124, v124, v125
	v_cvt_pk_bf16_f32 v125, v126, v127
	v_and_or_b32 v126, v135, s10, v64
	v_pk_mul_f32 v[64:65], v[112:113], s[78:79] op_sel_hi:[1,0]
	v_pk_mul_f32 v[66:67], v[110:111], s[78:79] op_sel_hi:[1,0]
	v_pk_mul_f32 v[110:111], v[108:109], s[78:79] op_sel_hi:[1,0]
	v_pk_mul_f32 v[108:109], v[106:107], s[78:79] op_sel_hi:[1,0]
	s_addc_u32 s7, s11, s7
	v_cvt_pk_bf16_f32 v106, v66, v67
	v_cvt_pk_bf16_f32 v107, v64, v65
	v_cvt_pk_bf16_f32 v108, v108, v109
	v_cvt_pk_bf16_f32 v109, v110, v111
	global_store_dwordx4 v126, v[106:109], s[6:7] offset:256
	v_pk_mul_f32 v[64:65], v[120:121], s[78:79] op_sel_hi:[1,0]
	v_pk_mul_f32 v[66:67], v[118:119], s[78:79] op_sel_hi:[1,0]
	v_pk_mul_f32 v[110:111], v[116:117], s[78:79] op_sel_hi:[1,0]
	v_pk_mul_f32 v[108:109], v[114:115], s[78:79] op_sel_hi:[1,0]
	v_cvt_pk_bf16_f32 v106, v66, v67
	v_cvt_pk_bf16_f32 v107, v64, v65
	v_cvt_pk_bf16_f32 v108, v108, v109
	v_cvt_pk_bf16_f32 v109, v110, v111
	v_add_u32_e32 v64, 0x30000, v126
	global_store_dwordx4 v64, v[106:109], s[6:7]
	v_pk_mul_f32 v[64:65], v[94:95], s[78:79] op_sel_hi:[1,0]
	v_pk_mul_f32 v[66:67], v[92:93], s[78:79] op_sel_hi:[1,0]
	v_pk_mul_f32 v[92:93], v[90:91], s[78:79] op_sel_hi:[1,0]
	v_pk_mul_f32 v[90:91], v[88:89], s[78:79] op_sel_hi:[1,0]
	v_cvt_pk_bf16_f32 v88, v66, v67
	v_cvt_pk_bf16_f32 v89, v64, v65
	v_cvt_pk_bf16_f32 v90, v90, v91
	v_cvt_pk_bf16_f32 v91, v92, v93
	v_add_u32_e32 v64, 0x30100, v126
	global_store_dwordx4 v126, v[122:125], s[6:7]
	global_store_dwordx4 v64, v[88:91], s[6:7]
	v_pk_mul_f32 v[64:65], v[104:105], s[78:79] op_sel_hi:[1,0]
	v_pk_mul_f32 v[66:67], v[102:103], s[78:79] op_sel_hi:[1,0]
	v_pk_mul_f32 v[92:93], v[100:101], s[78:79] op_sel_hi:[1,0]
	v_pk_mul_f32 v[90:91], v[98:99], s[78:79] op_sel_hi:[1,0]
	v_cvt_pk_bf16_f32 v88, v66, v67
	v_cvt_pk_bf16_f32 v89, v64, v65
	v_cvt_pk_bf16_f32 v90, v90, v91
	v_cvt_pk_bf16_f32 v91, v92, v93
	v_add_u32_e32 v64, 0x60000, v126
	global_store_dwordx4 v64, v[88:91], s[6:7]
	v_pk_mul_f32 v[64:65], v[78:79], s[78:79] op_sel_hi:[1,0]
	v_pk_mul_f32 v[66:67], v[76:77], s[78:79] op_sel_hi:[1,0]
	v_pk_mul_f32 v[76:77], v[74:75], s[78:79] op_sel_hi:[1,0]
	v_pk_mul_f32 v[74:75], v[72:73], s[78:79] op_sel_hi:[1,0]
	v_cvt_pk_bf16_f32 v72, v66, v67
	v_cvt_pk_bf16_f32 v73, v64, v65
	v_cvt_pk_bf16_f32 v74, v74, v75
	v_cvt_pk_bf16_f32 v75, v76, v77
	v_add_u32_e32 v64, 0x60100, v126
	global_store_dwordx4 v64, v[72:75], s[6:7]
	v_pk_mul_f32 v[64:65], v[86:87], s[78:79] op_sel_hi:[1,0]
	v_pk_mul_f32 v[66:67], v[84:85], s[78:79] op_sel_hi:[1,0]
	v_cvt_pk_bf16_f32 v73, v64, v65
	v_cvt_pk_bf16_f32 v72, v66, v67
	v_pk_mul_f32 v[66:67], v[70:71], s[78:79] op_sel_hi:[1,0]
	v_pk_mul_f32 v[64:65], v[68:69], s[78:79] op_sel_hi:[1,0]
	v_pk_mul_f32 v[16:17], v[16:17], s[78:79] op_sel_hi:[1,0]
	v_pk_mul_f32 v[76:77], v[82:83], s[78:79] op_sel_hi:[1,0]
	v_pk_mul_f32 v[74:75], v[80:81], s[78:79] op_sel_hi:[1,0]
	v_cvt_pk_bf16_f32 v64, v64, v65
	v_cvt_pk_bf16_f32 v65, v66, v67
	v_cvt_pk_bf16_f32 v66, v16, v17
	v_cvt_pk_bf16_f32 v67, v18, v19
	v_pk_mul_f32 v[16:17], v[62:63], s[78:79] op_sel_hi:[1,0]
	v_pk_mul_f32 v[18:19], v[60:61], s[78:79] op_sel_hi:[1,0]
	v_pk_mul_f32 v[60:61], v[58:59], s[78:79] op_sel_hi:[1,0]
	v_pk_mul_f32 v[58:59], v[56:57], s[78:79] op_sel_hi:[1,0]
	v_cvt_pk_bf16_f32 v74, v74, v75
	v_cvt_pk_bf16_f32 v75, v76, v77
	v_add_u32_e32 v76, 0x90000, v126
	v_cvt_pk_bf16_f32 v56, v18, v19
	v_cvt_pk_bf16_f32 v57, v16, v17
	v_cvt_pk_bf16_f32 v58, v58, v59
	v_cvt_pk_bf16_f32 v59, v60, v61
	v_add_u32_e32 v16, 0x180000, v126
	global_store_dwordx4 v76, v[72:75], s[6:7]
	global_store_dwordx4 v76, v[64:67], s[6:7] offset:256
	global_store_dwordx4 v16, v[56:59], s[6:7]
	v_pk_mul_f32 v[16:17], v[50:51], s[78:79] op_sel_hi:[1,0]
	v_pk_mul_f32 v[18:19], v[48:49], s[78:79] op_sel_hi:[1,0]
	v_pk_mul_f32 v[48:49], v[42:43], s[78:79] op_sel_hi:[1,0]
	v_pk_mul_f32 v[42:43], v[40:41], s[78:79] op_sel_hi:[1,0]
	v_cvt_pk_bf16_f32 v40, v18, v19
	v_cvt_pk_bf16_f32 v41, v16, v17
	v_cvt_pk_bf16_f32 v42, v42, v43
	v_cvt_pk_bf16_f32 v43, v48, v49
	v_add_u32_e32 v16, 0x180100, v126
	global_store_dwordx4 v16, v[40:43], s[6:7]
	v_pk_mul_f32 v[16:17], v[54:55], s[78:79] op_sel_hi:[1,0]
	v_pk_mul_f32 v[18:19], v[52:53], s[78:79] op_sel_hi:[1,0]
	v_cvt_pk_bf16_f32 v41, v16, v17
	v_cvt_pk_bf16_f32 v40, v18, v19
	v_pk_mul_f32 v[16:17], v[34:35], s[78:79] op_sel_hi:[1,0]
	v_pk_mul_f32 v[18:19], v[32:33], s[78:79] op_sel_hi:[1,0]
	v_pk_mul_f32 v[32:33], v[26:27], s[78:79] op_sel_hi:[1,0]
	v_pk_mul_f32 v[26:27], v[24:25], s[78:79] op_sel_hi:[1,0]
	v_pk_mul_f32 v[42:43], v[44:45], s[78:79] op_sel_hi:[1,0]
	v_add_u32_e32 v44, 0x1b0000, v126
	v_cvt_pk_bf16_f32 v24, v18, v19
	v_cvt_pk_bf16_f32 v25, v16, v17
	v_cvt_pk_bf16_f32 v26, v26, v27
	v_cvt_pk_bf16_f32 v27, v32, v33
	v_pk_mul_f32 v[46:47], v[46:47], s[78:79] op_sel_hi:[1,0]
	global_store_dwordx4 v44, v[24:27], s[6:7] offset:256
	v_pk_mul_f32 v[16:17], v[38:39], s[78:79] op_sel_hi:[1,0]
	v_pk_mul_f32 v[18:19], v[36:37], s[78:79] op_sel_hi:[1,0]
	v_pk_mul_f32 v[30:31], v[30:31], s[78:79] op_sel_hi:[1,0]
	v_pk_mul_f32 v[26:27], v[28:29], s[78:79] op_sel_hi:[1,0]
	v_cvt_pk_bf16_f32 v42, v42, v43
	v_cvt_pk_bf16_f32 v43, v46, v47
	v_cvt_pk_bf16_f32 v24, v18, v19
	v_cvt_pk_bf16_f32 v25, v16, v17
	v_cvt_pk_bf16_f32 v26, v26, v27
	v_cvt_pk_bf16_f32 v27, v30, v31
	v_add_u32_e32 v28, 0x1e0000, v126
	global_store_dwordx4 v44, v[40:43], s[6:7]
	global_store_dwordx4 v28, v[24:27], s[6:7]
	v_pk_mul_f32 v[16:17], v[210:211], s[78:79] op_sel_hi:[1,0]
	v_pk_mul_f32 v[18:19], v[208:209], s[78:79] op_sel_hi:[1,0]
	v_pk_mul_f32 v[24:25], v[10:11], s[78:79] op_sel_hi:[1,0]
	v_pk_mul_f32 v[10:11], v[8:9], s[78:79] op_sel_hi:[1,0]
	v_cvt_pk_bf16_f32 v8, v18, v19
	v_cvt_pk_bf16_f32 v9, v16, v17
	v_cvt_pk_bf16_f32 v10, v10, v11
	v_cvt_pk_bf16_f32 v11, v24, v25
	global_store_dwordx4 v28, v[8:11], s[6:7] offset:256
	v_pk_mul_f32 v[14:15], v[14:15], s[78:79] op_sel_hi:[1,0]
	v_pk_mul_f32 v[12:13], v[12:13], s[78:79] op_sel_hi:[1,0]
	v_pk_mul_f32 v[10:11], v[22:23], s[78:79] op_sel_hi:[1,0]
	v_pk_mul_f32 v[8:9], v[20:21], s[78:79] op_sel_hi:[1,0]
	v_pk_mul_f32 v[6:7], v[6:7], s[78:79] op_sel_hi:[1,0]
	v_cvt_pk_bf16_f32 v8, v8, v9
	v_cvt_pk_bf16_f32 v9, v10, v11
	v_cvt_pk_bf16_f32 v10, v12, v13
	v_cvt_pk_bf16_f32 v11, v14, v15
	v_add_u32_e32 v12, 0x210000, v126
	global_store_dwordx4 v12, v[8:11], s[6:7]
	v_pk_mul_f32 v[4:5], v[4:5], s[78:79] op_sel_hi:[1,0]
	s_and_b64 vcc, exec, s[4:5]
	v_pk_mul_f32 v[8:9], v[2:3], s[78:79] op_sel_hi:[1,0]
	v_pk_mul_f32 v[2:3], v[0:1], s[78:79] op_sel_hi:[1,0]
	v_cvt_pk_bf16_f32 v0, v4, v5
	v_cvt_pk_bf16_f32 v1, v6, v7
	v_cvt_pk_bf16_f32 v2, v2, v3
	v_cvt_pk_bf16_f32 v3, v8, v9
	s_mov_b32 s36, s30
	s_mov_b32 s37, s31
	s_mov_b32 s39, s35
	s_mov_b32 s10, s34
	v_mov_b32_e32 v242, v252
	v_mov_b32_e32 v252, v213
	v_mov_b32_e32 v213, 0x358637bd
	global_store_dwordx4 v12, v[0:3], s[6:7] offset:256
	s_cbranch_vccz .LBB0_344
	s_waitcnt vmcnt(0)
	s_cmpk_gt_u32 s0, 0xff
	s_cbranch_scc1 .LBB0_355
	s_barrier

.LBB0_484:
	ds_read_b128 v[136:139], v133
	ds_read_b128 v[140:143], v133 offset:1024
	ds_read_b128 v[144:147], v133 offset:2048
	ds_read_b128 v[148:151], v133 offset:3072
	s_add_i32 s10, s42, 0xffe80080
	s_cmp_eq_u32 s44, 4
	s_cselect_b32 s47, s6, s10
	s_cselect_b32 s45, s7, s43
	s_or_b32 s46, s47, 0x80
	s_mov_b32 m0, s31
	ds_read_b128 v[152:155], v134
	ds_read_b128 v[156:159], v134 offset:1024
	ds_read_b128 v[160:163], v134 offset:2048
	ds_read_b128 v[164:167], v134 offset:3072
	ds_read_b128 v[168:171], v134 offset:4096
	ds_read_b128 v[172:175], v134 offset:5120
	ds_read_b128 v[176:179], v134 offset:6144
	ds_read_b128 v[180:183], v134 offset:7168
	buffer_load_dwordx4 v96, s[72:75], s42 offen lds
	s_mov_b32 m0, s34
	s_nop 0
	buffer_load_dwordx4 v131, s[72:75], s42 offen lds
	s_waitcnt lgkmcnt(8)
	s_waitcnt vmcnt(10)
	s_barrier
	s_waitcnt lgkmcnt(0)
	s_setprio 1
	s_waitcnt lgkmcnt(7)
	v_mfma_f32_16x16x32_bf16 v[126:129], v[136:139], v[152:155], v[126:129]
	v_mfma_f32_16x16x32_bf16 v[122:125], v[144:147], v[152:155], v[122:125]
	s_waitcnt lgkmcnt(5)
	v_mfma_f32_16x16x32_bf16 v[118:121], v[136:139], v[160:163], v[118:121]
	v_mfma_f32_16x16x32_bf16 v[114:117], v[144:147], v[160:163], v[114:117]
	s_waitcnt lgkmcnt(3)
	v_mfma_f32_16x16x32_bf16 v[102:105], v[136:139], v[168:171], v[102:105]
	v_mfma_f32_16x16x32_bf16 v[98:101], v[144:147], v[168:171], v[98:101]
	s_waitcnt lgkmcnt(1)
	v_mfma_f32_16x16x32_bf16 v[84:87], v[136:139], v[176:179], v[84:87]
	v_mfma_f32_16x16x32_bf16 v[80:83], v[144:147], v[176:179], v[80:83]
	v_mfma_f32_16x16x32_bf16 v[126:129], v[140:143], v[156:159], v[126:129]
	v_mfma_f32_16x16x32_bf16 v[122:125], v[148:151], v[156:159], v[122:125]
	v_mfma_f32_16x16x32_bf16 v[118:121], v[140:143], v[164:167], v[118:121]
	v_mfma_f32_16x16x32_bf16 v[114:117], v[148:151], v[164:167], v[114:117]
	v_mfma_f32_16x16x32_bf16 v[102:105], v[140:143], v[172:175], v[102:105]
	v_mfma_f32_16x16x32_bf16 v[98:101], v[148:151], v[172:175], v[98:101]
	s_waitcnt lgkmcnt(0)
	v_mfma_f32_16x16x32_bf16 v[84:87], v[140:143], v[180:183], v[84:87]
	v_mfma_f32_16x16x32_bf16 v[80:83], v[148:151], v[180:183], v[80:83]
	s_setprio 0
	s_barrier
	s_mov_b32 s10, s74
	s_mov_b32 s11, s75
	s_mov_b32 m0, s16
	ds_read_b128 v[184:187], v133 offset:16384
	ds_read_b128 v[188:191], v133 offset:17408
	ds_read_b128 v[192:195], v133 offset:18432
	ds_read_b128 v[196:199], v133 offset:19456
	buffer_load_dwordx4 v130, s[8:11], s45 offen lds
	s_mov_b32 m0, s17
	s_nop 0
	buffer_load_dwordx4 v132, s[8:11], s45 offen lds
	s_waitcnt vmcnt(10)
	s_barrier
	s_waitcnt lgkmcnt(0)
	s_setprio 1
	s_waitcnt lgkmcnt(3)
	v_mfma_f32_16x16x32_bf16 v[110:113], v[184:187], v[152:155], v[110:113]
	s_waitcnt lgkmcnt(1)
	v_mfma_f32_16x16x32_bf16 v[106:109], v[192:195], v[152:155], v[106:109]
	v_mfma_f32_16x16x32_bf16 v[92:95], v[184:187], v[160:163], v[92:95]
	v_mfma_f32_16x16x32_bf16 v[88:91], v[192:195], v[160:163], v[88:91]
	v_mfma_f32_16x16x32_bf16 v[76:79], v[184:187], v[168:171], v[76:79]
	v_mfma_f32_16x16x32_bf16 v[72:75], v[192:195], v[168:171], v[72:75]
	v_mfma_f32_16x16x32_bf16 v[68:71], v[184:187], v[176:179], v[68:71]
	v_mfma_f32_16x16x32_bf16 v[64:67], v[192:195], v[176:179], v[64:67]
	v_mfma_f32_16x16x32_bf16 v[110:113], v[188:191], v[156:159], v[110:113]
	s_waitcnt lgkmcnt(0)
	v_mfma_f32_16x16x32_bf16 v[106:109], v[196:199], v[156:159], v[106:109]
	v_mfma_f32_16x16x32_bf16 v[92:95], v[188:191], v[164:167], v[92:95]
	v_mfma_f32_16x16x32_bf16 v[88:91], v[196:199], v[164:167], v[88:91]
	v_mfma_f32_16x16x32_bf16 v[76:79], v[188:191], v[172:175], v[76:79]
	v_mfma_f32_16x16x32_bf16 v[72:75], v[196:199], v[172:175], v[72:75]
	v_mfma_f32_16x16x32_bf16 v[68:71], v[188:191], v[180:183], v[68:71]
	v_mfma_f32_16x16x32_bf16 v[64:67], v[196:199], v[180:183], v[64:67]
	s_setprio 0
	s_mov_b32 m0, s15
	s_barrier
	ds_read_b128 v[152:155], v134 offset:16384
	ds_read_b128 v[156:159], v134 offset:17408
	ds_read_b128 v[160:163], v134 offset:18432
	ds_read_b128 v[164:167], v134 offset:19456
	ds_read_b128 v[168:171], v134 offset:20480
	ds_read_b128 v[172:175], v134 offset:21504
	ds_read_b128 v[176:179], v134 offset:22528
	ds_read_b128 v[180:183], v134 offset:23552
	buffer_load_dwordx4 v96, s[72:75], s47 offen lds
	s_mov_b32 m0, s18
	s_nop 0
	buffer_load_dwordx4 v131, s[72:75], s47 offen lds
	s_barrier
	s_waitcnt lgkmcnt(0)
	s_setprio 1
	s_waitcnt lgkmcnt(7)
	v_mfma_f32_16x16x32_bf16 v[60:63], v[136:139], v[152:155], v[60:63]
	v_mfma_f32_16x16x32_bf16 v[56:59], v[144:147], v[152:155], v[56:59]
	s_waitcnt lgkmcnt(5)
	v_mfma_f32_16x16x32_bf16 v[52:55], v[136:139], v[160:163], v[52:55]
	v_mfma_f32_16x16x32_bf16 v[48:51], v[144:147], v[160:163], v[48:51]
	s_waitcnt lgkmcnt(3)
	v_mfma_f32_16x16x32_bf16 v[36:39], v[136:139], v[168:171], v[36:39]
	v_mfma_f32_16x16x32_bf16 v[32:35], v[144:147], v[168:171], v[32:35]
	s_waitcnt lgkmcnt(1)
	v_mfma_f32_16x16x32_bf16 v[20:23], v[136:139], v[176:179], v[20:23]
	v_mfma_f32_16x16x32_bf16 v[16:19], v[144:147], v[176:179], v[16:19]
	v_mfma_f32_16x16x32_bf16 v[60:63], v[140:143], v[156:159], v[60:63]
	v_mfma_f32_16x16x32_bf16 v[56:59], v[148:151], v[156:159], v[56:59]
	v_mfma_f32_16x16x32_bf16 v[52:55], v[140:143], v[164:167], v[52:55]
	v_mfma_f32_16x16x32_bf16 v[48:51], v[148:151], v[164:167], v[48:51]
	v_mfma_f32_16x16x32_bf16 v[36:39], v[140:143], v[172:175], v[36:39]
	v_mfma_f32_16x16x32_bf16 v[32:35], v[148:151], v[172:175], v[32:35]
	s_waitcnt lgkmcnt(0)
	v_mfma_f32_16x16x32_bf16 v[20:23], v[140:143], v[180:183], v[20:23]
	v_mfma_f32_16x16x32_bf16 v[16:19], v[148:151], v[180:183], v[16:19]
	s_setprio 0
	s_barrier
	s_add_i32 s48, s45, 0x20000
	s_mov_b32 m0, s19
	s_nop 0
	buffer_load_dwordx4 v130, s[8:11], s48 offen lds
	s_mov_b32 m0, s20
	s_nop 0
	buffer_load_dwordx4 v132, s[8:11], s48 offen lds
	s_waitcnt vmcnt(10)
	s_barrier
	s_setprio 1
	v_mfma_f32_16x16x32_bf16 v[44:47], v[184:187], v[152:155], v[44:47]
	v_mfma_f32_16x16x32_bf16 v[40:43], v[192:195], v[152:155], v[40:43]
	v_mfma_f32_16x16x32_bf16 v[28:31], v[184:187], v[160:163], v[28:31]
	v_mfma_f32_16x16x32_bf16 v[24:27], v[192:195], v[160:163], v[24:27]
	v_mfma_f32_16x16x32_bf16 v[12:15], v[184:187], v[168:171], v[12:15]
	v_mfma_f32_16x16x32_bf16 v[8:11], v[192:195], v[168:171], v[8:11]
	v_mfma_f32_16x16x32_bf16 v[4:7], v[184:187], v[176:179], v[4:7]
	v_mfma_f32_16x16x32_bf16 v[0:3], v[192:195], v[176:179], v[0:3]
	v_mfma_f32_16x16x32_bf16 v[44:47], v[188:191], v[156:159], v[44:47]
	v_mfma_f32_16x16x32_bf16 v[40:43], v[196:199], v[156:159], v[40:43]
	v_mfma_f32_16x16x32_bf16 v[28:31], v[188:191], v[164:167], v[28:31]
	v_mfma_f32_16x16x32_bf16 v[24:27], v[196:199], v[164:167], v[24:27]
	v_mfma_f32_16x16x32_bf16 v[12:15], v[188:191], v[172:175], v[12:15]
	v_mfma_f32_16x16x32_bf16 v[8:11], v[196:199], v[172:175], v[8:11]
	v_mfma_f32_16x16x32_bf16 v[4:7], v[188:191], v[180:183], v[4:7]
	v_mfma_f32_16x16x32_bf16 v[0:3], v[196:199], v[180:183], v[0:3]
	s_setprio 0
	s_barrier
	ds_read_b128 v[136:139], v133 offset:32768
	ds_read_b128 v[140:143], v133 offset:33792
	ds_read_b128 v[144:147], v133 offset:34816
	ds_read_b128 v[148:151], v133 offset:35840
	s_add_i32 s47, s47, 0x180000
	s_mov_b32 m0, s21
	ds_read_b128 v[152:155], v134 offset:32768
	ds_read_b128 v[156:159], v134 offset:33792
	ds_read_b128 v[160:163], v134 offset:34816
	ds_read_b128 v[164:167], v134 offset:35840
	ds_read_b128 v[168:171], v134 offset:36864
	ds_read_b128 v[172:175], v134 offset:37888
	ds_read_b128 v[176:179], v134 offset:38912
	ds_read_b128 v[180:183], v134 offset:39936
	buffer_load_dwordx4 v96, s[72:75], s47 offen lds
	s_mov_b32 m0, s22
	s_nop 0
	buffer_load_dwordx4 v131, s[72:75], s47 offen lds
	s_waitcnt lgkmcnt(8)
	s_waitcnt vmcnt(10)
	s_barrier
	s_waitcnt lgkmcnt(0)
	s_setprio 1
	s_waitcnt lgkmcnt(7)
	v_mfma_f32_16x16x32_bf16 v[126:129], v[136:139], v[152:155], v[126:129]
	v_mfma_f32_16x16x32_bf16 v[122:125], v[144:147], v[152:155], v[122:125]
	s_waitcnt lgkmcnt(5)
	v_mfma_f32_16x16x32_bf16 v[118:121], v[136:139], v[160:163], v[118:121]
	v_mfma_f32_16x16x32_bf16 v[114:117], v[144:147], v[160:163], v[114:117]
	s_waitcnt lgkmcnt(3)
	v_mfma_f32_16x16x32_bf16 v[102:105], v[136:139], v[168:171], v[102:105]
	v_mfma_f32_16x16x32_bf16 v[98:101], v[144:147], v[168:171], v[98:101]
	s_waitcnt lgkmcnt(1)
	v_mfma_f32_16x16x32_bf16 v[84:87], v[136:139], v[176:179], v[84:87]
	v_mfma_f32_16x16x32_bf16 v[80:83], v[144:147], v[176:179], v[80:83]
	v_mfma_f32_16x16x32_bf16 v[126:129], v[140:143], v[156:159], v[126:129]
	v_mfma_f32_16x16x32_bf16 v[122:125], v[148:151], v[156:159], v[122:125]
	v_mfma_f32_16x16x32_bf16 v[118:121], v[140:143], v[164:167], v[118:121]
	v_mfma_f32_16x16x32_bf16 v[114:117], v[148:151], v[164:167], v[114:117]
	v_mfma_f32_16x16x32_bf16 v[102:105], v[140:143], v[172:175], v[102:105]
	v_mfma_f32_16x16x32_bf16 v[98:101], v[148:151], v[172:175], v[98:101]
	s_waitcnt lgkmcnt(0)
	v_mfma_f32_16x16x32_bf16 v[84:87], v[140:143], v[180:183], v[84:87]
	v_mfma_f32_16x16x32_bf16 v[80:83], v[148:151], v[180:183], v[80:83]
	s_setprio 0
	s_barrier
	s_or_b32 s47, s45, 0x80
	s_mov_b32 m0, s25
	ds_read_b128 v[184:187], v133 offset:49152
	ds_read_b128 v[188:191], v133 offset:50176
	ds_read_b128 v[192:195], v133 offset:51200
	ds_read_b128 v[196:199], v133 offset:52224
	buffer_load_dwordx4 v130, s[8:11], s47 offen lds
	s_mov_b32 m0, s26
	s_nop 0
	buffer_load_dwordx4 v132, s[8:11], s47 offen lds
	s_waitcnt vmcnt(10)
	s_barrier
	s_waitcnt lgkmcnt(0)
	s_setprio 1
	s_waitcnt lgkmcnt(3)
	v_mfma_f32_16x16x32_bf16 v[110:113], v[184:187], v[152:155], v[110:113]
	s_waitcnt lgkmcnt(1)
	v_mfma_f32_16x16x32_bf16 v[106:109], v[192:195], v[152:155], v[106:109]
	v_mfma_f32_16x16x32_bf16 v[92:95], v[184:187], v[160:163], v[92:95]
	v_mfma_f32_16x16x32_bf16 v[88:91], v[192:195], v[160:163], v[88:91]
	v_mfma_f32_16x16x32_bf16 v[76:79], v[184:187], v[168:171], v[76:79]
	v_mfma_f32_16x16x32_bf16 v[72:75], v[192:195], v[168:171], v[72:75]
	v_mfma_f32_16x16x32_bf16 v[68:71], v[184:187], v[176:179], v[68:71]
	v_mfma_f32_16x16x32_bf16 v[64:67], v[192:195], v[176:179], v[64:67]
	v_mfma_f32_16x16x32_bf16 v[110:113], v[188:191], v[156:159], v[110:113]
	s_waitcnt lgkmcnt(0)
	v_mfma_f32_16x16x32_bf16 v[106:109], v[196:199], v[156:159], v[106:109]
	v_mfma_f32_16x16x32_bf16 v[92:95], v[188:191], v[164:167], v[92:95]
	v_mfma_f32_16x16x32_bf16 v[88:91], v[196:199], v[164:167], v[88:91]
	v_mfma_f32_16x16x32_bf16 v[76:79], v[188:191], v[172:175], v[76:79]
	v_mfma_f32_16x16x32_bf16 v[72:75], v[196:199], v[172:175], v[72:75]
	v_mfma_f32_16x16x32_bf16 v[68:71], v[188:191], v[180:183], v[68:71]
	v_mfma_f32_16x16x32_bf16 v[64:67], v[196:199], v[180:183], v[64:67]
	s_setprio 0
	s_mov_b32 m0, s27
	s_barrier
	ds_read_b128 v[152:155], v134 offset:49152
	ds_read_b128 v[156:159], v134 offset:50176
	ds_read_b128 v[160:163], v134 offset:51200
	ds_read_b128 v[164:167], v134 offset:52224
	ds_read_b128 v[168:171], v134 offset:53248
	ds_read_b128 v[172:175], v134 offset:54272
	ds_read_b128 v[176:179], v134 offset:55296
	ds_read_b128 v[180:183], v134 offset:56320
	buffer_load_dwordx4 v96, s[72:75], s46 offen lds
	s_mov_b32 m0, s28
	s_nop 0
	buffer_load_dwordx4 v131, s[72:75], s46 offen lds
	s_barrier
	s_waitcnt lgkmcnt(0)
	s_setprio 1
	s_waitcnt lgkmcnt(7)
	v_mfma_f32_16x16x32_bf16 v[60:63], v[136:139], v[152:155], v[60:63]
	v_mfma_f32_16x16x32_bf16 v[56:59], v[144:147], v[152:155], v[56:59]
	s_waitcnt lgkmcnt(5)
	v_mfma_f32_16x16x32_bf16 v[52:55], v[136:139], v[160:163], v[52:55]
	v_mfma_f32_16x16x32_bf16 v[48:51], v[144:147], v[160:163], v[48:51]
	s_waitcnt lgkmcnt(3)
	v_mfma_f32_16x16x32_bf16 v[36:39], v[136:139], v[168:171], v[36:39]
	v_mfma_f32_16x16x32_bf16 v[32:35], v[144:147], v[168:171], v[32:35]
	s_waitcnt lgkmcnt(1)
	v_mfma_f32_16x16x32_bf16 v[20:23], v[136:139], v[176:179], v[20:23]
	v_mfma_f32_16x16x32_bf16 v[16:19], v[144:147], v[176:179], v[16:19]
	v_mfma_f32_16x16x32_bf16 v[60:63], v[140:143], v[156:159], v[60:63]
	v_mfma_f32_16x16x32_bf16 v[56:59], v[148:151], v[156:159], v[56:59]
	v_mfma_f32_16x16x32_bf16 v[52:55], v[140:143], v[164:167], v[52:55]
	v_mfma_f32_16x16x32_bf16 v[48:51], v[148:151], v[164:167], v[48:51]
	v_mfma_f32_16x16x32_bf16 v[36:39], v[140:143], v[172:175], v[36:39]
	v_mfma_f32_16x16x32_bf16 v[32:35], v[148:151], v[172:175], v[32:35]
	s_waitcnt lgkmcnt(0)
	v_mfma_f32_16x16x32_bf16 v[20:23], v[140:143], v[180:183], v[20:23]
	v_mfma_f32_16x16x32_bf16 v[16:19], v[148:151], v[180:183], v[16:19]
	s_setprio 0
	s_barrier
	s_add_i32 s45, s45, 0x20080
	s_mov_b32 m0, s29
	s_nop 0
	buffer_load_dwordx4 v130, s[8:11], s45 offen lds
	s_mov_b32 m0, s30
	s_nop 0
	buffer_load_dwordx4 v132, s[8:11], s45 offen lds
	s_waitcnt vmcnt(10)
	s_barrier
	s_setprio 1
	v_mfma_f32_16x16x32_bf16 v[44:47], v[184:187], v[152:155], v[44:47]
	v_mfma_f32_16x16x32_bf16 v[40:43], v[192:195], v[152:155], v[40:43]
	v_mfma_f32_16x16x32_bf16 v[28:31], v[184:187], v[160:163], v[28:31]
	v_mfma_f32_16x16x32_bf16 v[24:27], v[192:195], v[160:163], v[24:27]
	v_mfma_f32_16x16x32_bf16 v[12:15], v[184:187], v[168:171], v[12:15]
	v_mfma_f32_16x16x32_bf16 v[8:11], v[192:195], v[168:171], v[8:11]
	v_mfma_f32_16x16x32_bf16 v[4:7], v[184:187], v[176:179], v[4:7]
	v_mfma_f32_16x16x32_bf16 v[0:3], v[192:195], v[176:179], v[0:3]
	v_mfma_f32_16x16x32_bf16 v[44:47], v[188:191], v[156:159], v[44:47]
	v_mfma_f32_16x16x32_bf16 v[40:43], v[196:199], v[156:159], v[40:43]
	v_mfma_f32_16x16x32_bf16 v[28:31], v[188:191], v[164:167], v[28:31]
	v_mfma_f32_16x16x32_bf16 v[24:27], v[196:199], v[164:167], v[24:27]
	v_mfma_f32_16x16x32_bf16 v[12:15], v[188:191], v[172:175], v[12:15]
	v_mfma_f32_16x16x32_bf16 v[8:11], v[196:199], v[172:175], v[8:11]
	v_mfma_f32_16x16x32_bf16 v[4:7], v[188:191], v[180:183], v[4:7]
	v_mfma_f32_16x16x32_bf16 v[0:3], v[196:199], v[180:183], v[0:3]
	s_setprio 0
	s_add_i32 s44, s44, 2
	s_addk_i32 s42, 0x100
	s_addk_i32 s43, 0x100
	s_cmp_gt_u32 s44, 5
	s_barrier
	s_cbranch_scc0 .LBB0_484
	s_getreg_b32 s6, hwreg(HW_REG_HW_ID, 0, 6)
	s_and_b32 s6, s6, 63
	s_lshl_b32 s6, s6, 2
	s_add_i32 s6, s6, 0
	s_add_i32 s6, s6, 0x20010
	v_mov_b32_e32 v135, s6
	ds_read_b32 v135, v135
	s_lshl_b32 s6, s41, 8
	s_mul_i32 s7, s41, 0x60000
	v_mbcnt_lo_u32_b32 v136, -1, 0
	v_mbcnt_hi_u32_b32 v136, -1, v136
	s_mul_hi_i32 s6, s6, 0x600
	s_waitcnt lgkmcnt(0)
	v_readfirstlane_b32 s10, v135
	v_and_b32_e32 v137, 15, v136
	v_cvt_pk_bf16_f32 v126, v126, v127
	v_lshl_or_b32 v135, s10, 6, v136
	s_add_u32 s10, s23, s7
	s_addc_u32 s11, s24, s6
	s_lshl_b32 s6, s40, 8
	s_ashr_i32 s7, s6, 31
	s_lshl_b64 s[6:7], s[6:7], 1
	s_add_u32 s6, s10, s6
	v_lshrrev_b32_e32 v136, 2, v135
	s_mov_b32 s10, 0x7fffc0
	v_and_or_b32 v136, v136, s10, v137
	v_cvt_pk_bf16_f32 v127, v128, v129
	v_cvt_pk_bf16_f32 v128, v122, v123
	v_mul_u32_u24_e32 v122, 0x600, v136
	s_movk_i32 s10, 0xf0
	s_addc_u32 s7, s11, s7
	v_and_or_b32 v122, v135, s10, v122
	v_cvt_pk_bf16_f32 v110, v110, v111
	v_cvt_pk_bf16_f32 v111, v112, v113
	v_cvt_pk_bf16_f32 v112, v106, v107
	v_cvt_pk_bf16_f32 v113, v108, v109
	v_cvt_pk_bf16_f32 v129, v124, v125
	global_store_dwordx4 v122, v[110:113], s[6:7] offset:256
	v_cvt_pk_bf16_f32 v106, v118, v119
	v_cvt_pk_bf16_f32 v107, v120, v121
	v_cvt_pk_bf16_f32 v108, v114, v115
	v_cvt_pk_bf16_f32 v109, v116, v117
	v_add_u32_e32 v110, 0x6000, v122
	v_cvt_pk_bf16_f32 v92, v92, v93
	v_cvt_pk_bf16_f32 v93, v94, v95
	v_cvt_pk_bf16_f32 v94, v88, v89
	v_cvt_pk_bf16_f32 v95, v90, v91
	v_add_u32_e32 v88, 0x6100, v122
	global_store_dwordx4 v122, v[126:129], s[6:7]
	global_store_dwordx4 v110, v[106:109], s[6:7]
	global_store_dwordx4 v88, v[92:95], s[6:7]
	v_cvt_pk_bf16_f32 v88, v102, v103
	v_cvt_pk_bf16_f32 v89, v104, v105
	v_cvt_pk_bf16_f32 v90, v98, v99
	v_cvt_pk_bf16_f32 v91, v100, v101
	v_add_u32_e32 v92, 0xc000, v122
	v_cvt_pk_bf16_f32 v76, v76, v77
	v_cvt_pk_bf16_f32 v77, v78, v79
	v_cvt_pk_bf16_f32 v78, v72, v73
	v_cvt_pk_bf16_f32 v79, v74, v75
	v_add_u32_e32 v72, 0xc100, v122
	global_store_dwordx4 v92, v[88:91], s[6:7]
	global_store_dwordx4 v72, v[76:79], s[6:7]
	v_cvt_pk_bf16_f32 v72, v84, v85
	v_cvt_pk_bf16_f32 v73, v86, v87
	v_cvt_pk_bf16_f32 v74, v80, v81
	v_cvt_pk_bf16_f32 v75, v82, v83
	v_add_u32_e32 v76, 0x12000, v122
	v_cvt_pk_bf16_f32 v68, v68, v69
	v_cvt_pk_bf16_f32 v69, v70, v71
	v_cvt_pk_bf16_f32 v70, v64, v65
	v_cvt_pk_bf16_f32 v71, v66, v67
	v_cvt_pk_bf16_f32 v60, v60, v61
	v_cvt_pk_bf16_f32 v61, v62, v63
	v_cvt_pk_bf16_f32 v62, v56, v57
	v_cvt_pk_bf16_f32 v63, v58, v59
	v_add_u32_e32 v56, 0x30000, v122
	v_cvt_pk_bf16_f32 v44, v44, v45
	v_cvt_pk_bf16_f32 v45, v46, v47
	v_cvt_pk_bf16_f32 v46, v40, v41
	v_cvt_pk_bf16_f32 v47, v42, v43
	v_add_u32_e32 v40, 0x30100, v122
	global_store_dwordx4 v76, v[72:75], s[6:7]
	global_store_dwordx4 v76, v[68:71], s[6:7] offset:256
	global_store_dwordx4 v56, v[60:63], s[6:7]
	global_store_dwordx4 v40, v[44:47], s[6:7]
	v_cvt_pk_bf16_f32 v28, v28, v29
	v_cvt_pk_bf16_f32 v29, v30, v31
	v_add_u32_e32 v44, 0x36000, v122
	v_cvt_pk_bf16_f32 v30, v24, v25
	v_cvt_pk_bf16_f32 v31, v26, v27
	v_cvt_pk_bf16_f32 v40, v52, v53
	v_cvt_pk_bf16_f32 v41, v54, v55
	v_cvt_pk_bf16_f32 v42, v48, v49
	v_cvt_pk_bf16_f32 v43, v50, v51
	global_store_dwordx4 v44, v[28:31], s[6:7] offset:256
	v_cvt_pk_bf16_f32 v12, v12, v13
	v_cvt_pk_bf16_f32 v13, v14, v15
	v_add_u32_e32 v28, 0x3c000, v122
	v_cvt_pk_bf16_f32 v14, v8, v9
	v_cvt_pk_bf16_f32 v15, v10, v11
	global_store_dwordx4 v44, v[40:43], s[6:7]
	v_cvt_pk_bf16_f32 v24, v36, v37
	v_cvt_pk_bf16_f32 v25, v38, v39
	v_cvt_pk_bf16_f32 v26, v32, v33
	v_cvt_pk_bf16_f32 v27, v34, v35
	global_store_dwordx4 v28, v[12:15], s[6:7] offset:256
	v_cvt_pk_bf16_f32 v8, v20, v21
	v_cvt_pk_bf16_f32 v9, v22, v23
	v_cvt_pk_bf16_f32 v10, v16, v17
	v_cvt_pk_bf16_f32 v11, v18, v19
	v_add_u32_e32 v12, 0x42000, v122
	v_cvt_pk_bf16_f32 v4, v4, v5
	v_cvt_pk_bf16_f32 v5, v6, v7
	v_cvt_pk_bf16_f32 v6, v0, v1
	v_cvt_pk_bf16_f32 v7, v2, v3
	s_and_b64 vcc, exec, s[4:5]
	s_mov_b32 s40, s36
	s_mov_b32 s41, s37
	s_mov_b32 s10, s39
	s_mov_b32 s11, s38
	global_store_dwordx4 v28, v[24:27], s[6:7]
	global_store_dwordx4 v12, v[8:11], s[6:7]
	global_store_dwordx4 v12, v[4:7], s[6:7] offset:256
	s_cbranch_vccz .LBB0_481
	s_waitcnt vmcnt(0)
	s_cmpk_gt_u32 s14, 0xff
	s_cbranch_scc1 .LBB0_488
	s_barrier

.LBB0_1358:
	ds_read_b128 v[138:141], v135
	ds_read_b128 v[142:145], v135 offset:1024
	ds_read_b128 v[146:149], v135 offset:2048
	ds_read_b128 v[150:153], v135 offset:3072
	s_add_i32 s10, s45, 0xfff80080
	s_cmp_eq_u32 s47, 4
	s_cselect_b32 s50, s15, s10
	s_cselect_b32 s48, s44, s46
	s_add_i32 s49, s50, 0x80
	s_mov_b32 m0, s38
	ds_read_b128 v[154:157], v136
	ds_read_b128 v[158:161], v136 offset:1024
	ds_read_b128 v[162:165], v136 offset:2048
	ds_read_b128 v[166:169], v136 offset:3072
	ds_read_b128 v[170:173], v136 offset:4096
	ds_read_b128 v[174:177], v136 offset:5120
	ds_read_b128 v[178:181], v136 offset:6144
	ds_read_b128 v[182:185], v136 offset:7168
	buffer_load_dwordx4 v131, s[72:75], s45 offen lds
	s_mov_b32 m0, s39
	s_nop 0
	buffer_load_dwordx4 v133, s[72:75], s45 offen lds
	s_waitcnt lgkmcnt(8)
	s_waitcnt vmcnt(10)
	s_barrier
	s_waitcnt lgkmcnt(0)
	s_setprio 1
	s_waitcnt lgkmcnt(7)
	v_mfma_f32_16x16x32_bf16 v[126:129], v[138:141], v[154:157], v[126:129]
	v_mfma_f32_16x16x32_bf16 v[122:125], v[146:149], v[154:157], v[122:125]
	s_waitcnt lgkmcnt(5)
	v_mfma_f32_16x16x32_bf16 v[118:121], v[138:141], v[162:165], v[118:121]
	v_mfma_f32_16x16x32_bf16 v[114:117], v[146:149], v[162:165], v[114:117]
	s_waitcnt lgkmcnt(3)
	v_mfma_f32_16x16x32_bf16 v[102:105], v[138:141], v[170:173], v[102:105]
	v_mfma_f32_16x16x32_bf16 v[98:101], v[146:149], v[170:173], v[98:101]
	s_waitcnt lgkmcnt(1)
	v_mfma_f32_16x16x32_bf16 v[84:87], v[138:141], v[178:181], v[84:87]
	v_mfma_f32_16x16x32_bf16 v[80:83], v[146:149], v[178:181], v[80:83]
	v_mfma_f32_16x16x32_bf16 v[126:129], v[142:145], v[158:161], v[126:129]
	v_mfma_f32_16x16x32_bf16 v[122:125], v[150:153], v[158:161], v[122:125]
	v_mfma_f32_16x16x32_bf16 v[118:121], v[142:145], v[166:169], v[118:121]
	v_mfma_f32_16x16x32_bf16 v[114:117], v[150:153], v[166:169], v[114:117]
	v_mfma_f32_16x16x32_bf16 v[102:105], v[142:145], v[174:177], v[102:105]
	v_mfma_f32_16x16x32_bf16 v[98:101], v[150:153], v[174:177], v[98:101]
	s_waitcnt lgkmcnt(0)
	v_mfma_f32_16x16x32_bf16 v[84:87], v[142:145], v[182:185], v[84:87]
	v_mfma_f32_16x16x32_bf16 v[80:83], v[150:153], v[182:185], v[80:83]
	s_setprio 0
	s_barrier
	s_mov_b32 s10, s74
	s_mov_b32 s11, s75
	s_mov_b32 m0, s21
	ds_read_b128 v[186:189], v135 offset:16384
	ds_read_b128 v[190:193], v135 offset:17408
	ds_read_b128 v[194:197], v135 offset:18432
	ds_read_b128 v[198:201], v135 offset:19456
	buffer_load_dwordx4 v132, s[8:11], s48 offen lds
	s_mov_b32 m0, s22
	s_nop 0
	buffer_load_dwordx4 v134, s[8:11], s48 offen lds
	s_waitcnt vmcnt(10)
	s_barrier
	s_waitcnt lgkmcnt(0)
	s_setprio 1
	s_waitcnt lgkmcnt(3)
	v_mfma_f32_16x16x32_bf16 v[110:113], v[186:189], v[154:157], v[110:113]
	s_waitcnt lgkmcnt(1)
	v_mfma_f32_16x16x32_bf16 v[106:109], v[194:197], v[154:157], v[106:109]
	v_mfma_f32_16x16x32_bf16 v[92:95], v[186:189], v[162:165], v[92:95]
	v_mfma_f32_16x16x32_bf16 v[88:91], v[194:197], v[162:165], v[88:91]
	v_mfma_f32_16x16x32_bf16 v[76:79], v[186:189], v[170:173], v[76:79]
	v_mfma_f32_16x16x32_bf16 v[72:75], v[194:197], v[170:173], v[72:75]
	v_mfma_f32_16x16x32_bf16 v[68:71], v[186:189], v[178:181], v[68:71]
	v_mfma_f32_16x16x32_bf16 v[64:67], v[194:197], v[178:181], v[64:67]
	v_mfma_f32_16x16x32_bf16 v[110:113], v[190:193], v[158:161], v[110:113]
	s_waitcnt lgkmcnt(0)
	v_mfma_f32_16x16x32_bf16 v[106:109], v[198:201], v[158:161], v[106:109]
	v_mfma_f32_16x16x32_bf16 v[92:95], v[190:193], v[166:169], v[92:95]
	v_mfma_f32_16x16x32_bf16 v[88:91], v[198:201], v[166:169], v[88:91]
	v_mfma_f32_16x16x32_bf16 v[76:79], v[190:193], v[174:177], v[76:79]
	v_mfma_f32_16x16x32_bf16 v[72:75], v[198:201], v[174:177], v[72:75]
	v_mfma_f32_16x16x32_bf16 v[68:71], v[190:193], v[182:185], v[68:71]
	v_mfma_f32_16x16x32_bf16 v[64:67], v[198:201], v[182:185], v[64:67]
	s_setprio 0
	s_mov_b32 m0, s2
	s_barrier
	ds_read_b128 v[154:157], v136 offset:16384
	ds_read_b128 v[158:161], v136 offset:17408
	ds_read_b128 v[162:165], v136 offset:18432
	ds_read_b128 v[166:169], v136 offset:19456
	ds_read_b128 v[170:173], v136 offset:20480
	ds_read_b128 v[174:177], v136 offset:21504
	ds_read_b128 v[178:181], v136 offset:22528
	ds_read_b128 v[182:185], v136 offset:23552
	buffer_load_dwordx4 v131, s[72:75], s50 offen lds
	s_mov_b32 m0, s23
	s_nop 0
	buffer_load_dwordx4 v133, s[72:75], s50 offen lds
	s_barrier
	s_waitcnt lgkmcnt(0)
	s_setprio 1
	s_waitcnt lgkmcnt(7)
	v_mfma_f32_16x16x32_bf16 v[60:63], v[138:141], v[154:157], v[60:63]
	v_mfma_f32_16x16x32_bf16 v[56:59], v[146:149], v[154:157], v[56:59]
	s_waitcnt lgkmcnt(5)
	v_mfma_f32_16x16x32_bf16 v[52:55], v[138:141], v[162:165], v[52:55]
	v_mfma_f32_16x16x32_bf16 v[48:51], v[146:149], v[162:165], v[48:51]
	s_waitcnt lgkmcnt(3)
	v_mfma_f32_16x16x32_bf16 v[36:39], v[138:141], v[170:173], v[36:39]
	v_mfma_f32_16x16x32_bf16 v[32:35], v[146:149], v[170:173], v[32:35]
	s_waitcnt lgkmcnt(1)
	v_mfma_f32_16x16x32_bf16 v[20:23], v[138:141], v[178:181], v[20:23]
	v_mfma_f32_16x16x32_bf16 v[16:19], v[146:149], v[178:181], v[16:19]
	v_mfma_f32_16x16x32_bf16 v[60:63], v[142:145], v[158:161], v[60:63]
	v_mfma_f32_16x16x32_bf16 v[56:59], v[150:153], v[158:161], v[56:59]
	v_mfma_f32_16x16x32_bf16 v[52:55], v[142:145], v[166:169], v[52:55]
	v_mfma_f32_16x16x32_bf16 v[48:51], v[150:153], v[166:169], v[48:51]
	v_mfma_f32_16x16x32_bf16 v[36:39], v[142:145], v[174:177], v[36:39]
	v_mfma_f32_16x16x32_bf16 v[32:35], v[150:153], v[174:177], v[32:35]
	s_waitcnt lgkmcnt(0)
	v_mfma_f32_16x16x32_bf16 v[20:23], v[142:145], v[182:185], v[20:23]
	v_mfma_f32_16x16x32_bf16 v[16:19], v[150:153], v[182:185], v[16:19]
	s_setprio 0
	s_barrier
	s_add_i32 s51, s48, 0x20000
	s_mov_b32 m0, s24
	s_nop 0
	buffer_load_dwordx4 v132, s[8:11], s51 offen lds
	s_mov_b32 m0, s25
	s_nop 0
	buffer_load_dwordx4 v134, s[8:11], s51 offen lds
	s_waitcnt vmcnt(10)
	s_barrier
	s_setprio 1
	v_mfma_f32_16x16x32_bf16 v[44:47], v[186:189], v[154:157], v[44:47]
	v_mfma_f32_16x16x32_bf16 v[40:43], v[194:197], v[154:157], v[40:43]
	v_mfma_f32_16x16x32_bf16 v[28:31], v[186:189], v[162:165], v[28:31]
	v_mfma_f32_16x16x32_bf16 v[24:27], v[194:197], v[162:165], v[24:27]
	v_mfma_f32_16x16x32_bf16 v[12:15], v[186:189], v[170:173], v[12:15]
	v_mfma_f32_16x16x32_bf16 v[8:11], v[194:197], v[170:173], v[8:11]
	v_mfma_f32_16x16x32_bf16 v[4:7], v[186:189], v[178:181], v[4:7]
	v_mfma_f32_16x16x32_bf16 v[0:3], v[194:197], v[178:181], v[0:3]
	v_mfma_f32_16x16x32_bf16 v[44:47], v[190:193], v[158:161], v[44:47]
	v_mfma_f32_16x16x32_bf16 v[40:43], v[198:201], v[158:161], v[40:43]
	v_mfma_f32_16x16x32_bf16 v[28:31], v[190:193], v[166:169], v[28:31]
	v_mfma_f32_16x16x32_bf16 v[24:27], v[198:201], v[166:169], v[24:27]
	v_mfma_f32_16x16x32_bf16 v[12:15], v[190:193], v[174:177], v[12:15]
	v_mfma_f32_16x16x32_bf16 v[8:11], v[198:201], v[174:177], v[8:11]
	v_mfma_f32_16x16x32_bf16 v[4:7], v[190:193], v[182:185], v[4:7]
	v_mfma_f32_16x16x32_bf16 v[0:3], v[198:201], v[182:185], v[0:3]
	s_setprio 0
	s_barrier
	ds_read_b128 v[138:141], v135 offset:32768
	ds_read_b128 v[142:145], v135 offset:33792
	ds_read_b128 v[146:149], v135 offset:34816
	ds_read_b128 v[150:153], v135 offset:35840
	s_add_i32 s50, s50, 0x80000
	s_mov_b32 m0, s26
	ds_read_b128 v[154:157], v136 offset:32768
	ds_read_b128 v[158:161], v136 offset:33792
	ds_read_b128 v[162:165], v136 offset:34816
	ds_read_b128 v[166:169], v136 offset:35840
	ds_read_b128 v[170:173], v136 offset:36864
	ds_read_b128 v[174:177], v136 offset:37888
	ds_read_b128 v[178:181], v136 offset:38912
	ds_read_b128 v[182:185], v136 offset:39936
	buffer_load_dwordx4 v131, s[72:75], s50 offen lds
	s_mov_b32 m0, s27
	s_nop 0
	buffer_load_dwordx4 v133, s[72:75], s50 offen lds
	s_waitcnt lgkmcnt(8)
	s_waitcnt vmcnt(10)
	s_barrier
	s_waitcnt lgkmcnt(0)
	s_setprio 1
	s_waitcnt lgkmcnt(7)
	v_mfma_f32_16x16x32_bf16 v[126:129], v[138:141], v[154:157], v[126:129]
	v_mfma_f32_16x16x32_bf16 v[122:125], v[146:149], v[154:157], v[122:125]
	s_waitcnt lgkmcnt(5)
	v_mfma_f32_16x16x32_bf16 v[118:121], v[138:141], v[162:165], v[118:121]
	v_mfma_f32_16x16x32_bf16 v[114:117], v[146:149], v[162:165], v[114:117]
	s_waitcnt lgkmcnt(3)
	v_mfma_f32_16x16x32_bf16 v[102:105], v[138:141], v[170:173], v[102:105]
	v_mfma_f32_16x16x32_bf16 v[98:101], v[146:149], v[170:173], v[98:101]
	s_waitcnt lgkmcnt(1)
	v_mfma_f32_16x16x32_bf16 v[84:87], v[138:141], v[178:181], v[84:87]
	v_mfma_f32_16x16x32_bf16 v[80:83], v[146:149], v[178:181], v[80:83]
	v_mfma_f32_16x16x32_bf16 v[126:129], v[142:145], v[158:161], v[126:129]
	v_mfma_f32_16x16x32_bf16 v[122:125], v[150:153], v[158:161], v[122:125]
	v_mfma_f32_16x16x32_bf16 v[118:121], v[142:145], v[166:169], v[118:121]
	v_mfma_f32_16x16x32_bf16 v[114:117], v[150:153], v[166:169], v[114:117]
	v_mfma_f32_16x16x32_bf16 v[102:105], v[142:145], v[174:177], v[102:105]
	v_mfma_f32_16x16x32_bf16 v[98:101], v[150:153], v[174:177], v[98:101]
	s_waitcnt lgkmcnt(0)
	v_mfma_f32_16x16x32_bf16 v[84:87], v[142:145], v[182:185], v[84:87]
	v_mfma_f32_16x16x32_bf16 v[80:83], v[150:153], v[182:185], v[80:83]
	s_setprio 0
	s_barrier
	s_add_i32 s50, s48, 0x80
	s_mov_b32 m0, s30
	ds_read_b128 v[186:189], v135 offset:49152
	ds_read_b128 v[190:193], v135 offset:50176
	ds_read_b128 v[194:197], v135 offset:51200
	ds_read_b128 v[198:201], v135 offset:52224
	buffer_load_dwordx4 v132, s[8:11], s50 offen lds
	s_mov_b32 m0, s31
	s_nop 0
	buffer_load_dwordx4 v134, s[8:11], s50 offen lds
	s_waitcnt vmcnt(10)
	s_barrier
	s_waitcnt lgkmcnt(0)
	s_setprio 1
	s_waitcnt lgkmcnt(3)
	v_mfma_f32_16x16x32_bf16 v[110:113], v[186:189], v[154:157], v[110:113]
	s_waitcnt lgkmcnt(1)
	v_mfma_f32_16x16x32_bf16 v[106:109], v[194:197], v[154:157], v[106:109]
	v_mfma_f32_16x16x32_bf16 v[92:95], v[186:189], v[162:165], v[92:95]
	v_mfma_f32_16x16x32_bf16 v[88:91], v[194:197], v[162:165], v[88:91]
	v_mfma_f32_16x16x32_bf16 v[76:79], v[186:189], v[170:173], v[76:79]
	v_mfma_f32_16x16x32_bf16 v[72:75], v[194:197], v[170:173], v[72:75]
	v_mfma_f32_16x16x32_bf16 v[68:71], v[186:189], v[178:181], v[68:71]
	v_mfma_f32_16x16x32_bf16 v[64:67], v[194:197], v[178:181], v[64:67]
	v_mfma_f32_16x16x32_bf16 v[110:113], v[190:193], v[158:161], v[110:113]
	s_waitcnt lgkmcnt(0)
	v_mfma_f32_16x16x32_bf16 v[106:109], v[198:201], v[158:161], v[106:109]
	v_mfma_f32_16x16x32_bf16 v[92:95], v[190:193], v[166:169], v[92:95]
	v_mfma_f32_16x16x32_bf16 v[88:91], v[198:201], v[166:169], v[88:91]
	v_mfma_f32_16x16x32_bf16 v[76:79], v[190:193], v[174:177], v[76:79]
	v_mfma_f32_16x16x32_bf16 v[72:75], v[198:201], v[174:177], v[72:75]
	v_mfma_f32_16x16x32_bf16 v[68:71], v[190:193], v[182:185], v[68:71]
	v_mfma_f32_16x16x32_bf16 v[64:67], v[198:201], v[182:185], v[64:67]
	s_setprio 0
	s_mov_b32 m0, s34
	s_barrier
	ds_read_b128 v[154:157], v136 offset:49152
	ds_read_b128 v[158:161], v136 offset:50176
	ds_read_b128 v[162:165], v136 offset:51200
	ds_read_b128 v[166:169], v136 offset:52224
	ds_read_b128 v[170:173], v136 offset:53248
	ds_read_b128 v[174:177], v136 offset:54272
	ds_read_b128 v[178:181], v136 offset:55296
	ds_read_b128 v[182:185], v136 offset:56320
	buffer_load_dwordx4 v131, s[72:75], s49 offen lds
	s_mov_b32 m0, s35
	s_nop 0
	buffer_load_dwordx4 v133, s[72:75], s49 offen lds
	s_barrier
	s_waitcnt lgkmcnt(0)
	s_setprio 1
	s_waitcnt lgkmcnt(7)
	v_mfma_f32_16x16x32_bf16 v[60:63], v[138:141], v[154:157], v[60:63]
	v_mfma_f32_16x16x32_bf16 v[56:59], v[146:149], v[154:157], v[56:59]
	s_waitcnt lgkmcnt(5)
	v_mfma_f32_16x16x32_bf16 v[52:55], v[138:141], v[162:165], v[52:55]
	v_mfma_f32_16x16x32_bf16 v[48:51], v[146:149], v[162:165], v[48:51]
	s_waitcnt lgkmcnt(3)
	v_mfma_f32_16x16x32_bf16 v[36:39], v[138:141], v[170:173], v[36:39]
	v_mfma_f32_16x16x32_bf16 v[32:35], v[146:149], v[170:173], v[32:35]
	s_waitcnt lgkmcnt(1)
	v_mfma_f32_16x16x32_bf16 v[20:23], v[138:141], v[178:181], v[20:23]
	v_mfma_f32_16x16x32_bf16 v[16:19], v[146:149], v[178:181], v[16:19]
	v_mfma_f32_16x16x32_bf16 v[60:63], v[142:145], v[158:161], v[60:63]
	v_mfma_f32_16x16x32_bf16 v[56:59], v[150:153], v[158:161], v[56:59]
	v_mfma_f32_16x16x32_bf16 v[52:55], v[142:145], v[166:169], v[52:55]
	v_mfma_f32_16x16x32_bf16 v[48:51], v[150:153], v[166:169], v[48:51]
	v_mfma_f32_16x16x32_bf16 v[36:39], v[142:145], v[174:177], v[36:39]
	v_mfma_f32_16x16x32_bf16 v[32:35], v[150:153], v[174:177], v[32:35]
	s_waitcnt lgkmcnt(0)
	v_mfma_f32_16x16x32_bf16 v[20:23], v[142:145], v[182:185], v[20:23]
	v_mfma_f32_16x16x32_bf16 v[16:19], v[150:153], v[182:185], v[16:19]
	s_setprio 0
	s_barrier
	s_add_i32 s48, s48, 0x20080
	s_mov_b32 m0, s36
	s_nop 0
	buffer_load_dwordx4 v132, s[8:11], s48 offen lds
	s_mov_b32 m0, s37
	s_nop 0
	buffer_load_dwordx4 v134, s[8:11], s48 offen lds
	s_waitcnt vmcnt(10)
	s_barrier
	s_setprio 1
	v_mfma_f32_16x16x32_bf16 v[44:47], v[186:189], v[154:157], v[44:47]
	v_mfma_f32_16x16x32_bf16 v[40:43], v[194:197], v[154:157], v[40:43]
	v_mfma_f32_16x16x32_bf16 v[28:31], v[186:189], v[162:165], v[28:31]
	v_mfma_f32_16x16x32_bf16 v[24:27], v[194:197], v[162:165], v[24:27]
	v_mfma_f32_16x16x32_bf16 v[12:15], v[186:189], v[170:173], v[12:15]
	v_mfma_f32_16x16x32_bf16 v[8:11], v[194:197], v[170:173], v[8:11]
	v_mfma_f32_16x16x32_bf16 v[4:7], v[186:189], v[178:181], v[4:7]
	v_mfma_f32_16x16x32_bf16 v[0:3], v[194:197], v[178:181], v[0:3]
	v_mfma_f32_16x16x32_bf16 v[44:47], v[190:193], v[158:161], v[44:47]
	v_mfma_f32_16x16x32_bf16 v[40:43], v[198:201], v[158:161], v[40:43]
	v_mfma_f32_16x16x32_bf16 v[28:31], v[190:193], v[166:169], v[28:31]
	v_mfma_f32_16x16x32_bf16 v[24:27], v[198:201], v[166:169], v[24:27]
	v_mfma_f32_16x16x32_bf16 v[12:15], v[190:193], v[174:177], v[12:15]
	v_mfma_f32_16x16x32_bf16 v[8:11], v[198:201], v[174:177], v[8:11]
	v_mfma_f32_16x16x32_bf16 v[4:7], v[190:193], v[182:185], v[4:7]
	v_mfma_f32_16x16x32_bf16 v[0:3], v[198:201], v[182:185], v[0:3]
	s_setprio 0
	s_add_i32 s47, s47, 2
	s_addk_i32 s45, 0x100
	s_addk_i32 s46, 0x100
	s_cmp_gt_u32 s47, 5
	s_barrier
	s_cbranch_scc0 .LBB0_1358
	s_getreg_b32 s10, hwreg(HW_REG_HW_ID, 0, 6)
	s_and_b32 s10, s10, 63
	s_lshl_b32 s10, s10, 2
	s_add_i32 s10, s10, 0
	s_add_i32 s10, s10, 0x20010
	v_mov_b32_e32 v96, s10
	ds_read_b32 v96, v96
	s_ashr_i32 s15, s14, 31
	s_lshl_b64 s[10:11], s[14:15], 12
	v_mbcnt_lo_u32_b32 v137, -1, 0
	v_mbcnt_hi_u32_b32 v137, -1, v137
	v_cvt_pk_bf16_f32 v126, v126, v127
	s_waitcnt lgkmcnt(0)
	v_readfirstlane_b32 s14, v96
	s_lshl_b32 s14, s14, 6
	s_add_u32 s15, s28, s10
	s_addc_u32 s44, s29, s11
	s_lshl_b32 s10, s42, 8
	s_ashr_i32 s11, s10, 31
	s_lshl_b64 s[10:11], s[10:11], 14
	s_add_u32 s15, s15, s10
	s_addc_u32 s42, s44, s11
	s_lshl_b32 s10, s41, 8
	s_ashr_i32 s11, s10, 31
	v_or_b32_e32 v96, s14, v137
	s_lshl_b64 s[10:11], s[10:11], 1
	v_and_b32_e32 v138, 15, v137
	s_add_u32 s10, s15, s10
	v_lshrrev_b32_e32 v96, 2, v96
	s_mov_b32 s15, 0x3ffc0
	v_and_or_b32 v96, v96, s15, v138
	v_lshlrev_b32_e32 v138, 14, v96
	v_mov_b32_e32 v96, 0xf0
	v_bitop3_b32 v137, s14, v96, v137 bitop3:0xc8
	s_addc_u32 s11, s42, s11
	v_or_b32_e32 v96, v138, v137
	v_cvt_pk_bf16_f32 v127, v128, v129
	v_cvt_pk_bf16_f32 v128, v122, v123
	v_lshl_add_u64 v[122:123], s[10:11], 0, v[96:97]
	s_mov_b32 s14, 0x40000
	v_cvt_pk_bf16_f32 v92, v92, v93
	v_cvt_pk_bf16_f32 v93, v94, v95
	v_cvt_pk_bf16_f32 v94, v88, v89
	v_add_co_u32_e32 v88, vcc, s14, v122
	v_cvt_pk_bf16_f32 v110, v110, v111
	v_cvt_pk_bf16_f32 v111, v112, v113
	v_cvt_pk_bf16_f32 v112, v106, v107
	v_cvt_pk_bf16_f32 v113, v108, v109
	v_addc_co_u32_e32 v89, vcc, 0, v123, vcc
	s_mov_b32 s14, 0x80000
	v_cvt_pk_bf16_f32 v129, v124, v125
	global_store_dwordx4 v96, v[110:113], s[10:11] offset:256
	v_cvt_pk_bf16_f32 v106, v118, v119
	v_cvt_pk_bf16_f32 v107, v120, v121
	v_cvt_pk_bf16_f32 v108, v114, v115
	v_cvt_pk_bf16_f32 v109, v116, v117
	v_or_b32_e32 v110, 0x40000, v96
	v_cvt_pk_bf16_f32 v95, v90, v91
	v_cvt_pk_bf16_f32 v76, v76, v77
	v_cvt_pk_bf16_f32 v77, v78, v79
	v_cvt_pk_bf16_f32 v78, v72, v73
	v_add_co_u32_e32 v72, vcc, s14, v122
	global_store_dwordx4 v96, v[126:129], s[10:11]
	v_or_b32_e32 v124, 0x100, v137
	global_store_dwordx4 v110, v[106:109], s[10:11]
	global_store_dwordx4 v[88:89], v[92:95], off offset:256
	v_cvt_pk_bf16_f32 v88, v102, v103
	v_cvt_pk_bf16_f32 v89, v104, v105
	v_cvt_pk_bf16_f32 v90, v98, v99
	v_cvt_pk_bf16_f32 v91, v100, v101
	v_or_b32_e32 v92, 0x80000, v96
	v_cvt_pk_bf16_f32 v79, v74, v75
	v_addc_co_u32_e32 v73, vcc, 0, v123, vcc
	v_or_b32_e32 v125, v138, v124
	global_store_dwordx4 v92, v[88:91], s[10:11]
	global_store_dwordx4 v[72:73], v[76:79], off offset:256
	v_cvt_pk_bf16_f32 v72, v84, v85
	v_cvt_pk_bf16_f32 v73, v86, v87
	v_or_b32_e32 v76, 0xc0000, v138
	v_cvt_pk_bf16_f32 v74, v80, v81
	v_cvt_pk_bf16_f32 v75, v82, v83
	v_or_b32_e32 v77, v76, v137
	v_cvt_pk_bf16_f32 v68, v68, v69
	v_cvt_pk_bf16_f32 v69, v70, v71
	v_cvt_pk_bf16_f32 v70, v64, v65
	v_cvt_pk_bf16_f32 v71, v66, v67
	v_or_b32_e32 v64, v76, v124
	v_cvt_pk_bf16_f32 v60, v60, v61
	v_cvt_pk_bf16_f32 v61, v62, v63
	v_cvt_pk_bf16_f32 v62, v56, v57
	v_cvt_pk_bf16_f32 v63, v58, v59
	v_add_u32_e32 v56, 0x200000, v96
	v_cvt_pk_bf16_f32 v44, v44, v45
	v_cvt_pk_bf16_f32 v45, v46, v47
	v_cvt_pk_bf16_f32 v46, v40, v41
	v_cvt_pk_bf16_f32 v47, v42, v43
	v_add_u32_e32 v40, 0x200000, v125
	global_store_dwordx4 v77, v[72:75], s[10:11]
	global_store_dwordx4 v64, v[68:71], s[10:11]
	global_store_dwordx4 v56, v[60:63], s[10:11]
	global_store_dwordx4 v40, v[44:47], s[10:11]
	v_cvt_pk_bf16_f32 v28, v28, v29
	v_cvt_pk_bf16_f32 v29, v30, v31
	v_add_u32_e32 v44, 0x240000, v96
	v_cvt_pk_bf16_f32 v30, v24, v25
	v_cvt_pk_bf16_f32 v31, v26, v27
	v_cvt_pk_bf16_f32 v40, v52, v53
	v_cvt_pk_bf16_f32 v41, v54, v55
	v_cvt_pk_bf16_f32 v42, v48, v49
	v_cvt_pk_bf16_f32 v43, v50, v51
	global_store_dwordx4 v44, v[28:31], s[10:11] offset:256
	v_cvt_pk_bf16_f32 v12, v12, v13
	v_cvt_pk_bf16_f32 v13, v14, v15
	v_add_u32_e32 v28, 0x280000, v96
	v_cvt_pk_bf16_f32 v14, v8, v9
	v_cvt_pk_bf16_f32 v15, v10, v11
	global_store_dwordx4 v44, v[40:43], s[10:11]
	v_cvt_pk_bf16_f32 v24, v36, v37
	v_cvt_pk_bf16_f32 v25, v38, v39
	v_cvt_pk_bf16_f32 v26, v32, v33
	v_cvt_pk_bf16_f32 v27, v34, v35
	global_store_dwordx4 v28, v[12:15], s[10:11] offset:256
	v_cvt_pk_bf16_f32 v8, v20, v21
	v_cvt_pk_bf16_f32 v9, v22, v23
	v_cvt_pk_bf16_f32 v10, v16, v17
	v_cvt_pk_bf16_f32 v11, v18, v19
	v_add_u32_e32 v12, 0x2c0000, v96
	v_cvt_pk_bf16_f32 v4, v4, v5
	v_cvt_pk_bf16_f32 v5, v6, v7
	v_cvt_pk_bf16_f32 v6, v0, v1
	v_cvt_pk_bf16_f32 v7, v2, v3
	s_and_b64 vcc, exec, s[4:5]
	s_mov_b32 s14, s16
	s_mov_b32 s41, s17
	s_mov_b32 s42, s18
	s_mov_b32 s46, s43
	s_mov_b32 s45, s19
	global_store_dwordx4 v28, v[24:27], s[10:11]
	global_store_dwordx4 v12, v[8:11], s[10:11]
	global_store_dwordx4 v12, v[4:7], s[10:11] offset:256
	s_cbranch_vccz .LBB0_1352
	s_branch .LBB0_1361

.LBB0_1427:
	s_add_i32 s10, s46, 0xfffc0080
	s_cmp_eq_u32 s48, 12
	s_cselect_b32 s51, s19, s10
	s_cselect_b32 s49, s45, s47
	s_add_i32 s10, 0, 0x10000
	v_add_u32_e32 v213, s10, v228
	v_add_u32_e32 v252, s10, v229
	ds_read_b128 v[72:75], v213
	ds_read_b128 v[84:87], v213 offset:2048
	ds_read_b128 v[76:79], v252
	ds_read_b128 v[88:91], v252 offset:2048
	s_or_b32 s50, s51, 0x80
	s_mov_b32 m0, s42
	ds_read_b128 v[146:149], v230
	ds_read_b128 v[154:157], v230 offset:2048
	ds_read_b128 v[150:153], v231
	ds_read_b128 v[158:161], v231 offset:2048
	ds_read_b128 v[168:171], v230 offset:4096
	ds_read_b128 v[176:179], v230 offset:6144
	ds_read_b128 v[172:175], v231 offset:4096
	ds_read_b128 v[180:183], v231 offset:6144
	buffer_load_dwordx4 v96, s[72:75], s46 offen lds
	s_mov_b32 m0, s43
	s_nop 0
	buffer_load_dwordx4 v218, s[72:75], s46 offen lds
	s_waitcnt lgkmcnt(8)
	s_waitcnt vmcnt(10)
	s_barrier
	s_waitcnt lgkmcnt(0)
	s_setprio 1
	s_waitcnt lgkmcnt(5)
	v_mfma_scale_f32_16x16x128_f8f6f4 v[142:145], v[72:79], v[146:153], v[142:145], v212, v212 op_sel_hi:[0,0,0]
	v_mfma_scale_f32_16x16x128_f8f6f4 v[138:141], v[84:91], v[146:153], v[138:141], v212, v212 op_sel_hi:[0,0,0]
	s_waitcnt lgkmcnt(0)
	v_mfma_scale_f32_16x16x128_f8f6f4 v[92:95], v[72:79], v[176:183], v[92:95], v212, v212 op_sel_hi:[0,0,0]
	v_mfma_scale_f32_16x16x128_f8f6f4 v[80:83], v[84:91], v[176:183], v[80:83], v212, v212 op_sel_hi:[0,0,0]
	v_mfma_scale_f32_16x16x128_f8f6f4 v[162:165], v[72:79], v[154:161], v[126:129], v212, v212 op_sel_hi:[0,0,0]
	v_mfma_scale_f32_16x16x128_f8f6f4 v[184:187], v[84:91], v[154:161], v[122:125], v212, v212 op_sel_hi:[0,0,0]
	v_mfma_scale_f32_16x16x128_f8f6f4 v[188:191], v[72:79], v[168:175], v[110:113], v212, v212 op_sel_hi:[0,0,0]
	v_mfma_scale_f32_16x16x128_f8f6f4 v[192:195], v[84:91], v[168:175], v[106:109], v212, v212 op_sel_hi:[0,0,0]
	s_setprio 0
	s_barrier
	s_mov_b32 s10, s74
	s_mov_b32 s11, s75
	s_mov_b32 m0, s28
	s_nop 1
	ds_read_b128 v[106:109], v213 offset:16384
	ds_read_b128 v[122:125], v213 offset:18432
	ds_read_b128 v[110:113], v252 offset:16384
	ds_read_b128 v[126:129], v252 offset:18432
	buffer_load_dwordx4 v96, s[8:11], s49 offen lds
	s_mov_b32 m0, s29
	s_nop 0
	buffer_load_dwordx4 v218, s[8:11], s49 offen lds
	s_waitcnt vmcnt(10)
	s_barrier
	s_waitcnt lgkmcnt(0)
	s_setprio 1
	s_waitcnt lgkmcnt(1)
	v_mfma_scale_f32_16x16x128_f8f6f4 v[196:199], v[106:113], v[146:153], v[134:137], v212, v212 op_sel_hi:[0,0,0]
	s_waitcnt lgkmcnt(0)
	v_mfma_scale_f32_16x16x128_f8f6f4 v[146:149], v[122:129], v[146:153], v[130:133], v212, v212 op_sel_hi:[0,0,0]
	v_mfma_scale_f32_16x16x128_f8f6f4 v[150:153], v[106:113], v[154:161], v[118:121], v212, v212 op_sel_hi:[0,0,0]
	v_mfma_scale_f32_16x16x128_f8f6f4 v[154:157], v[122:129], v[154:161], v[114:117], v212, v212 op_sel_hi:[0,0,0]
	v_mfma_scale_f32_16x16x128_f8f6f4 v[158:161], v[106:113], v[168:175], v[102:105], v212, v212 op_sel_hi:[0,0,0]
	v_mfma_scale_f32_16x16x128_f8f6f4 v[166:169], v[122:129], v[168:175], v[98:101], v212, v212 op_sel_hi:[0,0,0]
	v_mfma_scale_f32_16x16x128_f8f6f4 v[170:173], v[106:113], v[176:183], v[68:71], v212, v212 op_sel_hi:[0,0,0]
	v_mfma_scale_f32_16x16x128_f8f6f4 v[174:177], v[122:129], v[176:183], v[64:67], v212, v212 op_sel_hi:[0,0,0]
	s_setprio 0
	s_mov_b32 m0, s27
	s_barrier
	s_nop 3
	ds_read_b128 v[64:67], v230 offset:16384
	ds_read_b128 v[98:101], v230 offset:18432
	ds_read_b128 v[68:71], v231 offset:16384
	ds_read_b128 v[102:105], v231 offset:18432
	ds_read_b128 v[114:117], v230 offset:20480
	ds_read_b128 v[130:133], v230 offset:22528
	ds_read_b128 v[118:121], v231 offset:20480
	ds_read_b128 v[134:137], v231 offset:22528
	buffer_load_dwordx4 v96, s[72:75], s51 offen lds
	s_mov_b32 m0, s30
	s_nop 0
	buffer_load_dwordx4 v218, s[72:75], s51 offen lds
	s_barrier
	s_waitcnt lgkmcnt(0)
	s_setprio 1
	s_waitcnt lgkmcnt(5)
	v_mfma_scale_f32_16x16x128_f8f6f4 v[60:63], v[72:79], v[64:71], v[60:63], v212, v212 op_sel_hi:[0,0,0]
	v_mfma_scale_f32_16x16x128_f8f6f4 v[56:59], v[84:91], v[64:71], v[56:59], v212, v212 op_sel_hi:[0,0,0]
	s_waitcnt lgkmcnt(4)
	v_mfma_scale_f32_16x16x128_f8f6f4 v[178:181], v[72:79], v[98:105], v[44:47], v212, v212 op_sel_hi:[0,0,0]
	v_mfma_scale_f32_16x16x128_f8f6f4 v[200:203], v[84:91], v[98:105], v[40:43], v212, v212 op_sel_hi:[0,0,0]
	s_waitcnt lgkmcnt(1)
	v_mfma_scale_f32_16x16x128_f8f6f4 v[204:207], v[72:79], v[114:121], v[28:31], v212, v212 op_sel_hi:[0,0,0]
	v_mfma_scale_f32_16x16x128_f8f6f4 v[208:211], v[84:91], v[114:121], v[24:27], v212, v212 op_sel_hi:[0,0,0]
	s_waitcnt lgkmcnt(0)
	v_mfma_scale_f32_16x16x128_f8f6f4 v[214:217], v[72:79], v[130:137], v[12:15], v212, v212 op_sel_hi:[0,0,0]
	v_mfma_scale_f32_16x16x128_f8f6f4 v[220:223], v[84:91], v[130:137], v[8:11], v212, v212 op_sel_hi:[0,0,0]
	s_setprio 0
	s_barrier
	s_add_i32 s52, s49, 0x40000
	s_mov_b32 m0, s31
	s_nop 0
	buffer_load_dwordx4 v96, s[8:11], s52 offen lds
	s_mov_b32 m0, s34
	s_nop 0
	buffer_load_dwordx4 v218, s[8:11], s52 offen lds
	s_waitcnt vmcnt(10)
	s_barrier
	s_setprio 1
	v_mfma_scale_f32_16x16x128_f8f6f4 v[52:55], v[106:113], v[64:71], v[52:55], v212, v212 op_sel_hi:[0,0,0]
	v_mfma_scale_f32_16x16x128_f8f6f4 v[48:51], v[122:129], v[64:71], v[48:51], v212, v212 op_sel_hi:[0,0,0]
	v_mfma_scale_f32_16x16x128_f8f6f4 v[232:235], v[106:113], v[98:105], v[36:39], v212, v212 op_sel_hi:[0,0,0]
	v_mfma_scale_f32_16x16x128_f8f6f4 v[236:239], v[122:129], v[98:105], v[32:35], v212, v212 op_sel_hi:[0,0,0]
	v_mfma_scale_f32_16x16x128_f8f6f4 v[240:243], v[106:113], v[114:121], v[20:23], v212, v212 op_sel_hi:[0,0,0]
	v_mfma_scale_f32_16x16x128_f8f6f4 v[244:247], v[122:129], v[114:121], v[16:19], v212, v212 op_sel_hi:[0,0,0]
	v_mfma_scale_f32_16x16x128_f8f6f4 v[248:251], v[106:113], v[130:137], v[4:7], v212, v212 op_sel_hi:[0,0,0]
	v_mfma_scale_f32_16x16x128_f8f6f4 v[224:227], v[122:129], v[130:137], v[0:3], v212, v212 op_sel_hi:[0,0,0]
	s_setprio 0
	s_barrier
	s_nop 4
	ds_read_b128 v[0:3], v213 offset:32768
	ds_read_b128 v[16:19], v213 offset:34816
	ds_read_b128 v[4:7], v252 offset:32768
	ds_read_b128 v[20:23], v252 offset:34816
	s_add_i32 s51, s51, 0x40000
	s_mov_b32 m0, s35
	ds_read_b128 v[8:11], v230 offset:32768
	ds_read_b128 v[24:27], v230 offset:34816
	ds_read_b128 v[12:15], v231 offset:32768
	ds_read_b128 v[28:31], v231 offset:34816
	ds_read_b128 v[32:35], v230 offset:36864
	ds_read_b128 v[40:43], v230 offset:38912
	ds_read_b128 v[36:39], v231 offset:36864
	ds_read_b128 v[44:47], v231 offset:38912
	buffer_load_dwordx4 v96, s[72:75], s51 offen lds
	s_mov_b32 m0, s36
	s_nop 0
	buffer_load_dwordx4 v218, s[72:75], s51 offen lds
	s_waitcnt lgkmcnt(8)
	s_waitcnt vmcnt(10)
	s_barrier
	s_waitcnt lgkmcnt(0)
	s_setprio 1
	s_waitcnt lgkmcnt(5)
	v_mfma_scale_f32_16x16x128_f8f6f4 v[142:145], v[0:7], v[8:15], v[142:145], v212, v212 op_sel_hi:[0,0,0]
	v_mfma_scale_f32_16x16x128_f8f6f4 v[138:141], v[16:23], v[8:15], v[138:141], v212, v212 op_sel_hi:[0,0,0]
	s_waitcnt lgkmcnt(4)
	v_mfma_scale_f32_16x16x128_f8f6f4 v[126:129], v[0:7], v[24:31], v[162:165], v212, v212 op_sel_hi:[0,0,0]
	v_mfma_scale_f32_16x16x128_f8f6f4 v[122:125], v[16:23], v[24:31], v[184:187], v212, v212 op_sel_hi:[0,0,0]
	s_waitcnt lgkmcnt(1)
	v_mfma_scale_f32_16x16x128_f8f6f4 v[110:113], v[0:7], v[32:39], v[188:191], v212, v212 op_sel_hi:[0,0,0]
	v_mfma_scale_f32_16x16x128_f8f6f4 v[106:109], v[16:23], v[32:39], v[192:195], v212, v212 op_sel_hi:[0,0,0]
	s_waitcnt lgkmcnt(0)
	v_mfma_scale_f32_16x16x128_f8f6f4 v[92:95], v[0:7], v[40:47], v[92:95], v212, v212 op_sel_hi:[0,0,0]
	v_mfma_scale_f32_16x16x128_f8f6f4 v[80:83], v[16:23], v[40:47], v[80:83], v212, v212 op_sel_hi:[0,0,0]
	s_setprio 0
	s_barrier
	s_or_b32 s51, s49, 0x80
	s_mov_b32 m0, s0
	ds_read_b128 v[72:75], v213 offset:49152
	ds_read_b128 v[84:87], v213 offset:51200
	ds_read_b128 v[76:79], v252 offset:49152
	ds_read_b128 v[88:91], v252 offset:51200
	buffer_load_dwordx4 v96, s[8:11], s51 offen lds
	s_mov_b32 m0, s37
	s_nop 0
	buffer_load_dwordx4 v218, s[8:11], s51 offen lds
	s_waitcnt vmcnt(10)
	s_barrier
	s_waitcnt lgkmcnt(0)
	s_setprio 1
	s_waitcnt lgkmcnt(1)
	v_mfma_scale_f32_16x16x128_f8f6f4 v[134:137], v[72:79], v[8:15], v[196:199], v212, v212 op_sel_hi:[0,0,0]
	s_waitcnt lgkmcnt(0)
	v_mfma_scale_f32_16x16x128_f8f6f4 v[130:133], v[84:91], v[8:15], v[146:149], v212, v212 op_sel_hi:[0,0,0]
	v_mfma_scale_f32_16x16x128_f8f6f4 v[118:121], v[72:79], v[24:31], v[150:153], v212, v212 op_sel_hi:[0,0,0]
	v_mfma_scale_f32_16x16x128_f8f6f4 v[114:117], v[84:91], v[24:31], v[154:157], v212, v212 op_sel_hi:[0,0,0]
	v_mfma_scale_f32_16x16x128_f8f6f4 v[102:105], v[72:79], v[32:39], v[158:161], v212, v212 op_sel_hi:[0,0,0]
	v_mfma_scale_f32_16x16x128_f8f6f4 v[98:101], v[84:91], v[32:39], v[166:169], v212, v212 op_sel_hi:[0,0,0]
	v_mfma_scale_f32_16x16x128_f8f6f4 v[68:71], v[72:79], v[40:47], v[170:173], v212, v212 op_sel_hi:[0,0,0]
	v_mfma_scale_f32_16x16x128_f8f6f4 v[64:67], v[84:91], v[40:47], v[174:177], v212, v212 op_sel_hi:[0,0,0]
	s_setprio 0
	s_mov_b32 m0, s38
	s_barrier
	ds_read_b128 v[32:35], v230 offset:49152
	ds_read_b128 v[146:149], v230 offset:51200
	ds_read_b128 v[36:39], v231 offset:49152
	ds_read_b128 v[150:153], v231 offset:51200
	ds_read_b128 v[154:157], v230 offset:53248
	ds_read_b128 v[168:171], v230 offset:55296
	ds_read_b128 v[158:161], v231 offset:53248
	ds_read_b128 v[172:175], v231 offset:55296
	buffer_load_dwordx4 v96, s[72:75], s50 offen lds
	s_mov_b32 m0, s39
	s_nop 0
	buffer_load_dwordx4 v218, s[72:75], s50 offen lds
	s_barrier
	s_waitcnt lgkmcnt(0)
	s_setprio 1
	s_waitcnt lgkmcnt(5)
	v_mfma_scale_f32_16x16x128_f8f6f4 v[60:63], v[0:7], v[32:39], v[60:63], v212, v212 op_sel_hi:[0,0,0]
	v_mfma_scale_f32_16x16x128_f8f6f4 v[56:59], v[16:23], v[32:39], v[56:59], v212, v212 op_sel_hi:[0,0,0]
	s_waitcnt lgkmcnt(4)
	v_mfma_scale_f32_16x16x128_f8f6f4 v[44:47], v[0:7], v[146:153], v[178:181], v212, v212 op_sel_hi:[0,0,0]
	v_mfma_scale_f32_16x16x128_f8f6f4 v[40:43], v[16:23], v[146:153], v[200:203], v212, v212 op_sel_hi:[0,0,0]
	s_waitcnt lgkmcnt(1)
	v_mfma_scale_f32_16x16x128_f8f6f4 v[28:31], v[0:7], v[154:161], v[204:207], v212, v212 op_sel_hi:[0,0,0]
	v_mfma_scale_f32_16x16x128_f8f6f4 v[24:27], v[16:23], v[154:161], v[208:211], v212, v212 op_sel_hi:[0,0,0]
	s_waitcnt lgkmcnt(0)
	v_mfma_scale_f32_16x16x128_f8f6f4 v[12:15], v[0:7], v[168:175], v[214:217], v212, v212 op_sel_hi:[0,0,0]
	v_mfma_scale_f32_16x16x128_f8f6f4 v[8:11], v[16:23], v[168:175], v[220:223], v212, v212 op_sel_hi:[0,0,0]
	s_setprio 0
	s_barrier
	s_add_i32 s49, s49, 0x40080
	s_mov_b32 m0, s40
	s_nop 0
	buffer_load_dwordx4 v96, s[8:11], s49 offen lds
	s_mov_b32 m0, s41
	s_nop 0
	buffer_load_dwordx4 v218, s[8:11], s49 offen lds
	s_waitcnt vmcnt(10)
	s_barrier
	s_setprio 1
	v_mfma_scale_f32_16x16x128_f8f6f4 v[52:55], v[72:79], v[32:39], v[52:55], v212, v212 op_sel_hi:[0,0,0]
	v_mfma_scale_f32_16x16x128_f8f6f4 v[48:51], v[84:91], v[32:39], v[48:51], v212, v212 op_sel_hi:[0,0,0]
	v_mfma_scale_f32_16x16x128_f8f6f4 v[36:39], v[72:79], v[146:153], v[232:235], v212, v212 op_sel_hi:[0,0,0]
	v_mfma_scale_f32_16x16x128_f8f6f4 v[32:35], v[84:91], v[146:153], v[236:239], v212, v212 op_sel_hi:[0,0,0]
	v_mfma_scale_f32_16x16x128_f8f6f4 v[20:23], v[72:79], v[154:161], v[240:243], v212, v212 op_sel_hi:[0,0,0]
	v_mfma_scale_f32_16x16x128_f8f6f4 v[16:19], v[84:91], v[154:161], v[244:247], v212, v212 op_sel_hi:[0,0,0]
	v_mfma_scale_f32_16x16x128_f8f6f4 v[4:7], v[72:79], v[168:175], v[248:251], v212, v212 op_sel_hi:[0,0,0]
	v_mfma_scale_f32_16x16x128_f8f6f4 v[0:3], v[84:91], v[168:175], v[224:227], v212, v212 op_sel_hi:[0,0,0]
	s_setprio 0
	s_add_i32 s48, s48, 2
	s_addk_i32 s46, 0x100
	s_addk_i32 s47, 0x100
	s_cmp_gt_u32 s48, 13
	s_barrier
	s_cbranch_scc0 .LBB0_1427
	s_getreg_b32 s10, hwreg(HW_REG_HW_ID, 0, 6)
	s_and_b32 s10, s10, 63
	s_lshl_b32 s10, s10, 2
	s_add_i32 s10, s10, 0
	s_add_i32 s10, s10, 0x20010
	v_mov_b32_e32 v72, s10
	ds_read_b32 v72, v72
	v_mbcnt_lo_u32_b32 v150, -1, 0
	v_mbcnt_hi_u32_b32 v150, -1, v150
	s_lshl_b32 s2, s2, 6
	v_lshrrev_b32_e32 v73, 2, v150
	v_and_b32_e32 v73, 12, v73
	s_waitcnt lgkmcnt(0)
	v_readfirstlane_b32 s10, v72
	s_movk_i32 s45, 0x2000
	s_ashr_i32 s19, s18, 31
	v_lshl_or_b32 v148, s10, 6, v150
	v_lshrrev_b32_e32 v72, 2, v148
	v_and_b32_e32 v72, 48, v72
	v_or3_b32 v146, v72, s2, v73
	v_ashrrev_i32_e32 v147, 31, v146
	v_lshl_add_u64 v[72:73], v[146:147], 2, s[16:17]
	v_add_co_u32_e32 v74, vcc, s45, v72
	v_ashrrev_i32_e32 v148, 2, v148
	s_nop 0
	v_addc_co_u32_e32 v75, vcc, 0, v73, vcc
	global_load_dwordx4 v[88:91], v[72:73], off
	global_load_dwordx4 v[84:87], v[74:75], off
	v_and_b32_e32 v148, 0xffffffc0, v148
	s_lshl_b64 s[10:11], s[18:19], 8
	v_ashrrev_i32_e32 v149, 31, v148
	s_movk_i32 s2, 0x4000
	v_lshl_add_u64 v[148:149], s[10:11], 0, v[148:149]
	v_add_co_u32_e32 v74, vcc, s2, v72
	v_and_or_b32 v148, v150, 15, v148
	s_nop 0
	v_addc_co_u32_e32 v75, vcc, 0, v73, vcc
	s_movk_i32 s2, 0x6000
	v_lshlrev_b64 v[150:151], 14, v[148:149]
	v_add_co_u32_e32 v72, vcc, s2, v72
	v_lshl_add_u64 v[150:151], s[14:15], 0, v[150:151]
	v_lshlrev_b64 v[146:147], 1, v[146:147]
	v_addc_co_u32_e32 v73, vcc, 0, v73, vcc
	v_lshl_add_u64 v[150:151], v[150:151], 0, v[146:147]
	v_add_co_u32_e32 v152, vcc, s45, v150
	global_load_dwordx4 v[76:79], v[74:75], off
	s_nop 0
	global_load_dwordx4 v[72:75], v[72:73], off
	v_addc_co_u32_e32 v153, vcc, 0, v151, vcc
	v_add_co_u32_e32 v154, vcc, s95, v150
	s_mov_b32 s2, 0x41000
	s_nop 0
	v_addc_co_u32_e32 v155, vcc, 0, v151, vcc
	global_load_dwordx2 v[166:167], v[150:151], off
	global_load_dwordx2 v[208:209], v[152:153], off offset:-4096
	global_load_dwordx2 v[204:205], v[152:153], off
	global_load_dwordx2 v[206:207], v[154:155], off
	v_add_co_u32_e32 v152, vcc, s2, v150
	s_mov_b32 s2, 0x43000
	s_nop 0
	v_addc_co_u32_e32 v153, vcc, 0, v151, vcc
	v_add_co_u32_e32 v154, vcc, s2, v150
	s_mov_b32 s2, 0x81000
	s_nop 0
	v_addc_co_u32_e32 v155, vcc, 0, v151, vcc
	global_load_dwordx2 v[200:201], v[152:153], off offset:-4096
	global_load_dwordx2 v[202:203], v[152:153], off
	global_load_dwordx2 v[196:197], v[154:155], off offset:-4096
	global_load_dwordx2 v[198:199], v[154:155], off
	v_add_co_u32_e32 v152, vcc, s2, v150
	s_mov_b32 s2, 0x83000
	s_nop 0
	v_addc_co_u32_e32 v153, vcc, 0, v151, vcc
	v_add_co_u32_e32 v154, vcc, s2, v150
	s_mov_b32 s2, 0xc1000
	s_nop 0
	v_addc_co_u32_e32 v155, vcc, 0, v151, vcc
	global_load_dwordx2 v[192:193], v[152:153], off offset:-4096
	global_load_dwordx2 v[194:195], v[152:153], off
	global_load_dwordx2 v[188:189], v[154:155], off offset:-4096
	global_load_dwordx2 v[190:191], v[154:155], off
	v_add_co_u32_e32 v152, vcc, s2, v150
	s_mov_b32 s2, 0xc3000
	s_nop 0
	v_addc_co_u32_e32 v153, vcc, 0, v151, vcc
	v_lshlrev_b64 v[148:149], 12, v[148:149]
	v_add_co_u32_e32 v154, vcc, s2, v150
	v_lshl_add_u64 v[148:149], s[12:13], 0, v[148:149]
	s_nop 0
	v_addc_co_u32_e32 v155, vcc, 0, v151, vcc
	s_mov_b32 s2, 0x201000
	v_lshl_add_u64 v[146:147], v[148:149], 0, v[146:147]
	v_add_co_u32_e32 v148, vcc, s2, v150
	s_mov_b32 s2, 0x203000
	s_nop 0
	v_addc_co_u32_e32 v149, vcc, 0, v151, vcc
	global_load_dwordx2 v[184:185], v[152:153], off offset:-4096
	global_load_dwordx2 v[186:187], v[152:153], off
	global_load_dwordx2 v[180:181], v[154:155], off offset:-4096
	global_load_dwordx2 v[182:183], v[154:155], off
	v_add_co_u32_e32 v152, vcc, s2, v150
	s_mov_b32 s2, 0x241000
	s_nop 0
	v_addc_co_u32_e32 v153, vcc, 0, v151, vcc
	global_load_dwordx2 v[176:177], v[148:149], off offset:-4096
	global_load_dwordx2 v[178:179], v[148:149], off
	global_load_dwordx2 v[172:173], v[152:153], off offset:-4096
	global_load_dwordx2 v[174:175], v[152:153], off
	v_add_co_u32_e32 v148, vcc, s2, v150
	s_mov_b32 s2, 0x243000
	s_nop 0
	v_addc_co_u32_e32 v149, vcc, 0, v151, vcc
	v_add_co_u32_e32 v152, vcc, s2, v150
	s_mov_b32 s2, 0x281000
	s_nop 0
	v_addc_co_u32_e32 v153, vcc, 0, v151, vcc
	global_load_dwordx2 v[168:169], v[148:149], off offset:-4096
	global_load_dwordx2 v[170:171], v[148:149], off
	global_load_dwordx2 v[162:163], v[152:153], off offset:-4096
	global_load_dwordx2 v[164:165], v[152:153], off
	v_add_co_u32_e32 v148, vcc, s2, v150
	s_mov_b32 s2, 0x283000
	s_nop 0
	v_addc_co_u32_e32 v149, vcc, 0, v151, vcc
	v_add_co_u32_e32 v152, vcc, s2, v150
	s_mov_b32 s2, 0x2c1000
	s_nop 0
	v_addc_co_u32_e32 v153, vcc, 0, v151, vcc
	s_waitcnt vmcnt(27)
	v_pk_fma_f32 v[214:215], v[142:143], s[78:79], v[88:89] op_sel_hi:[1,0,1]
	global_load_dwordx2 v[158:159], v[148:149], off offset:-4096
	global_load_dwordx2 v[160:161], v[148:149], off
	global_load_dwordx2 v[154:155], v[152:153], off offset:-4096
	global_load_dwordx2 v[156:157], v[152:153], off
	v_add_co_u32_e32 v148, vcc, s2, v150
	v_mul_f32_e32 v142, 0xbfb8aa3b, v214
	s_nop 0
	v_addc_co_u32_e32 v149, vcc, 0, v151, vcc
	s_mov_b32 s2, 0x2c3000
	v_exp_f32_e32 v214, v142
	v_add_co_u32_e32 v210, vcc, s2, v150
	v_pk_fma_f32 v[144:145], v[144:145], s[78:79], v[90:91] op_sel_hi:[1,0,1]
	s_nop 0
	v_addc_co_u32_e32 v211, vcc, 0, v151, vcc
	global_load_dwordx2 v[150:151], v[148:149], off offset:-4096
	global_load_dwordx2 v[152:153], v[148:149], off
	global_load_dwordx2 v[142:143], v[210:211], off offset:-4096
	s_nop 0
	global_load_dwordx2 v[148:149], v[210:211], off
	v_mul_f32_e32 v211, 0xbfb8aa3b, v215
	v_mul_f32_e32 v144, 0xbfb8aa3b, v144
	v_add_f32_e32 v210, 1.0, v214
	v_exp_f32_e32 v211, v211
	v_exp_f32_e32 v214, v144
	s_waitcnt vmcnt(34)
	v_pk_fma_f32 v[138:139], v[138:139], s[78:79], v[84:85] op_sel_hi:[1,0,1]
	v_rcp_f32_e32 v144, v210
	v_mul_f32_e32 v139, 0xbfb8aa3b, v139
	v_add_f32_e32 v210, 1.0, v211
	v_add_f32_e32 v211, 1.0, v214
	v_mul_f32_e32 v145, 0xbfb8aa3b, v145
	v_mul_f32_e32 v138, 0xbfb8aa3b, v138
	v_exp_f32_e32 v139, v139
	v_rcp_f32_e32 v214, v211
	v_exp_f32_e32 v145, v145
	v_exp_f32_e32 v211, v138
	v_pk_fma_f32 v[140:141], v[140:141], s[78:79], v[86:87] op_sel_hi:[1,0,1]
	v_add_f32_e32 v139, 1.0, v139
	v_add_f32_e32 v138, 1.0, v145
	v_add_f32_e32 v145, 1.0, v211
	v_rcp_f32_e32 v211, v139
	v_mul_f32_e32 v139, 0xbfb8aa3b, v140
	v_exp_f32_e32 v139, v139
	v_rcp_f32_e32 v145, v145
	v_rcp_f32_e32 v210, v210
	s_waitcnt vmcnt(30)
	v_lshlrev_b32_e32 v217, 16, v208
	v_add_f32_e32 v139, 1.0, v139
	v_lshlrev_b32_e32 v216, 16, v166
	v_rcp_f32_e32 v215, v139
	v_mul_f32_e32 v139, 0xbfb8aa3b, v141
	v_pk_mul_f32 v[144:145], v[144:145], v[216:217]
	v_exp_f32_e32 v139, v139
	v_add_f32_e32 v144, 0, v144
	v_add_f32_e32 v216, v144, v145
	v_and_b32_e32 v145, 0xffff0000, v208
	v_and_b32_e32 v144, 0xffff0000, v166
	v_pk_mul_f32 v[144:145], v[210:211], v[144:145]
	v_add_f32_e32 v139, 1.0, v139
	v_add_f32_e32 v140, 0, v144
	v_rcp_f32_e32 v138, v138
	v_add_f32_e32 v166, v140, v145
	v_lshlrev_b32_e32 v145, 16, v209
	v_lshlrev_b32_e32 v144, 16, v167
	v_rcp_f32_e32 v139, v139
	v_pk_mul_f32 v[140:141], v[214:215], v[144:145]
	v_pk_fma_f32 v[134:135], v[134:135], s[78:79], v[76:77] op_sel_hi:[1,0,1]
	v_add_f32_e32 v140, 0, v140
	v_add_f32_e32 v144, v140, v141
	v_and_b32_e32 v141, 0xffff0000, v209
	v_and_b32_e32 v140, 0xffff0000, v167
	v_pk_mul_f32 v[138:139], v[138:139], v[140:141]
	v_pk_fma_f32 v[136:137], v[136:137], s[78:79], v[78:79] op_sel_hi:[1,0,1]
	v_mul_f32_e32 v135, 0xbfb8aa3b, v135
	v_add_f32_e32 v138, 0, v138
	v_exp_f32_e32 v135, v135
	v_mul_f32_e32 v136, 0xbfb8aa3b, v136
	v_add_f32_e32 v145, v138, v139
	v_exp_f32_e32 v138, v136
	v_add_f32_e32 v135, 1.0, v135
	v_pk_fma_f32 v[130:131], v[130:131], s[78:79], v[72:73] op_sel_hi:[1,0,1]
	v_rcp_f32_e32 v136, v135
	v_add_f32_e32 v135, 1.0, v138
	v_mul_f32_e32 v131, 0xbfb8aa3b, v131
	v_rcp_f32_e32 v138, v135
	v_mul_f32_e32 v135, 0xbfb8aa3b, v137
	v_mul_f32_e32 v130, 0xbfb8aa3b, v130
	v_exp_f32_e32 v131, v131
	v_exp_f32_e32 v135, v135
	v_exp_f32_e32 v137, v130
	v_mul_f32_e32 v134, 0xbfb8aa3b, v134
	v_exp_f32_e32 v134, v134
	v_pk_fma_f32 v[132:133], v[132:133], s[78:79], v[74:75] op_sel_hi:[1,0,1]
	v_add_f32_e32 v131, 1.0, v131
	v_add_f32_e32 v130, 1.0, v135
	v_add_f32_e32 v135, 1.0, v137
	v_rcp_f32_e32 v137, v131
	v_mul_f32_e32 v131, 0xbfb8aa3b, v132
	v_exp_f32_e32 v131, v131
	v_add_f32_e32 v134, 1.0, v134
	v_rcp_f32_e32 v134, v134
	v_rcp_f32_e32 v135, v135
	v_add_f32_e32 v131, 1.0, v131
	s_waitcnt vmcnt(28)
	v_lshlrev_b32_e32 v141, 16, v206
	v_lshlrev_b32_e32 v140, 16, v204
	v_rcp_f32_e32 v139, v131
	v_mul_f32_e32 v131, 0xbfb8aa3b, v133
	v_pk_mul_f32 v[134:135], v[134:135], v[140:141]
	v_exp_f32_e32 v131, v131
	v_add_f32_e32 v134, v216, v134
	v_add_f32_e32 v140, v134, v135
	v_and_b32_e32 v135, 0xffff0000, v206
	v_and_b32_e32 v134, 0xffff0000, v204
	v_pk_mul_f32 v[134:135], v[136:137], v[134:135]
	v_add_f32_e32 v131, 1.0, v131
	v_add_f32_e32 v132, v166, v134
	v_rcp_f32_e32 v130, v130
	v_add_f32_e32 v136, v132, v135
	v_lshlrev_b32_e32 v135, 16, v207
	v_lshlrev_b32_e32 v134, 16, v205
	v_rcp_f32_e32 v131, v131
	v_pk_mul_f32 v[132:133], v[138:139], v[134:135]
	v_pk_fma_f32 v[126:127], v[126:127], s[78:79], v[88:89] op_sel_hi:[1,0,1]
	v_add_f32_e32 v132, v144, v132
	v_add_f32_e32 v134, v132, v133
	v_and_b32_e32 v133, 0xffff0000, v207
	v_and_b32_e32 v132, 0xffff0000, v205
	v_pk_mul_f32 v[130:131], v[130:131], v[132:133]
	v_pk_fma_f32 v[128:129], v[128:129], s[78:79], v[90:91] op_sel_hi:[1,0,1]
	v_add_f32_e32 v130, v145, v130
	v_mul_f32_e32 v127, 0xbfb8aa3b, v127
	v_add_f32_e32 v131, v130, v131
	v_cvt_pk_bf16_f32 v130, v140, v136
	v_exp_f32_e32 v127, v127
	v_mul_f32_e32 v128, 0xbfb8aa3b, v128
	v_cvt_pk_bf16_f32 v131, v134, v131
	global_store_dwordx2 v[146:147], v[130:131], off
	v_exp_f32_e32 v130, v128
	v_add_f32_e32 v127, 1.0, v127
	v_pk_fma_f32 v[122:123], v[122:123], s[78:79], v[84:85] op_sel_hi:[1,0,1]
	v_rcp_f32_e32 v128, v127
	v_add_f32_e32 v127, 1.0, v130
	v_mul_f32_e32 v123, 0xbfb8aa3b, v123
	v_rcp_f32_e32 v130, v127
	v_mul_f32_e32 v127, 0xbfb8aa3b, v129
	v_mul_f32_e32 v122, 0xbfb8aa3b, v122
	v_exp_f32_e32 v123, v123
	v_exp_f32_e32 v127, v127
	v_exp_f32_e32 v129, v122
	v_mul_f32_e32 v126, 0xbfb8aa3b, v126
	v_exp_f32_e32 v126, v126
	v_pk_fma_f32 v[124:125], v[124:125], s[78:79], v[86:87] op_sel_hi:[1,0,1]
	v_add_f32_e32 v123, 1.0, v123
	v_add_f32_e32 v122, 1.0, v127
	v_add_f32_e32 v127, 1.0, v129
	v_rcp_f32_e32 v129, v123
	v_mul_f32_e32 v123, 0xbfb8aa3b, v124
	v_exp_f32_e32 v123, v123
	v_add_f32_e32 v126, 1.0, v126
	v_rcp_f32_e32 v126, v126
	v_rcp_f32_e32 v127, v127
	v_add_f32_e32 v123, 1.0, v123
	s_waitcnt vmcnt(27)
	v_lshlrev_b32_e32 v133, 16, v202
	v_lshlrev_b32_e32 v132, 16, v200
	v_rcp_f32_e32 v131, v123
	v_mul_f32_e32 v123, 0xbfb8aa3b, v125
	v_pk_mul_f32 v[126:127], v[126:127], v[132:133]
	v_exp_f32_e32 v123, v123
	v_add_f32_e32 v126, 0, v126
	v_add_f32_e32 v132, v126, v127
	v_and_b32_e32 v127, 0xffff0000, v202
	v_and_b32_e32 v126, 0xffff0000, v200
	v_pk_mul_f32 v[126:127], v[128:129], v[126:127]
	v_add_f32_e32 v123, 1.0, v123
	v_add_f32_e32 v124, 0, v126
	v_rcp_f32_e32 v122, v122
	v_add_f32_e32 v128, v124, v127
	v_lshlrev_b32_e32 v127, 16, v203
	v_lshlrev_b32_e32 v126, 16, v201
	v_rcp_f32_e32 v123, v123
	v_pk_mul_f32 v[124:125], v[130:131], v[126:127]
	v_pk_fma_f32 v[118:119], v[118:119], s[78:79], v[76:77] op_sel_hi:[1,0,1]
	v_add_f32_e32 v124, 0, v124
	v_add_f32_e32 v126, v124, v125
	v_and_b32_e32 v125, 0xffff0000, v203
	v_and_b32_e32 v124, 0xffff0000, v201
	v_pk_mul_f32 v[122:123], v[122:123], v[124:125]
	v_pk_fma_f32 v[120:121], v[120:121], s[78:79], v[78:79] op_sel_hi:[1,0,1]
	v_mul_f32_e32 v119, 0xbfb8aa3b, v119
	v_add_f32_e32 v122, 0, v122
	v_exp_f32_e32 v119, v119
	v_mul_f32_e32 v120, 0xbfb8aa3b, v120
	v_add_f32_e32 v127, v122, v123
	v_exp_f32_e32 v122, v120
	v_add_f32_e32 v119, 1.0, v119
	v_pk_fma_f32 v[114:115], v[114:115], s[78:79], v[72:73] op_sel_hi:[1,0,1]
	v_rcp_f32_e32 v120, v119
	v_add_f32_e32 v119, 1.0, v122
	v_mul_f32_e32 v115, 0xbfb8aa3b, v115
	v_rcp_f32_e32 v122, v119
	v_mul_f32_e32 v119, 0xbfb8aa3b, v121
	v_mul_f32_e32 v114, 0xbfb8aa3b, v114
	v_exp_f32_e32 v115, v115
	v_exp_f32_e32 v119, v119
	v_exp_f32_e32 v121, v114
	v_mul_f32_e32 v118, 0xbfb8aa3b, v118
	v_exp_f32_e32 v118, v118
	v_pk_fma_f32 v[116:117], v[116:117], s[78:79], v[74:75] op_sel_hi:[1,0,1]
	v_add_f32_e32 v115, 1.0, v115
	v_add_f32_e32 v114, 1.0, v119
	v_add_f32_e32 v119, 1.0, v121
	v_rcp_f32_e32 v121, v115
	v_mul_f32_e32 v115, 0xbfb8aa3b, v116
	v_exp_f32_e32 v115, v115
	v_add_f32_e32 v118, 1.0, v118
	v_rcp_f32_e32 v118, v118
	v_rcp_f32_e32 v119, v119
	v_add_f32_e32 v115, 1.0, v115
	s_waitcnt vmcnt(25)
	v_lshlrev_b32_e32 v125, 16, v198
	v_lshlrev_b32_e32 v124, 16, v196
	v_rcp_f32_e32 v123, v115
	v_mul_f32_e32 v115, 0xbfb8aa3b, v117
	v_pk_mul_f32 v[118:119], v[118:119], v[124:125]
	v_exp_f32_e32 v115, v115
	v_add_f32_e32 v118, v132, v118
	v_add_f32_e32 v124, v118, v119
	v_and_b32_e32 v119, 0xffff0000, v198
	v_and_b32_e32 v118, 0xffff0000, v196
	v_pk_mul_f32 v[118:119], v[120:121], v[118:119]
	v_add_f32_e32 v115, 1.0, v115
	v_add_f32_e32 v116, v128, v118
	v_rcp_f32_e32 v114, v114
	v_add_f32_e32 v120, v116, v119
	v_lshlrev_b32_e32 v119, 16, v199
	v_lshlrev_b32_e32 v118, 16, v197
	v_rcp_f32_e32 v115, v115
	v_pk_mul_f32 v[116:117], v[122:123], v[118:119]
	v_pk_fma_f32 v[110:111], v[110:111], s[78:79], v[88:89] op_sel_hi:[1,0,1]
	v_add_f32_e32 v116, v126, v116
	v_add_f32_e32 v118, v116, v117
	v_and_b32_e32 v117, 0xffff0000, v199
	v_and_b32_e32 v116, 0xffff0000, v197
	v_pk_mul_f32 v[114:115], v[114:115], v[116:117]
	s_mov_b32 s2, 0x10000
	v_add_f32_e32 v114, v127, v114
	v_add_co_u32_e32 v116, vcc, s2, v146
	v_pk_fma_f32 v[112:113], v[112:113], s[78:79], v[90:91] op_sel_hi:[1,0,1]
	v_mul_f32_e32 v111, 0xbfb8aa3b, v111
	v_add_f32_e32 v115, v114, v115
	v_cvt_pk_bf16_f32 v114, v124, v120
	v_addc_co_u32_e32 v117, vcc, 0, v147, vcc
	v_exp_f32_e32 v111, v111
	v_mul_f32_e32 v112, 0xbfb8aa3b, v112
	v_cvt_pk_bf16_f32 v115, v118, v115
	global_store_dwordx2 v[116:117], v[114:115], off
	v_exp_f32_e32 v114, v112
	v_add_f32_e32 v111, 1.0, v111
	v_pk_fma_f32 v[106:107], v[106:107], s[78:79], v[84:85] op_sel_hi:[1,0,1]
	v_rcp_f32_e32 v112, v111
	v_add_f32_e32 v111, 1.0, v114
	v_mul_f32_e32 v107, 0xbfb8aa3b, v107
	v_rcp_f32_e32 v114, v111
	v_mul_f32_e32 v111, 0xbfb8aa3b, v113
	v_mul_f32_e32 v106, 0xbfb8aa3b, v106
	v_exp_f32_e32 v107, v107
	v_exp_f32_e32 v111, v111
	v_exp_f32_e32 v113, v106
	v_mul_f32_e32 v110, 0xbfb8aa3b, v110
	v_exp_f32_e32 v110, v110
	v_pk_fma_f32 v[108:109], v[108:109], s[78:79], v[86:87] op_sel_hi:[1,0,1]
	v_add_f32_e32 v107, 1.0, v107
	v_add_f32_e32 v106, 1.0, v111
	v_add_f32_e32 v111, 1.0, v113
	v_rcp_f32_e32 v113, v107
	v_mul_f32_e32 v107, 0xbfb8aa3b, v108
	v_exp_f32_e32 v107, v107
	v_add_f32_e32 v110, 1.0, v110
	v_rcp_f32_e32 v110, v110
	v_rcp_f32_e32 v111, v111
	v_add_f32_e32 v107, 1.0, v107
	s_waitcnt vmcnt(24)
	v_lshlrev_b32_e32 v117, 16, v194
	v_lshlrev_b32_e32 v116, 16, v192
	v_rcp_f32_e32 v115, v107
	v_mul_f32_e32 v107, 0xbfb8aa3b, v109
	v_pk_mul_f32 v[110:111], v[110:111], v[116:117]
	v_exp_f32_e32 v107, v107
	v_add_f32_e32 v110, 0, v110
	v_add_f32_e32 v116, v110, v111
	v_and_b32_e32 v111, 0xffff0000, v194
	v_and_b32_e32 v110, 0xffff0000, v192
	v_pk_mul_f32 v[110:111], v[112:113], v[110:111]
	v_add_f32_e32 v107, 1.0, v107
	v_add_f32_e32 v108, 0, v110
	v_rcp_f32_e32 v106, v106
	v_add_f32_e32 v112, v108, v111
	v_lshlrev_b32_e32 v111, 16, v195
	v_lshlrev_b32_e32 v110, 16, v193
	v_rcp_f32_e32 v107, v107
	v_pk_mul_f32 v[108:109], v[114:115], v[110:111]
	v_pk_fma_f32 v[102:103], v[102:103], s[78:79], v[76:77] op_sel_hi:[1,0,1]
	v_add_f32_e32 v108, 0, v108
	v_add_f32_e32 v110, v108, v109
	v_and_b32_e32 v109, 0xffff0000, v195
	v_and_b32_e32 v108, 0xffff0000, v193
	v_pk_mul_f32 v[106:107], v[106:107], v[108:109]
	v_pk_fma_f32 v[104:105], v[104:105], s[78:79], v[78:79] op_sel_hi:[1,0,1]
	v_mul_f32_e32 v103, 0xbfb8aa3b, v103
	v_add_f32_e32 v106, 0, v106
	v_exp_f32_e32 v103, v103
	v_mul_f32_e32 v104, 0xbfb8aa3b, v104
	v_add_f32_e32 v111, v106, v107
	v_exp_f32_e32 v106, v104
	v_add_f32_e32 v103, 1.0, v103
	v_pk_fma_f32 v[98:99], v[98:99], s[78:79], v[72:73] op_sel_hi:[1,0,1]
	v_rcp_f32_e32 v104, v103
	v_add_f32_e32 v103, 1.0, v106
	v_mul_f32_e32 v99, 0xbfb8aa3b, v99
	v_rcp_f32_e32 v106, v103
	v_mul_f32_e32 v103, 0xbfb8aa3b, v105
	v_mul_f32_e32 v98, 0xbfb8aa3b, v98
	v_exp_f32_e32 v99, v99
	v_exp_f32_e32 v103, v103
	v_exp_f32_e32 v105, v98
	v_mul_f32_e32 v102, 0xbfb8aa3b, v102
	v_exp_f32_e32 v102, v102
	v_pk_fma_f32 v[100:101], v[100:101], s[78:79], v[74:75] op_sel_hi:[1,0,1]
	v_add_f32_e32 v99, 1.0, v99
	v_add_f32_e32 v98, 1.0, v103
	v_add_f32_e32 v103, 1.0, v105
	v_rcp_f32_e32 v105, v99
	v_mul_f32_e32 v99, 0xbfb8aa3b, v100
	v_exp_f32_e32 v99, v99
	v_add_f32_e32 v102, 1.0, v102
	v_rcp_f32_e32 v102, v102
	v_rcp_f32_e32 v103, v103
	v_add_f32_e32 v99, 1.0, v99
	s_waitcnt vmcnt(22)
	v_lshlrev_b32_e32 v109, 16, v190
	v_lshlrev_b32_e32 v108, 16, v188
	v_rcp_f32_e32 v107, v99
	v_mul_f32_e32 v99, 0xbfb8aa3b, v101
	v_pk_mul_f32 v[102:103], v[102:103], v[108:109]
	v_exp_f32_e32 v99, v99
	v_add_f32_e32 v102, v116, v102
	v_add_f32_e32 v108, v102, v103
	v_and_b32_e32 v103, 0xffff0000, v190
	v_and_b32_e32 v102, 0xffff0000, v188
	v_pk_mul_f32 v[102:103], v[104:105], v[102:103]
	v_add_f32_e32 v99, 1.0, v99
	v_add_f32_e32 v100, v112, v102
	v_rcp_f32_e32 v98, v98
	v_add_f32_e32 v104, v100, v103
	v_lshlrev_b32_e32 v103, 16, v191
	v_lshlrev_b32_e32 v102, 16, v189
	v_rcp_f32_e32 v99, v99
	v_pk_mul_f32 v[100:101], v[106:107], v[102:103]
	v_pk_fma_f32 v[92:93], v[92:93], s[78:79], v[88:89] op_sel_hi:[1,0,1]
	v_add_f32_e32 v100, v110, v100
	v_add_f32_e32 v102, v100, v101
	v_and_b32_e32 v101, 0xffff0000, v191
	v_and_b32_e32 v100, 0xffff0000, v189
	v_pk_mul_f32 v[98:99], v[98:99], v[100:101]
	v_add_co_u32_e32 v100, vcc, s75, v146
	v_add_f32_e32 v98, v111, v98
	v_pk_fma_f32 v[94:95], v[94:95], s[78:79], v[90:91] op_sel_hi:[1,0,1]
	v_mul_f32_e32 v93, 0xbfb8aa3b, v93
	v_add_f32_e32 v99, v98, v99
	v_cvt_pk_bf16_f32 v98, v108, v104
	v_addc_co_u32_e32 v101, vcc, 0, v147, vcc
	v_exp_f32_e32 v93, v93
	v_mul_f32_e32 v94, 0xbfb8aa3b, v94
	v_cvt_pk_bf16_f32 v99, v102, v99
	global_store_dwordx2 v[100:101], v[98:99], off
	v_exp_f32_e32 v98, v94
	v_add_f32_e32 v93, 1.0, v93
	v_pk_fma_f32 v[80:81], v[80:81], s[78:79], v[84:85] op_sel_hi:[1,0,1]
	v_rcp_f32_e32 v94, v93
	v_add_f32_e32 v93, 1.0, v98
	v_mul_f32_e32 v81, 0xbfb8aa3b, v81
	v_rcp_f32_e32 v98, v93
	v_mul_f32_e32 v93, 0xbfb8aa3b, v95
	v_mul_f32_e32 v80, 0xbfb8aa3b, v80
	v_exp_f32_e32 v81, v81
	v_exp_f32_e32 v93, v93
	v_exp_f32_e32 v95, v80
	v_mul_f32_e32 v92, 0xbfb8aa3b, v92
	v_exp_f32_e32 v92, v92
	v_pk_fma_f32 v[82:83], v[82:83], s[78:79], v[86:87] op_sel_hi:[1,0,1]
	v_add_f32_e32 v81, 1.0, v81
	v_add_f32_e32 v80, 1.0, v93
	v_add_f32_e32 v93, 1.0, v95
	v_rcp_f32_e32 v95, v81
	v_mul_f32_e32 v81, 0xbfb8aa3b, v82
	v_exp_f32_e32 v81, v81
	v_add_f32_e32 v92, 1.0, v92
	v_rcp_f32_e32 v92, v92
	v_rcp_f32_e32 v93, v93
	v_add_f32_e32 v81, 1.0, v81
	s_waitcnt vmcnt(21)
	v_lshlrev_b32_e32 v101, 16, v186
	v_lshlrev_b32_e32 v100, 16, v184
	v_rcp_f32_e32 v99, v81
	v_mul_f32_e32 v81, 0xbfb8aa3b, v83
	v_pk_mul_f32 v[92:93], v[92:93], v[100:101]
	v_exp_f32_e32 v81, v81
	v_add_f32_e32 v92, 0, v92
	v_add_f32_e32 v100, v92, v93
	v_and_b32_e32 v93, 0xffff0000, v186
	v_and_b32_e32 v92, 0xffff0000, v184
	v_pk_mul_f32 v[92:93], v[94:95], v[92:93]
	v_add_f32_e32 v81, 1.0, v81
	v_add_f32_e32 v82, 0, v92
	v_rcp_f32_e32 v80, v80
	v_add_f32_e32 v94, v82, v93
	v_lshlrev_b32_e32 v93, 16, v187
	v_lshlrev_b32_e32 v92, 16, v185
	v_rcp_f32_e32 v81, v81
	v_pk_mul_f32 v[82:83], v[98:99], v[92:93]
	v_pk_fma_f32 v[68:69], v[68:69], s[78:79], v[76:77] op_sel_hi:[1,0,1]
	v_add_f32_e32 v82, 0, v82
	v_add_f32_e32 v92, v82, v83
	v_and_b32_e32 v83, 0xffff0000, v187
	v_and_b32_e32 v82, 0xffff0000, v185
	v_pk_mul_f32 v[80:81], v[80:81], v[82:83]
	v_pk_fma_f32 v[70:71], v[70:71], s[78:79], v[78:79] op_sel_hi:[1,0,1]
	v_mul_f32_e32 v69, 0xbfb8aa3b, v69
	v_add_f32_e32 v80, 0, v80
	v_exp_f32_e32 v69, v69
	v_mul_f32_e32 v70, 0xbfb8aa3b, v70
	v_add_f32_e32 v93, v80, v81
	v_exp_f32_e32 v80, v70
	v_add_f32_e32 v69, 1.0, v69
	v_pk_fma_f32 v[64:65], v[64:65], s[78:79], v[72:73] op_sel_hi:[1,0,1]
	v_rcp_f32_e32 v70, v69
	v_add_f32_e32 v69, 1.0, v80
	v_mul_f32_e32 v65, 0xbfb8aa3b, v65
	v_rcp_f32_e32 v80, v69
	v_mul_f32_e32 v69, 0xbfb8aa3b, v71
	v_mul_f32_e32 v64, 0xbfb8aa3b, v64
	v_exp_f32_e32 v65, v65
	v_exp_f32_e32 v69, v69
	v_exp_f32_e32 v71, v64
	v_mul_f32_e32 v68, 0xbfb8aa3b, v68
	v_exp_f32_e32 v68, v68
	v_pk_fma_f32 v[66:67], v[66:67], s[78:79], v[74:75] op_sel_hi:[1,0,1]
	v_add_f32_e32 v65, 1.0, v65
	v_add_f32_e32 v64, 1.0, v69
	v_add_f32_e32 v69, 1.0, v71
	v_rcp_f32_e32 v71, v65
	v_mul_f32_e32 v65, 0xbfb8aa3b, v66
	v_exp_f32_e32 v65, v65
	v_add_f32_e32 v68, 1.0, v68
	v_rcp_f32_e32 v68, v68
	v_rcp_f32_e32 v69, v69
	v_add_f32_e32 v65, 1.0, v65
	s_waitcnt vmcnt(19)
	v_lshlrev_b32_e32 v83, 16, v182
	v_lshlrev_b32_e32 v82, 16, v180
	v_rcp_f32_e32 v81, v65
	v_mul_f32_e32 v65, 0xbfb8aa3b, v67
	v_pk_mul_f32 v[68:69], v[68:69], v[82:83]
	v_exp_f32_e32 v65, v65
	v_add_f32_e32 v68, v100, v68
	v_add_f32_e32 v82, v68, v69
	v_and_b32_e32 v69, 0xffff0000, v182
	v_and_b32_e32 v68, 0xffff0000, v180
	v_pk_mul_f32 v[68:69], v[70:71], v[68:69]
	v_add_f32_e32 v65, 1.0, v65
	v_add_f32_e32 v66, v94, v68
	v_rcp_f32_e32 v64, v64
	v_add_f32_e32 v70, v66, v69
	v_lshlrev_b32_e32 v69, 16, v183
	v_lshlrev_b32_e32 v68, 16, v181
	v_rcp_f32_e32 v65, v65
	v_pk_mul_f32 v[66:67], v[80:81], v[68:69]
	v_pk_fma_f32 v[60:61], v[60:61], s[78:79], v[88:89] op_sel_hi:[1,0,1]
	v_add_f32_e32 v66, v92, v66
	v_add_f32_e32 v68, v66, v67
	v_and_b32_e32 v67, 0xffff0000, v183
	v_and_b32_e32 v66, 0xffff0000, v181
	v_pk_mul_f32 v[64:65], v[64:65], v[66:67]
	s_mov_b32 s2, 0x30000
	v_add_f32_e32 v64, v93, v64
	v_add_co_u32_e32 v66, vcc, s2, v146
	v_pk_fma_f32 v[62:63], v[62:63], s[78:79], v[90:91] op_sel_hi:[1,0,1]
	v_mul_f32_e32 v61, 0xbfb8aa3b, v61
	v_add_f32_e32 v65, v64, v65
	v_cvt_pk_bf16_f32 v64, v82, v70
	v_addc_co_u32_e32 v67, vcc, 0, v147, vcc
	v_exp_f32_e32 v61, v61
	v_mul_f32_e32 v62, 0xbfb8aa3b, v62
	v_cvt_pk_bf16_f32 v65, v68, v65
	global_store_dwordx2 v[66:67], v[64:65], off
	v_exp_f32_e32 v64, v62
	v_add_f32_e32 v61, 1.0, v61
	v_pk_fma_f32 v[56:57], v[56:57], s[78:79], v[84:85] op_sel_hi:[1,0,1]
	v_rcp_f32_e32 v62, v61
	v_add_f32_e32 v61, 1.0, v64
	v_mul_f32_e32 v57, 0xbfb8aa3b, v57
	v_rcp_f32_e32 v64, v61
	v_mul_f32_e32 v61, 0xbfb8aa3b, v63
	v_mul_f32_e32 v56, 0xbfb8aa3b, v56
	v_exp_f32_e32 v57, v57
	v_exp_f32_e32 v61, v61
	v_exp_f32_e32 v63, v56
	v_mul_f32_e32 v60, 0xbfb8aa3b, v60
	v_exp_f32_e32 v60, v60
	v_pk_fma_f32 v[58:59], v[58:59], s[78:79], v[86:87] op_sel_hi:[1,0,1]
	v_add_f32_e32 v57, 1.0, v57
	v_add_f32_e32 v56, 1.0, v61
	v_add_f32_e32 v61, 1.0, v63
	v_rcp_f32_e32 v63, v57
	v_mul_f32_e32 v57, 0xbfb8aa3b, v58
	v_exp_f32_e32 v57, v57
	v_add_f32_e32 v60, 1.0, v60
	v_rcp_f32_e32 v60, v60
	v_rcp_f32_e32 v61, v61
	v_add_f32_e32 v57, 1.0, v57
	s_waitcnt vmcnt(18)
	v_lshlrev_b32_e32 v67, 16, v178
	v_lshlrev_b32_e32 v66, 16, v176
	v_rcp_f32_e32 v65, v57
	v_mul_f32_e32 v57, 0xbfb8aa3b, v59
	v_pk_mul_f32 v[60:61], v[60:61], v[66:67]
	v_exp_f32_e32 v57, v57
	v_add_f32_e32 v60, 0, v60
	v_add_f32_e32 v66, v60, v61
	v_and_b32_e32 v61, 0xffff0000, v178
	v_and_b32_e32 v60, 0xffff0000, v176
	v_pk_mul_f32 v[60:61], v[62:63], v[60:61]
	v_add_f32_e32 v57, 1.0, v57
	v_add_f32_e32 v58, 0, v60
	v_rcp_f32_e32 v56, v56
	v_add_f32_e32 v62, v58, v61
	v_lshlrev_b32_e32 v61, 16, v179
	v_lshlrev_b32_e32 v60, 16, v177
	v_rcp_f32_e32 v57, v57
	v_pk_mul_f32 v[58:59], v[64:65], v[60:61]
	v_pk_fma_f32 v[52:53], v[52:53], s[78:79], v[76:77] op_sel_hi:[1,0,1]
	v_add_f32_e32 v58, 0, v58
	v_add_f32_e32 v60, v58, v59
	v_and_b32_e32 v59, 0xffff0000, v179
	v_and_b32_e32 v58, 0xffff0000, v177
	v_pk_mul_f32 v[56:57], v[56:57], v[58:59]
	v_pk_fma_f32 v[54:55], v[54:55], s[78:79], v[78:79] op_sel_hi:[1,0,1]
	v_mul_f32_e32 v53, 0xbfb8aa3b, v53
	v_add_f32_e32 v56, 0, v56
	v_exp_f32_e32 v53, v53
	v_mul_f32_e32 v54, 0xbfb8aa3b, v54
	v_add_f32_e32 v61, v56, v57
	v_exp_f32_e32 v56, v54
	v_add_f32_e32 v53, 1.0, v53
	v_pk_fma_f32 v[48:49], v[48:49], s[78:79], v[72:73] op_sel_hi:[1,0,1]
	v_rcp_f32_e32 v54, v53
	v_add_f32_e32 v53, 1.0, v56
	v_mul_f32_e32 v49, 0xbfb8aa3b, v49
	v_rcp_f32_e32 v56, v53
	v_mul_f32_e32 v53, 0xbfb8aa3b, v55
	v_mul_f32_e32 v48, 0xbfb8aa3b, v48
	v_exp_f32_e32 v49, v49
	v_exp_f32_e32 v53, v53
	v_exp_f32_e32 v55, v48
	v_mul_f32_e32 v52, 0xbfb8aa3b, v52
	v_exp_f32_e32 v52, v52
	v_pk_fma_f32 v[50:51], v[50:51], s[78:79], v[74:75] op_sel_hi:[1,0,1]
	v_add_f32_e32 v49, 1.0, v49
	v_add_f32_e32 v48, 1.0, v53
	v_add_f32_e32 v53, 1.0, v55
	v_rcp_f32_e32 v55, v49
	v_mul_f32_e32 v49, 0xbfb8aa3b, v50
	v_exp_f32_e32 v49, v49
	v_add_f32_e32 v52, 1.0, v52
	v_rcp_f32_e32 v52, v52
	v_rcp_f32_e32 v53, v53
	v_add_f32_e32 v49, 1.0, v49
	s_waitcnt vmcnt(16)
	v_lshlrev_b32_e32 v59, 16, v174
	v_lshlrev_b32_e32 v58, 16, v172
	v_rcp_f32_e32 v57, v49
	v_mul_f32_e32 v49, 0xbfb8aa3b, v51
	v_pk_mul_f32 v[52:53], v[52:53], v[58:59]
	v_exp_f32_e32 v49, v49
	v_add_f32_e32 v52, v66, v52
	v_add_f32_e32 v58, v52, v53
	v_and_b32_e32 v53, 0xffff0000, v174
	v_and_b32_e32 v52, 0xffff0000, v172
	v_pk_mul_f32 v[52:53], v[54:55], v[52:53]
	v_add_f32_e32 v49, 1.0, v49
	v_add_f32_e32 v50, v62, v52
	v_rcp_f32_e32 v48, v48
	v_add_f32_e32 v54, v50, v53
	v_lshlrev_b32_e32 v53, 16, v175
	v_lshlrev_b32_e32 v52, 16, v173
	v_rcp_f32_e32 v49, v49
	v_pk_mul_f32 v[50:51], v[56:57], v[52:53]
	v_pk_fma_f32 v[44:45], v[44:45], s[78:79], v[88:89] op_sel_hi:[1,0,1]
	v_add_f32_e32 v50, v60, v50
	v_add_f32_e32 v52, v50, v51
	v_and_b32_e32 v51, 0xffff0000, v175
	v_and_b32_e32 v50, 0xffff0000, v173
	v_pk_mul_f32 v[48:49], v[48:49], v[50:51]
	s_mov_b32 s2, 0x80000
	v_add_f32_e32 v48, v61, v48
	v_add_co_u32_e32 v50, vcc, s2, v146
	v_pk_fma_f32 v[46:47], v[46:47], s[78:79], v[90:91] op_sel_hi:[1,0,1]
	v_mul_f32_e32 v45, 0xbfb8aa3b, v45
	v_add_f32_e32 v49, v48, v49
	v_cvt_pk_bf16_f32 v48, v58, v54
	v_addc_co_u32_e32 v51, vcc, 0, v147, vcc
	v_exp_f32_e32 v45, v45
	v_mul_f32_e32 v46, 0xbfb8aa3b, v46
	v_cvt_pk_bf16_f32 v49, v52, v49
	global_store_dwordx2 v[50:51], v[48:49], off
	v_exp_f32_e32 v48, v46
	v_add_f32_e32 v45, 1.0, v45
	v_pk_fma_f32 v[40:41], v[40:41], s[78:79], v[84:85] op_sel_hi:[1,0,1]
	v_rcp_f32_e32 v46, v45
	v_add_f32_e32 v45, 1.0, v48
	v_mul_f32_e32 v41, 0xbfb8aa3b, v41
	v_rcp_f32_e32 v48, v45
	v_mul_f32_e32 v45, 0xbfb8aa3b, v47
	v_mul_f32_e32 v40, 0xbfb8aa3b, v40
	v_exp_f32_e32 v41, v41
	v_exp_f32_e32 v45, v45
	v_exp_f32_e32 v47, v40
	v_mul_f32_e32 v44, 0xbfb8aa3b, v44
	v_exp_f32_e32 v44, v44
	v_pk_fma_f32 v[42:43], v[42:43], s[78:79], v[86:87] op_sel_hi:[1,0,1]
	v_add_f32_e32 v41, 1.0, v41
	v_add_f32_e32 v40, 1.0, v45
	v_add_f32_e32 v45, 1.0, v47
	v_rcp_f32_e32 v47, v41
	v_mul_f32_e32 v41, 0xbfb8aa3b, v42
	v_exp_f32_e32 v41, v41
	v_add_f32_e32 v44, 1.0, v44
	v_rcp_f32_e32 v44, v44
	v_rcp_f32_e32 v45, v45
	v_add_f32_e32 v41, 1.0, v41
	s_waitcnt vmcnt(15)
	v_lshlrev_b32_e32 v51, 16, v170
	v_lshlrev_b32_e32 v50, 16, v168
	v_rcp_f32_e32 v49, v41
	v_mul_f32_e32 v41, 0xbfb8aa3b, v43
	v_pk_mul_f32 v[44:45], v[44:45], v[50:51]
	v_exp_f32_e32 v41, v41
	v_add_f32_e32 v44, 0, v44
	v_add_f32_e32 v50, v44, v45
	v_and_b32_e32 v45, 0xffff0000, v170
	v_and_b32_e32 v44, 0xffff0000, v168
	v_pk_mul_f32 v[44:45], v[46:47], v[44:45]
	v_add_f32_e32 v41, 1.0, v41
	v_add_f32_e32 v42, 0, v44
	v_rcp_f32_e32 v40, v40
	v_add_f32_e32 v46, v42, v45
	v_lshlrev_b32_e32 v45, 16, v171
	v_lshlrev_b32_e32 v44, 16, v169
	v_rcp_f32_e32 v41, v41
	v_pk_mul_f32 v[42:43], v[48:49], v[44:45]
	v_pk_fma_f32 v[36:37], v[36:37], s[78:79], v[76:77] op_sel_hi:[1,0,1]
	v_add_f32_e32 v42, 0, v42
	v_add_f32_e32 v44, v42, v43
	v_and_b32_e32 v43, 0xffff0000, v171
	v_and_b32_e32 v42, 0xffff0000, v169
	v_pk_mul_f32 v[40:41], v[40:41], v[42:43]
	v_pk_fma_f32 v[38:39], v[38:39], s[78:79], v[78:79] op_sel_hi:[1,0,1]
	v_mul_f32_e32 v37, 0xbfb8aa3b, v37
	v_add_f32_e32 v40, 0, v40
	v_exp_f32_e32 v37, v37
	v_mul_f32_e32 v38, 0xbfb8aa3b, v38
	v_add_f32_e32 v45, v40, v41
	v_exp_f32_e32 v40, v38
	v_add_f32_e32 v37, 1.0, v37
	v_pk_fma_f32 v[32:33], v[32:33], s[78:79], v[72:73] op_sel_hi:[1,0,1]
	v_rcp_f32_e32 v38, v37
	v_add_f32_e32 v37, 1.0, v40
	v_mul_f32_e32 v33, 0xbfb8aa3b, v33
	v_rcp_f32_e32 v40, v37
	v_mul_f32_e32 v37, 0xbfb8aa3b, v39
	v_mul_f32_e32 v32, 0xbfb8aa3b, v32
	v_exp_f32_e32 v33, v33
	v_exp_f32_e32 v37, v37
	v_exp_f32_e32 v39, v32
	v_mul_f32_e32 v36, 0xbfb8aa3b, v36
	v_exp_f32_e32 v36, v36
	v_pk_fma_f32 v[34:35], v[34:35], s[78:79], v[74:75] op_sel_hi:[1,0,1]
	v_add_f32_e32 v33, 1.0, v33
	v_add_f32_e32 v32, 1.0, v37
	v_add_f32_e32 v37, 1.0, v39
	v_rcp_f32_e32 v39, v33
	v_mul_f32_e32 v33, 0xbfb8aa3b, v34
	v_exp_f32_e32 v33, v33
	v_add_f32_e32 v36, 1.0, v36
	v_rcp_f32_e32 v36, v36
	v_rcp_f32_e32 v37, v37
	v_add_f32_e32 v33, 1.0, v33
	s_waitcnt vmcnt(13)
	v_lshlrev_b32_e32 v43, 16, v164
	v_lshlrev_b32_e32 v42, 16, v162
	v_rcp_f32_e32 v41, v33
	v_mul_f32_e32 v33, 0xbfb8aa3b, v35
	v_pk_mul_f32 v[36:37], v[36:37], v[42:43]
	v_exp_f32_e32 v33, v33
	v_add_f32_e32 v36, v50, v36
	v_add_f32_e32 v42, v36, v37
	v_and_b32_e32 v37, 0xffff0000, v164
	v_and_b32_e32 v36, 0xffff0000, v162
	v_pk_mul_f32 v[36:37], v[38:39], v[36:37]
	v_add_f32_e32 v33, 1.0, v33
	v_add_f32_e32 v34, v46, v36
	v_rcp_f32_e32 v32, v32
	v_add_f32_e32 v38, v34, v37
	v_lshlrev_b32_e32 v37, 16, v165
	v_lshlrev_b32_e32 v36, 16, v163
	v_rcp_f32_e32 v33, v33
	v_pk_mul_f32 v[34:35], v[40:41], v[36:37]
	v_pk_fma_f32 v[28:29], v[28:29], s[78:79], v[88:89] op_sel_hi:[1,0,1]
	v_add_f32_e32 v34, v44, v34
	v_add_f32_e32 v36, v34, v35
	v_and_b32_e32 v35, 0xffff0000, v165
	v_and_b32_e32 v34, 0xffff0000, v163
	v_pk_mul_f32 v[32:33], v[32:33], v[34:35]
	s_mov_b32 s2, 0x90000
	v_add_f32_e32 v32, v45, v32
	v_add_co_u32_e32 v34, vcc, s2, v146
	v_pk_fma_f32 v[30:31], v[30:31], s[78:79], v[90:91] op_sel_hi:[1,0,1]
	v_mul_f32_e32 v29, 0xbfb8aa3b, v29
	v_add_f32_e32 v33, v32, v33
	v_cvt_pk_bf16_f32 v32, v42, v38
	v_addc_co_u32_e32 v35, vcc, 0, v147, vcc
	v_exp_f32_e32 v29, v29
	v_mul_f32_e32 v30, 0xbfb8aa3b, v30
	v_cvt_pk_bf16_f32 v33, v36, v33
	global_store_dwordx2 v[34:35], v[32:33], off
	v_exp_f32_e32 v32, v30
	v_add_f32_e32 v29, 1.0, v29
	v_pk_fma_f32 v[24:25], v[24:25], s[78:79], v[84:85] op_sel_hi:[1,0,1]
	v_rcp_f32_e32 v30, v29
	v_add_f32_e32 v29, 1.0, v32
	v_mul_f32_e32 v25, 0xbfb8aa3b, v25
	v_rcp_f32_e32 v32, v29
	v_mul_f32_e32 v29, 0xbfb8aa3b, v31
	v_mul_f32_e32 v24, 0xbfb8aa3b, v24
	v_exp_f32_e32 v25, v25
	v_exp_f32_e32 v29, v29
	v_exp_f32_e32 v31, v24
	v_mul_f32_e32 v28, 0xbfb8aa3b, v28
	v_exp_f32_e32 v28, v28
	v_pk_fma_f32 v[26:27], v[26:27], s[78:79], v[86:87] op_sel_hi:[1,0,1]
	v_add_f32_e32 v25, 1.0, v25
	v_add_f32_e32 v24, 1.0, v29
	v_add_f32_e32 v29, 1.0, v31
	v_rcp_f32_e32 v31, v25
	v_mul_f32_e32 v25, 0xbfb8aa3b, v26
	v_exp_f32_e32 v25, v25
	v_add_f32_e32 v28, 1.0, v28
	v_rcp_f32_e32 v28, v28
	v_rcp_f32_e32 v29, v29
	v_add_f32_e32 v25, 1.0, v25
	s_waitcnt vmcnt(12)
	v_lshlrev_b32_e32 v35, 16, v160
	v_lshlrev_b32_e32 v34, 16, v158
	v_rcp_f32_e32 v33, v25
	v_mul_f32_e32 v25, 0xbfb8aa3b, v27
	v_pk_mul_f32 v[28:29], v[28:29], v[34:35]
	v_exp_f32_e32 v25, v25
	v_add_f32_e32 v28, 0, v28
	v_add_f32_e32 v34, v28, v29
	v_and_b32_e32 v29, 0xffff0000, v160
	v_and_b32_e32 v28, 0xffff0000, v158
	v_pk_mul_f32 v[28:29], v[30:31], v[28:29]
	v_add_f32_e32 v25, 1.0, v25
	v_add_f32_e32 v26, 0, v28
	v_rcp_f32_e32 v24, v24
	v_add_f32_e32 v30, v26, v29
	v_lshlrev_b32_e32 v29, 16, v161
	v_lshlrev_b32_e32 v28, 16, v159
	v_rcp_f32_e32 v25, v25
	v_pk_mul_f32 v[26:27], v[32:33], v[28:29]
	v_pk_fma_f32 v[20:21], v[20:21], s[78:79], v[76:77] op_sel_hi:[1,0,1]
	v_add_f32_e32 v26, 0, v26
	v_add_f32_e32 v28, v26, v27
	v_and_b32_e32 v27, 0xffff0000, v161
	v_and_b32_e32 v26, 0xffff0000, v159
	v_pk_mul_f32 v[24:25], v[24:25], v[26:27]
	v_pk_fma_f32 v[22:23], v[22:23], s[78:79], v[78:79] op_sel_hi:[1,0,1]
	v_mul_f32_e32 v21, 0xbfb8aa3b, v21
	v_add_f32_e32 v24, 0, v24
	v_exp_f32_e32 v21, v21
	v_mul_f32_e32 v22, 0xbfb8aa3b, v22
	v_add_f32_e32 v29, v24, v25
	v_exp_f32_e32 v24, v22
	v_add_f32_e32 v21, 1.0, v21
	v_pk_fma_f32 v[16:17], v[16:17], s[78:79], v[72:73] op_sel_hi:[1,0,1]
	v_rcp_f32_e32 v22, v21
	v_add_f32_e32 v21, 1.0, v24
	v_mul_f32_e32 v17, 0xbfb8aa3b, v17
	v_rcp_f32_e32 v24, v21
	v_mul_f32_e32 v21, 0xbfb8aa3b, v23
	v_mul_f32_e32 v16, 0xbfb8aa3b, v16
	v_exp_f32_e32 v17, v17
	v_exp_f32_e32 v21, v21
	v_exp_f32_e32 v23, v16
	v_mul_f32_e32 v20, 0xbfb8aa3b, v20
	v_exp_f32_e32 v20, v20
	v_pk_fma_f32 v[18:19], v[18:19], s[78:79], v[74:75] op_sel_hi:[1,0,1]
	v_add_f32_e32 v17, 1.0, v17
	v_add_f32_e32 v16, 1.0, v21
	v_add_f32_e32 v21, 1.0, v23
	v_rcp_f32_e32 v23, v17
	v_mul_f32_e32 v17, 0xbfb8aa3b, v18
	v_exp_f32_e32 v17, v17
	v_add_f32_e32 v20, 1.0, v20
	v_rcp_f32_e32 v20, v20
	v_rcp_f32_e32 v21, v21
	v_add_f32_e32 v17, 1.0, v17
	s_waitcnt vmcnt(10)
	v_lshlrev_b32_e32 v27, 16, v156
	v_lshlrev_b32_e32 v26, 16, v154
	v_rcp_f32_e32 v25, v17
	v_mul_f32_e32 v17, 0xbfb8aa3b, v19
	v_pk_mul_f32 v[20:21], v[20:21], v[26:27]
	v_exp_f32_e32 v17, v17
	v_add_f32_e32 v20, v34, v20
	v_add_f32_e32 v26, v20, v21
	v_and_b32_e32 v21, 0xffff0000, v156
	v_and_b32_e32 v20, 0xffff0000, v154
	v_pk_mul_f32 v[20:21], v[22:23], v[20:21]
	v_add_f32_e32 v17, 1.0, v17
	v_add_f32_e32 v18, v30, v20
	v_rcp_f32_e32 v16, v16
	v_add_f32_e32 v22, v18, v21
	v_lshlrev_b32_e32 v21, 16, v157
	v_lshlrev_b32_e32 v20, 16, v155
	v_rcp_f32_e32 v17, v17
	v_pk_mul_f32 v[18:19], v[24:25], v[20:21]
	v_pk_fma_f32 v[12:13], v[12:13], s[78:79], v[88:89] op_sel_hi:[1,0,1]
	v_add_f32_e32 v18, v28, v18
	v_add_f32_e32 v20, v18, v19
	v_and_b32_e32 v19, 0xffff0000, v157
	v_and_b32_e32 v18, 0xffff0000, v155
	v_pk_mul_f32 v[16:17], v[16:17], v[18:19]
	s_mov_b32 s2, 0xa0000
	v_add_f32_e32 v16, v29, v16
	v_add_co_u32_e32 v18, vcc, s2, v146
	v_pk_fma_f32 v[14:15], v[14:15], s[78:79], v[90:91] op_sel_hi:[1,0,1]
	v_mul_f32_e32 v13, 0xbfb8aa3b, v13
	v_add_f32_e32 v17, v16, v17
	v_cvt_pk_bf16_f32 v16, v26, v22
	v_addc_co_u32_e32 v19, vcc, 0, v147, vcc
	v_exp_f32_e32 v13, v13
	v_mul_f32_e32 v14, 0xbfb8aa3b, v14
	v_cvt_pk_bf16_f32 v17, v20, v17
	global_store_dwordx2 v[18:19], v[16:17], off
	v_exp_f32_e32 v16, v14
	v_add_f32_e32 v13, 1.0, v13
	v_pk_fma_f32 v[8:9], v[8:9], s[78:79], v[84:85] op_sel_hi:[1,0,1]
	v_rcp_f32_e32 v14, v13
	v_add_f32_e32 v13, 1.0, v16
	v_mul_f32_e32 v9, 0xbfb8aa3b, v9
	v_rcp_f32_e32 v16, v13
	v_mul_f32_e32 v13, 0xbfb8aa3b, v15
	v_mul_f32_e32 v8, 0xbfb8aa3b, v8
	v_exp_f32_e32 v9, v9
	v_exp_f32_e32 v13, v13
	v_exp_f32_e32 v15, v8
	v_mul_f32_e32 v12, 0xbfb8aa3b, v12
	v_exp_f32_e32 v12, v12
	v_pk_fma_f32 v[10:11], v[10:11], s[78:79], v[86:87] op_sel_hi:[1,0,1]
	v_add_f32_e32 v9, 1.0, v9
	v_add_f32_e32 v8, 1.0, v13
	v_add_f32_e32 v13, 1.0, v15
	v_rcp_f32_e32 v15, v9
	v_mul_f32_e32 v9, 0xbfb8aa3b, v10
	v_exp_f32_e32 v9, v9
	v_add_f32_e32 v12, 1.0, v12
	v_rcp_f32_e32 v12, v12
	v_rcp_f32_e32 v13, v13
	v_add_f32_e32 v9, 1.0, v9
	s_waitcnt vmcnt(9)
	v_lshlrev_b32_e32 v19, 16, v152
	v_lshlrev_b32_e32 v18, 16, v150
	v_rcp_f32_e32 v17, v9
	v_mul_f32_e32 v9, 0xbfb8aa3b, v11
	v_pk_mul_f32 v[12:13], v[12:13], v[18:19]
	v_exp_f32_e32 v9, v9
	v_add_f32_e32 v12, 0, v12
	v_add_f32_e32 v18, v12, v13
	v_and_b32_e32 v13, 0xffff0000, v152
	v_and_b32_e32 v12, 0xffff0000, v150
	v_pk_mul_f32 v[12:13], v[14:15], v[12:13]
	v_add_f32_e32 v9, 1.0, v9
	v_add_f32_e32 v10, 0, v12
	v_rcp_f32_e32 v8, v8
	v_add_f32_e32 v14, v10, v13
	v_lshlrev_b32_e32 v13, 16, v153
	v_lshlrev_b32_e32 v12, 16, v151
	v_rcp_f32_e32 v9, v9
	v_pk_mul_f32 v[10:11], v[16:17], v[12:13]
	v_pk_fma_f32 v[4:5], v[4:5], s[78:79], v[76:77] op_sel_hi:[1,0,1]
	v_add_f32_e32 v10, 0, v10
	v_add_f32_e32 v12, v10, v11
	v_and_b32_e32 v11, 0xffff0000, v153
	v_and_b32_e32 v10, 0xffff0000, v151
	v_pk_mul_f32 v[8:9], v[8:9], v[10:11]
	v_pk_fma_f32 v[6:7], v[6:7], s[78:79], v[78:79] op_sel_hi:[1,0,1]
	v_mul_f32_e32 v5, 0xbfb8aa3b, v5
	v_add_f32_e32 v8, 0, v8
	v_exp_f32_e32 v5, v5
	v_mul_f32_e32 v6, 0xbfb8aa3b, v6
	v_add_f32_e32 v13, v8, v9
	v_exp_f32_e32 v8, v6
	v_add_f32_e32 v5, 1.0, v5
	v_pk_fma_f32 v[0:1], v[0:1], s[78:79], v[72:73] op_sel_hi:[1,0,1]
	v_rcp_f32_e32 v6, v5
	v_add_f32_e32 v5, 1.0, v8
	v_mul_f32_e32 v1, 0xbfb8aa3b, v1
	v_rcp_f32_e32 v8, v5
	v_mul_f32_e32 v5, 0xbfb8aa3b, v7
	v_mul_f32_e32 v0, 0xbfb8aa3b, v0
	v_exp_f32_e32 v1, v1
	v_exp_f32_e32 v5, v5
	v_exp_f32_e32 v7, v0
	v_mul_f32_e32 v4, 0xbfb8aa3b, v4
	v_exp_f32_e32 v4, v4
	v_pk_fma_f32 v[2:3], v[2:3], s[78:79], v[74:75] op_sel_hi:[1,0,1]
	v_add_f32_e32 v1, 1.0, v1
	v_add_f32_e32 v0, 1.0, v5
	v_add_f32_e32 v5, 1.0, v7
	v_rcp_f32_e32 v7, v1
	v_mul_f32_e32 v1, 0xbfb8aa3b, v2
	v_exp_f32_e32 v1, v1
	v_add_f32_e32 v4, 1.0, v4
	v_rcp_f32_e32 v4, v4
	v_rcp_f32_e32 v5, v5
	v_add_f32_e32 v1, 1.0, v1
	s_waitcnt vmcnt(7)
	v_lshlrev_b32_e32 v11, 16, v148
	v_lshlrev_b32_e32 v10, 16, v142
	v_rcp_f32_e32 v9, v1
	v_mul_f32_e32 v1, 0xbfb8aa3b, v3
	v_pk_mul_f32 v[4:5], v[4:5], v[10:11]
	v_exp_f32_e32 v1, v1
	v_add_f32_e32 v4, v18, v4
	v_add_f32_e32 v10, v4, v5
	v_and_b32_e32 v5, 0xffff0000, v148
	v_and_b32_e32 v4, 0xffff0000, v142
	v_pk_mul_f32 v[4:5], v[6:7], v[4:5]
	v_add_f32_e32 v1, 1.0, v1
	v_add_f32_e32 v2, v14, v4
	v_rcp_f32_e32 v0, v0
	v_add_f32_e32 v6, v2, v5
	v_lshlrev_b32_e32 v5, 16, v149
	v_lshlrev_b32_e32 v4, 16, v143
	v_rcp_f32_e32 v1, v1
	v_pk_mul_f32 v[2:3], v[8:9], v[4:5]
	s_mov_b32 s2, s20
	v_add_f32_e32 v2, v12, v2
	v_add_f32_e32 v4, v2, v3
	v_and_b32_e32 v3, 0xffff0000, v149
	v_and_b32_e32 v2, 0xffff0000, v143
	v_pk_mul_f32 v[0:1], v[0:1], v[2:3]
	v_add_co_u32_e32 v2, vcc, 0xb0000, v146
	v_add_f32_e32 v0, v13, v0
	s_nop 0
	v_addc_co_u32_e32 v3, vcc, 0, v147, vcc
	v_add_f32_e32 v1, v0, v1
	s_and_b64 vcc, exec, s[4:5]
	s_mov_b32 s18, s21
	s_mov_b32 s47, s23
	s_mov_b32 s46, s22
	v_mov_b32_e32 v213, 0x358637bd
	v_mov_b32_e32 v252, 0x3ba10414
	v_mov_b32_e32 v242, 2
	v_cvt_pk_bf16_f32 v0, v10, v6
	v_cvt_pk_bf16_f32 v1, v4, v1
	global_store_dwordx2 v[2:3], v[0:1], off
	s_cbranch_vccz .LBB0_1421
	s_branch .LBB0_1430

.LBB0_1496:
	ds_read_b128 v[32:35], v153
	ds_read_b128 v[36:39], v153 offset:1024
	ds_read_b128 v[40:43], v153 offset:2048
	ds_read_b128 v[44:47], v153 offset:3072
	s_add_i32 s10, s50, 0xfff80080
	s_cmp_eq_u32 s52, 28
	s_cselect_b32 s55, s48, s10
	s_cselect_b32 s53, s49, s51
	s_or_b32 s54, s55, 0x80
	s_mov_b32 m0, s44
	ds_read_b128 v[156:159], v154
	ds_read_b128 v[160:163], v154 offset:1024
	ds_read_b128 v[164:167], v154 offset:2048
	ds_read_b128 v[168:171], v154 offset:3072
	ds_read_b128 v[172:175], v154 offset:4096
	ds_read_b128 v[176:179], v154 offset:5120
	ds_read_b128 v[180:183], v154 offset:6144
	ds_read_b128 v[184:187], v154 offset:7168
	buffer_load_dwordx4 v149, s[72:75], s50 offen lds
	s_mov_b32 m0, s45
	s_nop 0
	buffer_load_dwordx4 v151, s[72:75], s50 offen lds
	s_waitcnt lgkmcnt(8)
	s_waitcnt vmcnt(10)
	s_barrier
	s_waitcnt lgkmcnt(0)
	s_setprio 1
	s_waitcnt lgkmcnt(7)
	v_mfma_f32_16x16x32_bf16 v[142:145], v[32:35], v[156:159], v[142:145]
	v_mfma_f32_16x16x32_bf16 v[138:141], v[40:43], v[156:159], v[138:141]
	s_waitcnt lgkmcnt(5)
	v_mfma_f32_16x16x32_bf16 v[134:137], v[32:35], v[164:167], v[134:137]
	v_mfma_f32_16x16x32_bf16 v[130:133], v[40:43], v[164:167], v[130:133]
	s_waitcnt lgkmcnt(3)
	v_mfma_f32_16x16x32_bf16 v[110:113], v[32:35], v[172:175], v[110:113]
	v_mfma_f32_16x16x32_bf16 v[106:109], v[40:43], v[172:175], v[106:109]
	s_waitcnt lgkmcnt(1)
	v_mfma_f32_16x16x32_bf16 v[102:105], v[32:35], v[180:183], v[102:105]
	v_mfma_f32_16x16x32_bf16 v[98:101], v[40:43], v[180:183], v[98:101]
	v_mfma_f32_16x16x32_bf16 v[142:145], v[36:39], v[160:163], v[142:145]
	v_mfma_f32_16x16x32_bf16 v[138:141], v[44:47], v[160:163], v[138:141]
	v_mfma_f32_16x16x32_bf16 v[134:137], v[36:39], v[168:171], v[134:137]
	v_mfma_f32_16x16x32_bf16 v[130:133], v[44:47], v[168:171], v[130:133]
	v_mfma_f32_16x16x32_bf16 v[110:113], v[36:39], v[176:179], v[110:113]
	v_mfma_f32_16x16x32_bf16 v[106:109], v[44:47], v[176:179], v[106:109]
	s_waitcnt lgkmcnt(0)
	v_mfma_f32_16x16x32_bf16 v[102:105], v[36:39], v[184:187], v[102:105]
	v_mfma_f32_16x16x32_bf16 v[98:101], v[44:47], v[184:187], v[98:101]
	s_setprio 0
	s_barrier
	s_mov_b32 s10, s74
	s_mov_b32 s11, s75
	s_mov_b32 m0, s29
	ds_read_b128 v[188:191], v153 offset:16384
	ds_read_b128 v[192:195], v153 offset:17408
	ds_read_b128 v[196:199], v153 offset:18432
	ds_read_b128 v[200:203], v153 offset:19456
	buffer_load_dwordx4 v150, s[8:11], s53 offen lds
	s_mov_b32 m0, s30
	s_nop 0
	buffer_load_dwordx4 v152, s[8:11], s53 offen lds
	s_waitcnt vmcnt(10)
	s_barrier
	s_waitcnt lgkmcnt(0)
	s_setprio 1
	s_waitcnt lgkmcnt(3)
	v_mfma_f32_16x16x32_bf16 v[126:129], v[188:191], v[156:159], v[126:129]
	s_waitcnt lgkmcnt(1)
	v_mfma_f32_16x16x32_bf16 v[122:125], v[196:199], v[156:159], v[122:125]
	v_mfma_f32_16x16x32_bf16 v[118:121], v[188:191], v[164:167], v[118:121]
	v_mfma_f32_16x16x32_bf16 v[114:117], v[196:199], v[164:167], v[114:117]
	v_mfma_f32_16x16x32_bf16 v[92:95], v[188:191], v[172:175], v[92:95]
	v_mfma_f32_16x16x32_bf16 v[88:91], v[196:199], v[172:175], v[88:91]
	v_mfma_f32_16x16x32_bf16 v[84:87], v[188:191], v[180:183], v[84:87]
	v_mfma_f32_16x16x32_bf16 v[80:83], v[196:199], v[180:183], v[80:83]
	v_mfma_f32_16x16x32_bf16 v[126:129], v[192:195], v[160:163], v[126:129]
	s_waitcnt lgkmcnt(0)
	v_mfma_f32_16x16x32_bf16 v[122:125], v[200:203], v[160:163], v[122:125]
	v_mfma_f32_16x16x32_bf16 v[118:121], v[192:195], v[168:171], v[118:121]
	v_mfma_f32_16x16x32_bf16 v[114:117], v[200:203], v[168:171], v[114:117]
	v_mfma_f32_16x16x32_bf16 v[92:95], v[192:195], v[176:179], v[92:95]
	v_mfma_f32_16x16x32_bf16 v[88:91], v[200:203], v[176:179], v[88:91]
	v_mfma_f32_16x16x32_bf16 v[84:87], v[192:195], v[184:187], v[84:87]
	v_mfma_f32_16x16x32_bf16 v[80:83], v[200:203], v[184:187], v[80:83]
	s_setprio 0
	s_mov_b32 m0, s28
	s_barrier
	ds_read_b128 v[156:159], v154 offset:16384
	ds_read_b128 v[160:163], v154 offset:17408
	ds_read_b128 v[164:167], v154 offset:18432
	ds_read_b128 v[168:171], v154 offset:19456
	ds_read_b128 v[172:175], v154 offset:20480
	ds_read_b128 v[176:179], v154 offset:21504
	ds_read_b128 v[180:183], v154 offset:22528
	ds_read_b128 v[184:187], v154 offset:23552
	buffer_load_dwordx4 v149, s[72:75], s55 offen lds
	s_mov_b32 m0, s31
	s_nop 0
	buffer_load_dwordx4 v151, s[72:75], s55 offen lds
	s_barrier
	s_waitcnt lgkmcnt(0)
	s_setprio 1
	s_waitcnt lgkmcnt(7)
	v_mfma_f32_16x16x32_bf16 v[76:79], v[32:35], v[156:159], v[76:79]
	v_mfma_f32_16x16x32_bf16 v[72:75], v[40:43], v[156:159], v[72:75]
	s_waitcnt lgkmcnt(5)
	v_mfma_f32_16x16x32_bf16 v[68:71], v[32:35], v[164:167], v[68:71]
	v_mfma_f32_16x16x32_bf16 v[64:67], v[40:43], v[164:167], v[64:67]
	s_waitcnt lgkmcnt(3)
	v_mfma_f32_16x16x32_bf16 v[28:31], v[32:35], v[172:175], v[28:31]
	v_mfma_f32_16x16x32_bf16 v[24:27], v[40:43], v[172:175], v[24:27]
	s_waitcnt lgkmcnt(1)
	v_mfma_f32_16x16x32_bf16 v[16:19], v[32:35], v[180:183], v[16:19]
	v_mfma_f32_16x16x32_bf16 v[8:11], v[40:43], v[180:183], v[8:11]
	v_mfma_f32_16x16x32_bf16 v[76:79], v[36:39], v[160:163], v[76:79]
	v_mfma_f32_16x16x32_bf16 v[72:75], v[44:47], v[160:163], v[72:75]
	v_mfma_f32_16x16x32_bf16 v[68:71], v[36:39], v[168:171], v[68:71]
	v_mfma_f32_16x16x32_bf16 v[64:67], v[44:47], v[168:171], v[64:67]
	v_mfma_f32_16x16x32_bf16 v[28:31], v[36:39], v[176:179], v[28:31]
	v_mfma_f32_16x16x32_bf16 v[24:27], v[44:47], v[176:179], v[24:27]
	s_waitcnt lgkmcnt(0)
	v_mfma_f32_16x16x32_bf16 v[16:19], v[36:39], v[184:187], v[16:19]
	v_mfma_f32_16x16x32_bf16 v[8:11], v[44:47], v[184:187], v[8:11]
	s_setprio 0
	s_barrier
	s_add_i32 s56, s53, 0x80000
	s_mov_b32 m0, s34
	s_nop 0
	buffer_load_dwordx4 v150, s[8:11], s56 offen lds
	s_mov_b32 m0, s35
	s_nop 0
	buffer_load_dwordx4 v152, s[8:11], s56 offen lds
	s_waitcnt vmcnt(10)
	s_barrier
	s_setprio 1
	v_mfma_f32_16x16x32_bf16 v[20:23], v[188:191], v[172:175], v[20:23]
	v_mfma_f32_16x16x32_bf16 v[12:15], v[196:199], v[172:175], v[12:15]
	v_mfma_f32_16x16x32_bf16 v[4:7], v[188:191], v[180:183], v[4:7]
	v_mfma_f32_16x16x32_bf16 v[0:3], v[196:199], v[180:183], v[0:3]
	v_mfma_f32_16x16x32_bf16 v[32:35], v[188:191], v[156:159], v[60:63]
	v_mfma_f32_16x16x32_bf16 v[36:39], v[196:199], v[156:159], v[56:59]
	v_mfma_f32_16x16x32_bf16 v[40:43], v[188:191], v[164:167], v[52:55]
	v_mfma_f32_16x16x32_bf16 v[44:47], v[196:199], v[164:167], v[48:51]
	v_mfma_f32_16x16x32_bf16 v[20:23], v[192:195], v[176:179], v[20:23]
	v_mfma_f32_16x16x32_bf16 v[12:15], v[200:203], v[176:179], v[12:15]
	v_mfma_f32_16x16x32_bf16 v[4:7], v[192:195], v[184:187], v[4:7]
	v_mfma_f32_16x16x32_bf16 v[0:3], v[200:203], v[184:187], v[0:3]
	v_mfma_f32_16x16x32_bf16 v[32:35], v[192:195], v[160:163], v[32:35]
	v_mfma_f32_16x16x32_bf16 v[36:39], v[200:203], v[160:163], v[36:39]
	v_mfma_f32_16x16x32_bf16 v[40:43], v[192:195], v[168:171], v[40:43]
	v_mfma_f32_16x16x32_bf16 v[44:47], v[200:203], v[168:171], v[44:47]
	s_setprio 0
	s_barrier
	ds_read_b128 v[48:51], v153 offset:32768
	ds_read_b128 v[52:55], v153 offset:33792
	ds_read_b128 v[56:59], v153 offset:34816
	ds_read_b128 v[60:63], v153 offset:35840
	s_add_i32 s55, s55, 0x80000
	s_mov_b32 m0, s36
	ds_read_b128 v[156:159], v154 offset:32768
	ds_read_b128 v[160:163], v154 offset:33792
	ds_read_b128 v[164:167], v154 offset:34816
	ds_read_b128 v[168:171], v154 offset:35840
	ds_read_b128 v[172:175], v154 offset:36864
	ds_read_b128 v[176:179], v154 offset:37888
	ds_read_b128 v[180:183], v154 offset:38912
	ds_read_b128 v[184:187], v154 offset:39936
	buffer_load_dwordx4 v149, s[72:75], s55 offen lds
	s_mov_b32 m0, s37
	s_nop 0
	buffer_load_dwordx4 v151, s[72:75], s55 offen lds
	s_waitcnt lgkmcnt(8)
	s_waitcnt vmcnt(10)
	s_barrier
	s_waitcnt lgkmcnt(0)
	s_setprio 1
	s_waitcnt lgkmcnt(7)
	v_mfma_f32_16x16x32_bf16 v[142:145], v[48:51], v[156:159], v[142:145]
	v_mfma_f32_16x16x32_bf16 v[138:141], v[56:59], v[156:159], v[138:141]
	s_waitcnt lgkmcnt(5)
	v_mfma_f32_16x16x32_bf16 v[134:137], v[48:51], v[164:167], v[134:137]
	v_mfma_f32_16x16x32_bf16 v[130:133], v[56:59], v[164:167], v[130:133]
	s_waitcnt lgkmcnt(3)
	v_mfma_f32_16x16x32_bf16 v[110:113], v[48:51], v[172:175], v[110:113]
	v_mfma_f32_16x16x32_bf16 v[106:109], v[56:59], v[172:175], v[106:109]
	s_waitcnt lgkmcnt(1)
	v_mfma_f32_16x16x32_bf16 v[102:105], v[48:51], v[180:183], v[102:105]
	v_mfma_f32_16x16x32_bf16 v[98:101], v[56:59], v[180:183], v[98:101]
	v_mfma_f32_16x16x32_bf16 v[142:145], v[52:55], v[160:163], v[142:145]
	v_mfma_f32_16x16x32_bf16 v[138:141], v[60:63], v[160:163], v[138:141]
	v_mfma_f32_16x16x32_bf16 v[134:137], v[52:55], v[168:171], v[134:137]
	v_mfma_f32_16x16x32_bf16 v[130:133], v[60:63], v[168:171], v[130:133]
	v_mfma_f32_16x16x32_bf16 v[110:113], v[52:55], v[176:179], v[110:113]
	v_mfma_f32_16x16x32_bf16 v[106:109], v[60:63], v[176:179], v[106:109]
	s_waitcnt lgkmcnt(0)
	v_mfma_f32_16x16x32_bf16 v[102:105], v[52:55], v[184:187], v[102:105]
	v_mfma_f32_16x16x32_bf16 v[98:101], v[60:63], v[184:187], v[98:101]
	s_setprio 0
	s_barrier
	s_or_b32 s55, s53, 0x80
	s_mov_b32 m0, s38
	ds_read_b128 v[188:191], v153 offset:49152
	ds_read_b128 v[192:195], v153 offset:50176
	ds_read_b128 v[196:199], v153 offset:51200
	ds_read_b128 v[200:203], v153 offset:52224
	buffer_load_dwordx4 v150, s[8:11], s55 offen lds
	s_mov_b32 m0, s39
	s_nop 0
	buffer_load_dwordx4 v152, s[8:11], s55 offen lds
	s_waitcnt vmcnt(10)
	s_barrier
	s_waitcnt lgkmcnt(0)
	s_setprio 1
	s_waitcnt lgkmcnt(3)
	v_mfma_f32_16x16x32_bf16 v[126:129], v[188:191], v[156:159], v[126:129]
	s_waitcnt lgkmcnt(1)
	v_mfma_f32_16x16x32_bf16 v[122:125], v[196:199], v[156:159], v[122:125]
	v_mfma_f32_16x16x32_bf16 v[118:121], v[188:191], v[164:167], v[118:121]
	v_mfma_f32_16x16x32_bf16 v[114:117], v[196:199], v[164:167], v[114:117]
	v_mfma_f32_16x16x32_bf16 v[92:95], v[188:191], v[172:175], v[92:95]
	v_mfma_f32_16x16x32_bf16 v[88:91], v[196:199], v[172:175], v[88:91]
	v_mfma_f32_16x16x32_bf16 v[84:87], v[188:191], v[180:183], v[84:87]
	v_mfma_f32_16x16x32_bf16 v[80:83], v[196:199], v[180:183], v[80:83]
	v_mfma_f32_16x16x32_bf16 v[126:129], v[192:195], v[160:163], v[126:129]
	s_waitcnt lgkmcnt(0)
	v_mfma_f32_16x16x32_bf16 v[122:125], v[200:203], v[160:163], v[122:125]
	v_mfma_f32_16x16x32_bf16 v[118:121], v[192:195], v[168:171], v[118:121]
	v_mfma_f32_16x16x32_bf16 v[114:117], v[200:203], v[168:171], v[114:117]
	v_mfma_f32_16x16x32_bf16 v[92:95], v[192:195], v[176:179], v[92:95]
	v_mfma_f32_16x16x32_bf16 v[88:91], v[200:203], v[176:179], v[88:91]
	v_mfma_f32_16x16x32_bf16 v[84:87], v[192:195], v[184:187], v[84:87]
	v_mfma_f32_16x16x32_bf16 v[80:83], v[200:203], v[184:187], v[80:83]
	s_setprio 0
	s_mov_b32 m0, s40
	s_barrier
	ds_read_b128 v[156:159], v154 offset:49152
	ds_read_b128 v[160:163], v154 offset:50176
	ds_read_b128 v[164:167], v154 offset:51200
	ds_read_b128 v[168:171], v154 offset:52224
	ds_read_b128 v[172:175], v154 offset:53248
	ds_read_b128 v[176:179], v154 offset:54272
	ds_read_b128 v[180:183], v154 offset:55296
	ds_read_b128 v[184:187], v154 offset:56320
	buffer_load_dwordx4 v149, s[72:75], s54 offen lds
	s_mov_b32 m0, s41
	s_nop 0
	buffer_load_dwordx4 v151, s[72:75], s54 offen lds
	s_barrier
	s_waitcnt lgkmcnt(0)
	s_setprio 1
	s_waitcnt lgkmcnt(7)
	v_mfma_f32_16x16x32_bf16 v[76:79], v[48:51], v[156:159], v[76:79]
	v_mfma_f32_16x16x32_bf16 v[72:75], v[56:59], v[156:159], v[72:75]
	s_waitcnt lgkmcnt(5)
	v_mfma_f32_16x16x32_bf16 v[68:71], v[48:51], v[164:167], v[68:71]
	v_mfma_f32_16x16x32_bf16 v[64:67], v[56:59], v[164:167], v[64:67]
	s_waitcnt lgkmcnt(3)
	v_mfma_f32_16x16x32_bf16 v[28:31], v[48:51], v[172:175], v[28:31]
	v_mfma_f32_16x16x32_bf16 v[24:27], v[56:59], v[172:175], v[24:27]
	s_waitcnt lgkmcnt(1)
	v_mfma_f32_16x16x32_bf16 v[16:19], v[48:51], v[180:183], v[16:19]
	v_mfma_f32_16x16x32_bf16 v[8:11], v[56:59], v[180:183], v[8:11]
	v_mfma_f32_16x16x32_bf16 v[76:79], v[52:55], v[160:163], v[76:79]
	v_mfma_f32_16x16x32_bf16 v[72:75], v[60:63], v[160:163], v[72:75]
	v_mfma_f32_16x16x32_bf16 v[68:71], v[52:55], v[168:171], v[68:71]
	v_mfma_f32_16x16x32_bf16 v[64:67], v[60:63], v[168:171], v[64:67]
	v_mfma_f32_16x16x32_bf16 v[28:31], v[52:55], v[176:179], v[28:31]
	v_mfma_f32_16x16x32_bf16 v[24:27], v[60:63], v[176:179], v[24:27]
	s_waitcnt lgkmcnt(0)
	v_mfma_f32_16x16x32_bf16 v[16:19], v[52:55], v[184:187], v[16:19]
	v_mfma_f32_16x16x32_bf16 v[8:11], v[60:63], v[184:187], v[8:11]
	s_setprio 0
	s_barrier
	s_add_i32 s53, s53, 0x80080
	s_mov_b32 m0, s42
	s_nop 0
	buffer_load_dwordx4 v150, s[8:11], s53 offen lds
	s_mov_b32 m0, s43
	s_nop 0
	buffer_load_dwordx4 v152, s[8:11], s53 offen lds
	s_waitcnt vmcnt(10)
	s_barrier
	s_setprio 1
	v_mfma_f32_16x16x32_bf16 v[32:35], v[188:191], v[156:159], v[32:35]
	v_mfma_f32_16x16x32_bf16 v[60:63], v[192:195], v[160:163], v[32:35]
	v_mfma_f32_16x16x32_bf16 v[32:35], v[196:199], v[156:159], v[36:39]
	v_mfma_f32_16x16x32_bf16 v[56:59], v[200:203], v[160:163], v[32:35]
	v_mfma_f32_16x16x32_bf16 v[32:35], v[188:191], v[164:167], v[40:43]
	v_mfma_f32_16x16x32_bf16 v[52:55], v[192:195], v[168:171], v[32:35]
	v_mfma_f32_16x16x32_bf16 v[32:35], v[196:199], v[164:167], v[44:47]
	v_mfma_f32_16x16x32_bf16 v[20:23], v[188:191], v[172:175], v[20:23]
	v_mfma_f32_16x16x32_bf16 v[12:15], v[196:199], v[172:175], v[12:15]
	v_mfma_f32_16x16x32_bf16 v[4:7], v[188:191], v[180:183], v[4:7]
	v_mfma_f32_16x16x32_bf16 v[0:3], v[196:199], v[180:183], v[0:3]
	v_mfma_f32_16x16x32_bf16 v[48:51], v[200:203], v[168:171], v[32:35]
	v_mfma_f32_16x16x32_bf16 v[20:23], v[192:195], v[176:179], v[20:23]
	v_mfma_f32_16x16x32_bf16 v[12:15], v[200:203], v[176:179], v[12:15]
	v_mfma_f32_16x16x32_bf16 v[4:7], v[192:195], v[184:187], v[4:7]
	v_mfma_f32_16x16x32_bf16 v[0:3], v[200:203], v[184:187], v[0:3]
	s_setprio 0
	s_add_i32 s52, s52, 2
	s_addk_i32 s50, 0x100
	s_addk_i32 s51, 0x100
	s_cmp_gt_u32 s52, 29
	s_barrier
	s_cbranch_scc0 .LBB0_1496
	s_getreg_b32 s10, hwreg(HW_REG_HW_ID, 0, 6)
	s_and_b32 s10, s10, 63
	s_lshl_b32 s10, s10, 2
	s_add_i32 s10, s10, 0
	s_add_i32 s10, s10, 0x20010
	v_mov_b32_e32 v32, s10
	ds_read_b32 v32, v32
	s_min_i32 s11, s2, 64
	s_ashr_i32 s11, s11, 3
	v_mbcnt_lo_u32_b32 v155, -1, 0
	v_mbcnt_hi_u32_b32 v155, -1, v155
	s_mov_b32 s51, s23
	s_waitcnt lgkmcnt(0)
	v_readfirstlane_b32 s10, v32
	v_lshrrev_b32_e32 v34, 1, v155
	v_and_b32_e32 v157, 24, v34
	v_lshl_or_b32 v146, s10, 6, v155
	s_lshl_b32 s10, s47, 8
	s_mul_hi_i32 s47, s11, 0xc000
	s_mul_i32 s11, s11, 0xc000
	s_add_u32 s50, s0, s11
	s_addc_u32 s47, s24, s47
	s_ashr_i32 s11, s10, 31
	s_lshl_b64 s[48:49], s[10:11], 2
	v_lshrrev_b32_e32 v32, 1, v146
	s_add_u32 s48, s50, s48
	v_and_b32_e32 v156, 0x60, v32
	s_addc_u32 s49, s47, s49
	v_lshlrev_b32_e32 v96, 2, v156
	v_lshl_add_u64 v[32:33], s[48:49], 0, v[96:97]
	v_lshlrev_b32_e32 v96, 2, v157
	v_lshl_add_u64 v[36:37], v[32:33], 0, v[96:97]
	v_ashrrev_i32_e32 v96, 2, v146
	s_lshl_b32 s48, s2, 8
	v_and_b32_e32 v146, 0xffffffc0, v96
	s_ashr_i32 s49, s48, 31
	v_ashrrev_i32_e32 v147, 31, v146
	v_lshl_add_u64 v[146:147], v[146:147], 0, s[48:49]
	v_and_or_b32 v146, v155, 15, v146
	v_lshlrev_b64 v[146:147], 12, v[146:147]
	v_lshl_add_u64 v[146:147], s[12:13], 0, v[146:147]
	v_lshl_add_u64 v[146:147], s[10:11], 1, v[146:147]
	v_lshlrev_b32_e32 v96, 1, v156
	v_lshl_add_u64 v[146:147], v[146:147], 0, v[96:97]
	v_lshlrev_b32_e32 v96, 1, v157
	v_lshl_add_u64 v[146:147], v[146:147], 0, v[96:97]
	global_load_dwordx4 v[40:43], v[36:37], off offset:16
	global_load_dwordx4 v[44:47], v[36:37], off
	global_load_dwordx4 v[32:35], v[36:37], off offset:528
	s_nop 0
	global_load_dwordx4 v[36:39], v[36:37], off offset:512
	s_mov_b32 s2, 0x10000
	global_load_dwordx4 v[156:159], v[146:147], off
	v_add_co_u32_e32 v176, vcc, s2, v146
	s_mov_b32 s2, 0x30000
	s_nop 0
	v_addc_co_u32_e32 v177, vcc, 0, v147, vcc
	s_mov_b32 s47, s20
	s_mov_b32 s50, s22
	s_waitcnt vmcnt(0)
	v_lshlrev_b32_e32 v160, 16, v156
	v_and_b32_e32 v161, 0xffff0000, v156
	v_lshlrev_b32_e32 v162, 16, v157
	v_and_b32_e32 v163, 0xffff0000, v157
	v_lshlrev_b32_e32 v164, 16, v158
	v_and_b32_e32 v165, 0xffff0000, v158
	v_lshlrev_b32_e32 v166, 16, v159
	v_and_b32_e32 v167, 0xffff0000, v159
	global_load_dwordx4 v[156:159], v[146:147], off offset:256
	v_pk_fma_f32 v[144:145], v[144:145], v[46:47], v[162:163]
	v_pk_fma_f32 v[142:143], v[142:143], v[44:45], v[160:161]
	v_pk_fma_f32 v[160:161], v[140:141], v[42:43], v[166:167]
	v_pk_fma_f32 v[140:141], v[138:139], v[40:41], v[164:165]
	v_cvt_pk_bf16_f32 v138, v142, v143
	v_cvt_pk_bf16_f32 v139, v144, v145
	v_cvt_pk_bf16_f32 v140, v140, v141
	v_cvt_pk_bf16_f32 v141, v160, v161
	global_store_dwordx4 v[146:147], v[138:141], off
	s_waitcnt vmcnt(1)
	v_lshlrev_b32_e32 v168, 16, v156
	v_and_b32_e32 v169, 0xffff0000, v156
	v_lshlrev_b32_e32 v170, 16, v157
	v_and_b32_e32 v171, 0xffff0000, v157
	v_lshlrev_b32_e32 v172, 16, v158
	v_and_b32_e32 v173, 0xffff0000, v158
	v_lshlrev_b32_e32 v174, 16, v159
	v_and_b32_e32 v175, 0xffff0000, v159
	global_load_dwordx4 v[156:159], v[176:177], off
	v_pk_fma_f32 v[128:129], v[128:129], v[38:39], v[170:171]
	v_pk_fma_f32 v[126:127], v[126:127], v[36:37], v[168:169]
	v_pk_fma_f32 v[138:139], v[124:125], v[34:35], v[174:175]
	v_pk_fma_f32 v[124:125], v[122:123], v[32:33], v[172:173]
	v_cvt_pk_bf16_f32 v122, v126, v127
	v_cvt_pk_bf16_f32 v123, v128, v129
	v_cvt_pk_bf16_f32 v124, v124, v125
	v_cvt_pk_bf16_f32 v125, v138, v139
	global_store_dwordx4 v[146:147], v[122:125], off offset:256
	s_waitcnt vmcnt(1)
	v_lshlrev_b32_e32 v178, 16, v156
	v_and_b32_e32 v179, 0xffff0000, v156
	v_lshlrev_b32_e32 v180, 16, v157
	v_and_b32_e32 v181, 0xffff0000, v157
	v_lshlrev_b32_e32 v182, 16, v158
	v_and_b32_e32 v183, 0xffff0000, v158
	v_lshlrev_b32_e32 v184, 16, v159
	v_and_b32_e32 v185, 0xffff0000, v159
	global_load_dwordx4 v[156:159], v[176:177], off offset:256
	v_pk_fma_f32 v[124:125], v[136:137], v[46:47], v[180:181]
	v_pk_fma_f32 v[122:123], v[134:135], v[44:45], v[178:179]
	v_pk_fma_f32 v[126:127], v[132:133], v[42:43], v[184:185]
	v_pk_fma_f32 v[128:129], v[130:131], v[40:41], v[182:183]
	v_cvt_pk_bf16_f32 v122, v122, v123
	v_cvt_pk_bf16_f32 v123, v124, v125
	v_cvt_pk_bf16_f32 v124, v128, v129
	v_cvt_pk_bf16_f32 v125, v126, v127
	global_store_dwordx4 v[176:177], v[122:125], off
	s_waitcnt vmcnt(1)
	v_lshlrev_b32_e32 v186, 16, v156
	v_and_b32_e32 v187, 0xffff0000, v156
	v_lshlrev_b32_e32 v156, 16, v157
	v_and_b32_e32 v157, 0xffff0000, v157
	v_lshlrev_b32_e32 v188, 16, v158
	v_and_b32_e32 v189, 0xffff0000, v158
	v_lshlrev_b32_e32 v158, 16, v159
	v_and_b32_e32 v159, 0xffff0000, v159
	v_pk_fma_f32 v[118:119], v[118:119], v[36:37], v[186:187]
	v_pk_fma_f32 v[120:121], v[120:121], v[38:39], v[156:157]
	v_pk_fma_f32 v[122:123], v[116:117], v[34:35], v[158:159]
	v_pk_fma_f32 v[116:117], v[114:115], v[32:33], v[188:189]
	v_cvt_pk_bf16_f32 v114, v118, v119
	v_add_co_u32_e32 v118, vcc, s75, v146
	v_cvt_pk_bf16_f32 v115, v120, v121
	v_cvt_pk_bf16_f32 v116, v116, v117
	v_cvt_pk_bf16_f32 v117, v122, v123
	v_addc_co_u32_e32 v119, vcc, 0, v147, vcc
	global_store_dwordx4 v[176:177], v[114:117], off offset:256
	global_load_dwordx4 v[114:117], v[118:119], off
	v_add_co_u32_e32 v136, vcc, s2, v146
	s_mov_b32 s2, 0x80000
	s_nop 0
	v_addc_co_u32_e32 v137, vcc, 0, v147, vcc
	s_waitcnt vmcnt(0)
	v_lshlrev_b32_e32 v120, 16, v114
	v_and_b32_e32 v121, 0xffff0000, v114
	v_lshlrev_b32_e32 v122, 16, v115
	v_and_b32_e32 v123, 0xffff0000, v115
	v_lshlrev_b32_e32 v124, 16, v116
	v_and_b32_e32 v125, 0xffff0000, v116
	v_lshlrev_b32_e32 v126, 16, v117
	v_and_b32_e32 v127, 0xffff0000, v117
	global_load_dwordx4 v[114:117], v[118:119], off offset:256
	v_pk_fma_f32 v[112:113], v[112:113], v[46:47], v[122:123]
	v_pk_fma_f32 v[110:111], v[110:111], v[44:45], v[120:121]
	v_pk_fma_f32 v[120:121], v[108:109], v[42:43], v[126:127]
	v_pk_fma_f32 v[108:109], v[106:107], v[40:41], v[124:125]
	v_cvt_pk_bf16_f32 v106, v110, v111
	v_cvt_pk_bf16_f32 v107, v112, v113
	v_cvt_pk_bf16_f32 v108, v108, v109
	v_cvt_pk_bf16_f32 v109, v120, v121
	global_store_dwordx4 v[118:119], v[106:109], off
	s_waitcnt vmcnt(1)
	v_lshlrev_b32_e32 v128, 16, v114
	v_and_b32_e32 v129, 0xffff0000, v114
	v_lshlrev_b32_e32 v130, 16, v115
	v_and_b32_e32 v131, 0xffff0000, v115
	v_lshlrev_b32_e32 v132, 16, v116
	v_and_b32_e32 v133, 0xffff0000, v116
	v_lshlrev_b32_e32 v134, 16, v117
	v_and_b32_e32 v135, 0xffff0000, v117
	global_load_dwordx4 v[114:117], v[136:137], off
	v_pk_fma_f32 v[94:95], v[94:95], v[38:39], v[130:131]
	v_pk_fma_f32 v[92:93], v[92:93], v[36:37], v[128:129]
	v_pk_fma_f32 v[106:107], v[90:91], v[34:35], v[134:135]
	v_pk_fma_f32 v[90:91], v[88:89], v[32:33], v[132:133]
	v_cvt_pk_bf16_f32 v88, v92, v93
	v_cvt_pk_bf16_f32 v89, v94, v95
	v_cvt_pk_bf16_f32 v90, v90, v91
	v_cvt_pk_bf16_f32 v91, v106, v107
	global_store_dwordx4 v[118:119], v[88:91], off offset:256
	s_waitcnt vmcnt(1)
	v_lshlrev_b32_e32 v138, 16, v114
	v_and_b32_e32 v139, 0xffff0000, v114
	v_lshlrev_b32_e32 v140, 16, v115
	v_and_b32_e32 v141, 0xffff0000, v115
	v_lshlrev_b32_e32 v142, 16, v116
	v_and_b32_e32 v143, 0xffff0000, v116
	v_lshlrev_b32_e32 v144, 16, v117
	v_and_b32_e32 v145, 0xffff0000, v117
	global_load_dwordx4 v[114:117], v[136:137], off offset:256
	v_pk_fma_f32 v[90:91], v[104:105], v[46:47], v[140:141]
	v_pk_fma_f32 v[88:89], v[102:103], v[44:45], v[138:139]
	v_pk_fma_f32 v[92:93], v[100:101], v[42:43], v[144:145]
	v_pk_fma_f32 v[94:95], v[98:99], v[40:41], v[142:143]
	v_cvt_pk_bf16_f32 v88, v88, v89
	v_cvt_pk_bf16_f32 v89, v90, v91
	v_cvt_pk_bf16_f32 v90, v94, v95
	v_cvt_pk_bf16_f32 v91, v92, v93
	global_store_dwordx4 v[136:137], v[88:91], off
	s_waitcnt vmcnt(1)
	v_lshlrev_b32_e32 v156, 16, v114
	v_and_b32_e32 v157, 0xffff0000, v114
	v_lshlrev_b32_e32 v114, 16, v115
	v_and_b32_e32 v115, 0xffff0000, v115
	v_lshlrev_b32_e32 v158, 16, v116
	v_and_b32_e32 v159, 0xffff0000, v116
	v_lshlrev_b32_e32 v116, 16, v117
	v_and_b32_e32 v117, 0xffff0000, v117
	v_pk_fma_f32 v[86:87], v[86:87], v[38:39], v[114:115]
	v_pk_fma_f32 v[84:85], v[84:85], v[36:37], v[156:157]
	v_pk_fma_f32 v[88:89], v[82:83], v[34:35], v[116:117]
	v_pk_fma_f32 v[82:83], v[80:81], v[32:33], v[158:159]
	v_cvt_pk_bf16_f32 v80, v84, v85
	v_cvt_pk_bf16_f32 v81, v86, v87
	v_cvt_pk_bf16_f32 v82, v82, v83
	v_cvt_pk_bf16_f32 v83, v88, v89
	global_store_dwordx4 v[136:137], v[80:83], off offset:256
	s_nop 1
	v_add_co_u32_e32 v80, vcc, s2, v146
	s_mov_b32 s2, 0x90000
	s_nop 0
	v_addc_co_u32_e32 v81, vcc, 0, v147, vcc
	global_load_dwordx4 v[82:85], v[80:81], off
	v_add_co_u32_e32 v104, vcc, s2, v146
	s_mov_b32 s2, 0xa0000
	s_nop 0
	v_addc_co_u32_e32 v105, vcc, 0, v147, vcc
	s_waitcnt vmcnt(0)
	v_lshlrev_b32_e32 v86, 16, v82
	v_and_b32_e32 v87, 0xffff0000, v82
	v_lshlrev_b32_e32 v88, 16, v83
	v_and_b32_e32 v89, 0xffff0000, v83
	v_lshlrev_b32_e32 v90, 16, v84
	v_and_b32_e32 v91, 0xffff0000, v84
	v_lshlrev_b32_e32 v92, 16, v85
	v_and_b32_e32 v93, 0xffff0000, v85
	global_load_dwordx4 v[82:85], v[80:81], off offset:256
	v_pk_fma_f32 v[78:79], v[78:79], v[46:47], v[88:89]
	v_pk_fma_f32 v[76:77], v[76:77], v[44:45], v[86:87]
	v_pk_fma_f32 v[86:87], v[74:75], v[42:43], v[92:93]
	v_pk_fma_f32 v[74:75], v[72:73], v[40:41], v[90:91]
	v_cvt_pk_bf16_f32 v72, v76, v77
	v_cvt_pk_bf16_f32 v73, v78, v79
	v_cvt_pk_bf16_f32 v74, v74, v75
	v_cvt_pk_bf16_f32 v75, v86, v87
	global_store_dwordx4 v[80:81], v[72:75], off
	s_waitcnt vmcnt(1)
	v_lshlrev_b32_e32 v94, 16, v82
	v_and_b32_e32 v95, 0xffff0000, v82
	v_lshlrev_b32_e32 v98, 16, v83
	v_and_b32_e32 v99, 0xffff0000, v83
	v_lshlrev_b32_e32 v100, 16, v84
	v_and_b32_e32 v101, 0xffff0000, v84
	v_lshlrev_b32_e32 v102, 16, v85
	v_and_b32_e32 v103, 0xffff0000, v85
	global_load_dwordx4 v[82:85], v[104:105], off
	v_pk_fma_f32 v[62:63], v[62:63], v[38:39], v[98:99]
	v_pk_fma_f32 v[60:61], v[60:61], v[36:37], v[94:95]
	v_pk_fma_f32 v[72:73], v[58:59], v[34:35], v[102:103]
	v_pk_fma_f32 v[58:59], v[56:57], v[32:33], v[100:101]
	v_cvt_pk_bf16_f32 v56, v60, v61
	v_cvt_pk_bf16_f32 v57, v62, v63
	v_cvt_pk_bf16_f32 v58, v58, v59
	v_cvt_pk_bf16_f32 v59, v72, v73
	global_store_dwordx4 v[80:81], v[56:59], off offset:256
	s_waitcnt vmcnt(1)
	v_lshlrev_b32_e32 v106, 16, v82
	v_and_b32_e32 v107, 0xffff0000, v82
	v_lshlrev_b32_e32 v108, 16, v83
	v_and_b32_e32 v109, 0xffff0000, v83
	v_lshlrev_b32_e32 v110, 16, v84
	v_and_b32_e32 v111, 0xffff0000, v84
	v_lshlrev_b32_e32 v112, 16, v85
	v_and_b32_e32 v113, 0xffff0000, v85
	global_load_dwordx4 v[82:85], v[104:105], off offset:256
	v_pk_fma_f32 v[58:59], v[70:71], v[46:47], v[108:109]
	v_pk_fma_f32 v[56:57], v[68:69], v[44:45], v[106:107]
	v_pk_fma_f32 v[60:61], v[66:67], v[42:43], v[112:113]
	v_pk_fma_f32 v[62:63], v[64:65], v[40:41], v[110:111]
	v_cvt_pk_bf16_f32 v56, v56, v57
	v_cvt_pk_bf16_f32 v57, v58, v59
	v_cvt_pk_bf16_f32 v58, v62, v63
	v_cvt_pk_bf16_f32 v59, v60, v61
	global_store_dwordx4 v[104:105], v[56:59], off
	s_waitcnt vmcnt(1)
	v_lshlrev_b32_e32 v114, 16, v82
	v_and_b32_e32 v115, 0xffff0000, v82
	v_lshlrev_b32_e32 v82, 16, v83
	v_and_b32_e32 v83, 0xffff0000, v83
	v_lshlrev_b32_e32 v116, 16, v84
	v_and_b32_e32 v117, 0xffff0000, v84
	v_lshlrev_b32_e32 v84, 16, v85
	v_and_b32_e32 v85, 0xffff0000, v85
	v_pk_fma_f32 v[52:53], v[52:53], v[36:37], v[114:115]
	v_pk_fma_f32 v[54:55], v[54:55], v[38:39], v[82:83]
	v_pk_fma_f32 v[56:57], v[50:51], v[34:35], v[84:85]
	v_pk_fma_f32 v[50:51], v[48:49], v[32:33], v[116:117]
	v_cvt_pk_bf16_f32 v48, v52, v53
	v_add_co_u32_e32 v52, vcc, s2, v146
	v_cvt_pk_bf16_f32 v49, v54, v55
	v_cvt_pk_bf16_f32 v50, v50, v51
	v_cvt_pk_bf16_f32 v51, v56, v57
	v_addc_co_u32_e32 v53, vcc, 0, v147, vcc
	global_store_dwordx4 v[104:105], v[48:51], off offset:256
	global_load_dwordx4 v[48:51], v[52:53], off
	s_mov_b32 s2, 0xb0000
	v_add_co_u32_e32 v62, vcc, s2, v146
	s_mov_b32 s2, s21
	s_nop 0
	v_addc_co_u32_e32 v63, vcc, 0, v147, vcc
	s_and_b64 vcc, exec, s[4:5]
	s_waitcnt vmcnt(0)
	v_lshlrev_b32_e32 v56, 16, v48
	v_and_b32_e32 v57, 0xffff0000, v48
	v_lshlrev_b32_e32 v60, 16, v49
	v_and_b32_e32 v61, 0xffff0000, v49
	v_lshlrev_b32_e32 v54, 16, v50
	v_and_b32_e32 v55, 0xffff0000, v50
	v_lshlrev_b32_e32 v58, 16, v51
	v_and_b32_e32 v59, 0xffff0000, v51
	global_load_dwordx4 v[48:51], v[52:53], off offset:256
	v_pk_fma_f32 v[30:31], v[30:31], v[46:47], v[60:61]
	v_pk_fma_f32 v[28:29], v[28:29], v[44:45], v[56:57]
	v_pk_fma_f32 v[56:57], v[26:27], v[42:43], v[58:59]
	v_pk_fma_f32 v[26:27], v[24:25], v[40:41], v[54:55]
	v_cvt_pk_bf16_f32 v24, v28, v29
	v_cvt_pk_bf16_f32 v25, v30, v31
	v_cvt_pk_bf16_f32 v26, v26, v27
	v_cvt_pk_bf16_f32 v27, v56, v57
	global_store_dwordx4 v[52:53], v[24:27], off
	s_waitcnt vmcnt(1)
	v_lshlrev_b32_e32 v66, 16, v48
	v_and_b32_e32 v67, 0xffff0000, v48
	v_lshlrev_b32_e32 v70, 16, v49
	v_and_b32_e32 v71, 0xffff0000, v49
	v_lshlrev_b32_e32 v64, 16, v50
	v_and_b32_e32 v65, 0xffff0000, v50
	v_lshlrev_b32_e32 v68, 16, v51
	v_and_b32_e32 v69, 0xffff0000, v51
	global_load_dwordx4 v[48:51], v[62:63], off
	v_pk_fma_f32 v[22:23], v[22:23], v[38:39], v[70:71]
	v_pk_fma_f32 v[20:21], v[20:21], v[36:37], v[66:67]
	v_pk_fma_f32 v[24:25], v[14:15], v[34:35], v[68:69]
	v_pk_fma_f32 v[14:15], v[12:13], v[32:33], v[64:65]
	v_cvt_pk_bf16_f32 v12, v20, v21
	v_cvt_pk_bf16_f32 v13, v22, v23
	v_cvt_pk_bf16_f32 v14, v14, v15
	v_cvt_pk_bf16_f32 v15, v24, v25
	global_store_dwordx4 v[52:53], v[12:15], off offset:256
	s_waitcnt vmcnt(1)
	v_lshlrev_b32_e32 v74, 16, v48
	v_and_b32_e32 v75, 0xffff0000, v48
	v_lshlrev_b32_e32 v78, 16, v49
	v_and_b32_e32 v79, 0xffff0000, v49
	v_lshlrev_b32_e32 v72, 16, v50
	v_and_b32_e32 v73, 0xffff0000, v50
	v_lshlrev_b32_e32 v76, 16, v51
	v_and_b32_e32 v77, 0xffff0000, v51
	global_load_dwordx4 v[48:51], v[62:63], off offset:256
	v_pk_fma_f32 v[12:13], v[18:19], v[46:47], v[78:79]
	v_pk_fma_f32 v[14:15], v[16:17], v[44:45], v[74:75]
	v_pk_fma_f32 v[16:17], v[10:11], v[42:43], v[76:77]
	v_pk_fma_f32 v[10:11], v[8:9], v[40:41], v[72:73]
	v_cvt_pk_bf16_f32 v8, v14, v15
	v_cvt_pk_bf16_f32 v9, v12, v13
	v_cvt_pk_bf16_f32 v10, v10, v11
	v_cvt_pk_bf16_f32 v11, v16, v17
	global_store_dwordx4 v[62:63], v[8:11], off
	s_waitcnt vmcnt(1)
	v_lshlrev_b32_e32 v80, 16, v48
	v_and_b32_e32 v81, 0xffff0000, v48
	v_lshlrev_b32_e32 v48, 16, v49
	v_and_b32_e32 v49, 0xffff0000, v49
	v_lshlrev_b32_e32 v82, 16, v50
	v_and_b32_e32 v83, 0xffff0000, v50
	v_lshlrev_b32_e32 v50, 16, v51
	v_and_b32_e32 v51, 0xffff0000, v51
	v_pk_fma_f32 v[6:7], v[6:7], v[38:39], v[48:49]
	v_pk_fma_f32 v[4:5], v[4:5], v[36:37], v[80:81]
	v_pk_fma_f32 v[8:9], v[2:3], v[34:35], v[50:51]
	v_pk_fma_f32 v[2:3], v[0:1], v[32:33], v[82:83]
	v_cvt_pk_bf16_f32 v0, v4, v5
	v_cvt_pk_bf16_f32 v1, v6, v7
	v_cvt_pk_bf16_f32 v2, v2, v3
	v_cvt_pk_bf16_f32 v3, v8, v9
	global_store_dwordx4 v[62:63], v[0:3], off offset:256
	s_cbranch_vccz .LBB0_1490
	s_branch .LBB0_1499

.LBB0_1514:
	ds_read_b128 v[64:67], v154
	ds_read_b128 v[68:71], v154 offset:1024
	ds_read_b128 v[72:75], v154 offset:2048
	ds_read_b128 v[76:79], v154 offset:3072
	s_add_i32 s10, s49, 0xfff80080
	s_cmp_eq_u32 s51, 28
	s_cselect_b32 s54, s47, s10
	s_cselect_b32 s52, s48, s50
	s_or_b32 s53, s54, 0x80
	s_mov_b32 m0, s41
	ds_read_b128 v[146:149], v155
	ds_read_b128 v[156:159], v155 offset:1024
	ds_read_b128 v[160:163], v155 offset:2048
	ds_read_b128 v[164:167], v155 offset:3072
	ds_read_b128 v[168:171], v155 offset:4096
	ds_read_b128 v[172:175], v155 offset:5120
	ds_read_b128 v[176:179], v155 offset:6144
	ds_read_b128 v[180:183], v155 offset:7168
	buffer_load_dwordx4 v150, s[72:75], s49 offen lds
	s_mov_b32 m0, s42
	s_nop 0
	buffer_load_dwordx4 v152, s[72:75], s49 offen lds
	s_waitcnt lgkmcnt(8)
	s_waitcnt vmcnt(10)
	s_barrier
	s_waitcnt lgkmcnt(0)
	s_setprio 1
	s_waitcnt lgkmcnt(7)
	v_mfma_f32_16x16x32_bf16 v[142:145], v[64:67], v[146:149], v[142:145]
	v_mfma_f32_16x16x32_bf16 v[138:141], v[72:75], v[146:149], v[138:141]
	s_waitcnt lgkmcnt(5)
	v_mfma_f32_16x16x32_bf16 v[134:137], v[64:67], v[160:163], v[134:137]
	v_mfma_f32_16x16x32_bf16 v[130:133], v[72:75], v[160:163], v[130:133]
	s_waitcnt lgkmcnt(3)
	v_mfma_f32_16x16x32_bf16 v[110:113], v[64:67], v[168:171], v[110:113]
	v_mfma_f32_16x16x32_bf16 v[106:109], v[72:75], v[168:171], v[106:109]
	s_waitcnt lgkmcnt(1)
	v_mfma_f32_16x16x32_bf16 v[102:105], v[64:67], v[176:179], v[102:105]
	v_mfma_f32_16x16x32_bf16 v[98:101], v[72:75], v[176:179], v[98:101]
	v_mfma_f32_16x16x32_bf16 v[142:145], v[68:71], v[156:159], v[142:145]
	v_mfma_f32_16x16x32_bf16 v[138:141], v[76:79], v[156:159], v[138:141]
	v_mfma_f32_16x16x32_bf16 v[134:137], v[68:71], v[164:167], v[134:137]
	v_mfma_f32_16x16x32_bf16 v[130:133], v[76:79], v[164:167], v[130:133]
	v_mfma_f32_16x16x32_bf16 v[110:113], v[68:71], v[172:175], v[110:113]
	v_mfma_f32_16x16x32_bf16 v[106:109], v[76:79], v[172:175], v[106:109]
	s_waitcnt lgkmcnt(0)
	v_mfma_f32_16x16x32_bf16 v[102:105], v[68:71], v[180:183], v[102:105]
	v_mfma_f32_16x16x32_bf16 v[98:101], v[76:79], v[180:183], v[98:101]
	s_setprio 0
	s_barrier
	s_mov_b32 s10, s74
	s_mov_b32 s11, s75
	s_mov_b32 m0, s26
	ds_read_b128 v[184:187], v154 offset:16384
	ds_read_b128 v[188:191], v154 offset:17408
	ds_read_b128 v[192:195], v154 offset:18432
	ds_read_b128 v[196:199], v154 offset:19456
	buffer_load_dwordx4 v151, s[8:11], s52 offen lds
	s_mov_b32 m0, s27
	s_nop 0
	buffer_load_dwordx4 v153, s[8:11], s52 offen lds
	s_waitcnt vmcnt(10)
	s_barrier
	s_waitcnt lgkmcnt(0)
	s_setprio 1
	s_waitcnt lgkmcnt(3)
	v_mfma_f32_16x16x32_bf16 v[126:129], v[184:187], v[146:149], v[126:129]
	s_waitcnt lgkmcnt(1)
	v_mfma_f32_16x16x32_bf16 v[122:125], v[192:195], v[146:149], v[122:125]
	v_mfma_f32_16x16x32_bf16 v[118:121], v[184:187], v[160:163], v[118:121]
	v_mfma_f32_16x16x32_bf16 v[114:117], v[192:195], v[160:163], v[114:117]
	v_mfma_f32_16x16x32_bf16 v[92:95], v[184:187], v[168:171], v[92:95]
	v_mfma_f32_16x16x32_bf16 v[88:91], v[192:195], v[168:171], v[88:91]
	v_mfma_f32_16x16x32_bf16 v[84:87], v[184:187], v[176:179], v[84:87]
	v_mfma_f32_16x16x32_bf16 v[80:83], v[192:195], v[176:179], v[80:83]
	v_mfma_f32_16x16x32_bf16 v[126:129], v[188:191], v[156:159], v[126:129]
	s_waitcnt lgkmcnt(0)
	v_mfma_f32_16x16x32_bf16 v[122:125], v[196:199], v[156:159], v[122:125]
	v_mfma_f32_16x16x32_bf16 v[118:121], v[188:191], v[164:167], v[118:121]
	v_mfma_f32_16x16x32_bf16 v[114:117], v[196:199], v[164:167], v[114:117]
	v_mfma_f32_16x16x32_bf16 v[92:95], v[188:191], v[172:175], v[92:95]
	v_mfma_f32_16x16x32_bf16 v[88:91], v[196:199], v[172:175], v[88:91]
	v_mfma_f32_16x16x32_bf16 v[84:87], v[188:191], v[180:183], v[84:87]
	v_mfma_f32_16x16x32_bf16 v[80:83], v[196:199], v[180:183], v[80:83]
	s_setprio 0
	s_mov_b32 m0, s23
	s_barrier
	ds_read_b128 v[146:149], v155 offset:16384
	ds_read_b128 v[156:159], v155 offset:17408
	ds_read_b128 v[160:163], v155 offset:18432
	ds_read_b128 v[164:167], v155 offset:19456
	ds_read_b128 v[168:171], v155 offset:20480
	ds_read_b128 v[172:175], v155 offset:21504
	ds_read_b128 v[176:179], v155 offset:22528
	ds_read_b128 v[180:183], v155 offset:23552
	buffer_load_dwordx4 v150, s[72:75], s54 offen lds
	s_mov_b32 m0, s28
	s_nop 0
	buffer_load_dwordx4 v152, s[72:75], s54 offen lds
	s_barrier
	s_waitcnt lgkmcnt(0)
	s_setprio 1
	s_waitcnt lgkmcnt(7)
	v_mfma_f32_16x16x32_bf16 v[60:63], v[64:67], v[146:149], v[60:63]
	v_mfma_f32_16x16x32_bf16 v[56:59], v[72:75], v[146:149], v[56:59]
	s_waitcnt lgkmcnt(5)
	v_mfma_f32_16x16x32_bf16 v[52:55], v[64:67], v[160:163], v[52:55]
	v_mfma_f32_16x16x32_bf16 v[48:51], v[72:75], v[160:163], v[48:51]
	s_waitcnt lgkmcnt(3)
	v_mfma_f32_16x16x32_bf16 v[28:31], v[64:67], v[168:171], v[28:31]
	v_mfma_f32_16x16x32_bf16 v[24:27], v[72:75], v[168:171], v[24:27]
	s_waitcnt lgkmcnt(1)
	v_mfma_f32_16x16x32_bf16 v[20:23], v[64:67], v[176:179], v[20:23]
	v_mfma_f32_16x16x32_bf16 v[16:19], v[72:75], v[176:179], v[16:19]
	v_mfma_f32_16x16x32_bf16 v[60:63], v[68:71], v[156:159], v[60:63]
	v_mfma_f32_16x16x32_bf16 v[56:59], v[76:79], v[156:159], v[56:59]
	v_mfma_f32_16x16x32_bf16 v[52:55], v[68:71], v[164:167], v[52:55]
	v_mfma_f32_16x16x32_bf16 v[48:51], v[76:79], v[164:167], v[48:51]
	v_mfma_f32_16x16x32_bf16 v[28:31], v[68:71], v[172:175], v[28:31]
	v_mfma_f32_16x16x32_bf16 v[24:27], v[76:79], v[172:175], v[24:27]
	s_waitcnt lgkmcnt(0)
	v_mfma_f32_16x16x32_bf16 v[20:23], v[68:71], v[180:183], v[20:23]
	v_mfma_f32_16x16x32_bf16 v[16:19], v[76:79], v[180:183], v[16:19]
	s_setprio 0
	s_barrier
	s_add_i32 s55, s52, 0x80000
	s_mov_b32 m0, s29
	s_nop 0
	buffer_load_dwordx4 v151, s[8:11], s55 offen lds
	s_mov_b32 m0, s30
	s_nop 0
	buffer_load_dwordx4 v153, s[8:11], s55 offen lds
	s_waitcnt vmcnt(10)
	s_barrier
	s_setprio 1
	v_mfma_f32_16x16x32_bf16 v[44:47], v[184:187], v[146:149], v[44:47]
	v_mfma_f32_16x16x32_bf16 v[40:43], v[192:195], v[146:149], v[40:43]
	v_mfma_f32_16x16x32_bf16 v[36:39], v[184:187], v[160:163], v[36:39]
	v_mfma_f32_16x16x32_bf16 v[32:35], v[192:195], v[160:163], v[32:35]
	v_mfma_f32_16x16x32_bf16 v[12:15], v[184:187], v[168:171], v[12:15]
	v_mfma_f32_16x16x32_bf16 v[8:11], v[192:195], v[168:171], v[8:11]
	v_mfma_f32_16x16x32_bf16 v[4:7], v[184:187], v[176:179], v[4:7]
	v_mfma_f32_16x16x32_bf16 v[0:3], v[192:195], v[176:179], v[0:3]
	v_mfma_f32_16x16x32_bf16 v[44:47], v[188:191], v[156:159], v[44:47]
	v_mfma_f32_16x16x32_bf16 v[40:43], v[196:199], v[156:159], v[40:43]
	v_mfma_f32_16x16x32_bf16 v[36:39], v[188:191], v[164:167], v[36:39]
	v_mfma_f32_16x16x32_bf16 v[32:35], v[196:199], v[164:167], v[32:35]
	v_mfma_f32_16x16x32_bf16 v[12:15], v[188:191], v[172:175], v[12:15]
	v_mfma_f32_16x16x32_bf16 v[8:11], v[196:199], v[172:175], v[8:11]
	v_mfma_f32_16x16x32_bf16 v[4:7], v[188:191], v[180:183], v[4:7]
	v_mfma_f32_16x16x32_bf16 v[0:3], v[196:199], v[180:183], v[0:3]
	s_setprio 0
	s_barrier
	ds_read_b128 v[64:67], v154 offset:32768
	ds_read_b128 v[68:71], v154 offset:33792
	ds_read_b128 v[72:75], v154 offset:34816
	ds_read_b128 v[76:79], v154 offset:35840
	s_add_i32 s54, s54, 0x80000
	s_mov_b32 m0, s31
	ds_read_b128 v[146:149], v155 offset:32768
	ds_read_b128 v[156:159], v155 offset:33792
	ds_read_b128 v[160:163], v155 offset:34816
	ds_read_b128 v[164:167], v155 offset:35840
	ds_read_b128 v[168:171], v155 offset:36864
	ds_read_b128 v[172:175], v155 offset:37888
	ds_read_b128 v[176:179], v155 offset:38912
	ds_read_b128 v[180:183], v155 offset:39936
	buffer_load_dwordx4 v150, s[72:75], s54 offen lds
	s_mov_b32 m0, s34
	s_nop 0
	buffer_load_dwordx4 v152, s[72:75], s54 offen lds
	s_waitcnt lgkmcnt(8)
	s_waitcnt vmcnt(10)
	s_barrier
	s_waitcnt lgkmcnt(0)
	s_setprio 1
	s_waitcnt lgkmcnt(7)
	v_mfma_f32_16x16x32_bf16 v[142:145], v[64:67], v[146:149], v[142:145]
	v_mfma_f32_16x16x32_bf16 v[138:141], v[72:75], v[146:149], v[138:141]
	s_waitcnt lgkmcnt(5)
	v_mfma_f32_16x16x32_bf16 v[134:137], v[64:67], v[160:163], v[134:137]
	v_mfma_f32_16x16x32_bf16 v[130:133], v[72:75], v[160:163], v[130:133]
	s_waitcnt lgkmcnt(3)
	v_mfma_f32_16x16x32_bf16 v[110:113], v[64:67], v[168:171], v[110:113]
	v_mfma_f32_16x16x32_bf16 v[106:109], v[72:75], v[168:171], v[106:109]
	s_waitcnt lgkmcnt(1)
	v_mfma_f32_16x16x32_bf16 v[102:105], v[64:67], v[176:179], v[102:105]
	v_mfma_f32_16x16x32_bf16 v[98:101], v[72:75], v[176:179], v[98:101]
	v_mfma_f32_16x16x32_bf16 v[142:145], v[68:71], v[156:159], v[142:145]
	v_mfma_f32_16x16x32_bf16 v[138:141], v[76:79], v[156:159], v[138:141]
	v_mfma_f32_16x16x32_bf16 v[134:137], v[68:71], v[164:167], v[134:137]
	v_mfma_f32_16x16x32_bf16 v[130:133], v[76:79], v[164:167], v[130:133]
	v_mfma_f32_16x16x32_bf16 v[110:113], v[68:71], v[172:175], v[110:113]
	v_mfma_f32_16x16x32_bf16 v[106:109], v[76:79], v[172:175], v[106:109]
	s_waitcnt lgkmcnt(0)
	v_mfma_f32_16x16x32_bf16 v[102:105], v[68:71], v[180:183], v[102:105]
	v_mfma_f32_16x16x32_bf16 v[98:101], v[76:79], v[180:183], v[98:101]
	s_setprio 0
	s_barrier
	s_or_b32 s54, s52, 0x80
	s_mov_b32 m0, s35
	ds_read_b128 v[184:187], v154 offset:49152
	ds_read_b128 v[188:191], v154 offset:50176
	ds_read_b128 v[192:195], v154 offset:51200
	ds_read_b128 v[196:199], v154 offset:52224
	buffer_load_dwordx4 v151, s[8:11], s54 offen lds
	s_mov_b32 m0, s36
	s_nop 0
	buffer_load_dwordx4 v153, s[8:11], s54 offen lds
	s_waitcnt vmcnt(10)
	s_barrier
	s_waitcnt lgkmcnt(0)
	s_setprio 1
	s_waitcnt lgkmcnt(3)
	v_mfma_f32_16x16x32_bf16 v[126:129], v[184:187], v[146:149], v[126:129]
	s_waitcnt lgkmcnt(1)
	v_mfma_f32_16x16x32_bf16 v[122:125], v[192:195], v[146:149], v[122:125]
	v_mfma_f32_16x16x32_bf16 v[118:121], v[184:187], v[160:163], v[118:121]
	v_mfma_f32_16x16x32_bf16 v[114:117], v[192:195], v[160:163], v[114:117]
	v_mfma_f32_16x16x32_bf16 v[92:95], v[184:187], v[168:171], v[92:95]
	v_mfma_f32_16x16x32_bf16 v[88:91], v[192:195], v[168:171], v[88:91]
	v_mfma_f32_16x16x32_bf16 v[84:87], v[184:187], v[176:179], v[84:87]
	v_mfma_f32_16x16x32_bf16 v[80:83], v[192:195], v[176:179], v[80:83]
	v_mfma_f32_16x16x32_bf16 v[126:129], v[188:191], v[156:159], v[126:129]
	s_waitcnt lgkmcnt(0)
	v_mfma_f32_16x16x32_bf16 v[122:125], v[196:199], v[156:159], v[122:125]
	v_mfma_f32_16x16x32_bf16 v[118:121], v[188:191], v[164:167], v[118:121]
	v_mfma_f32_16x16x32_bf16 v[114:117], v[196:199], v[164:167], v[114:117]
	v_mfma_f32_16x16x32_bf16 v[92:95], v[188:191], v[172:175], v[92:95]
	v_mfma_f32_16x16x32_bf16 v[88:91], v[196:199], v[172:175], v[88:91]
	v_mfma_f32_16x16x32_bf16 v[84:87], v[188:191], v[180:183], v[84:87]
	v_mfma_f32_16x16x32_bf16 v[80:83], v[196:199], v[180:183], v[80:83]
	s_setprio 0
	s_mov_b32 m0, s37
	s_barrier
	ds_read_b128 v[146:149], v155 offset:49152
	ds_read_b128 v[156:159], v155 offset:50176
	ds_read_b128 v[160:163], v155 offset:51200
	ds_read_b128 v[164:167], v155 offset:52224
	ds_read_b128 v[168:171], v155 offset:53248
	ds_read_b128 v[172:175], v155 offset:54272
	ds_read_b128 v[176:179], v155 offset:55296
	ds_read_b128 v[180:183], v155 offset:56320
	buffer_load_dwordx4 v150, s[72:75], s53 offen lds
	s_mov_b32 m0, s38
	s_nop 0
	buffer_load_dwordx4 v152, s[72:75], s53 offen lds
	s_barrier
	s_waitcnt lgkmcnt(0)
	s_setprio 1
	s_waitcnt lgkmcnt(7)
	v_mfma_f32_16x16x32_bf16 v[60:63], v[64:67], v[146:149], v[60:63]
	v_mfma_f32_16x16x32_bf16 v[56:59], v[72:75], v[146:149], v[56:59]
	s_waitcnt lgkmcnt(5)
	v_mfma_f32_16x16x32_bf16 v[52:55], v[64:67], v[160:163], v[52:55]
	v_mfma_f32_16x16x32_bf16 v[48:51], v[72:75], v[160:163], v[48:51]
	s_waitcnt lgkmcnt(3)
	v_mfma_f32_16x16x32_bf16 v[28:31], v[64:67], v[168:171], v[28:31]
	v_mfma_f32_16x16x32_bf16 v[24:27], v[72:75], v[168:171], v[24:27]
	s_waitcnt lgkmcnt(1)
	v_mfma_f32_16x16x32_bf16 v[20:23], v[64:67], v[176:179], v[20:23]
	v_mfma_f32_16x16x32_bf16 v[16:19], v[72:75], v[176:179], v[16:19]
	v_mfma_f32_16x16x32_bf16 v[60:63], v[68:71], v[156:159], v[60:63]
	v_mfma_f32_16x16x32_bf16 v[56:59], v[76:79], v[156:159], v[56:59]
	v_mfma_f32_16x16x32_bf16 v[52:55], v[68:71], v[164:167], v[52:55]
	v_mfma_f32_16x16x32_bf16 v[48:51], v[76:79], v[164:167], v[48:51]
	v_mfma_f32_16x16x32_bf16 v[28:31], v[68:71], v[172:175], v[28:31]
	v_mfma_f32_16x16x32_bf16 v[24:27], v[76:79], v[172:175], v[24:27]
	s_waitcnt lgkmcnt(0)
	v_mfma_f32_16x16x32_bf16 v[20:23], v[68:71], v[180:183], v[20:23]
	v_mfma_f32_16x16x32_bf16 v[16:19], v[76:79], v[180:183], v[16:19]
	s_setprio 0
	s_barrier
	s_add_i32 s52, s52, 0x80080
	s_mov_b32 m0, s39
	s_nop 0
	buffer_load_dwordx4 v151, s[8:11], s52 offen lds
	s_mov_b32 m0, s40
	s_nop 0
	buffer_load_dwordx4 v153, s[8:11], s52 offen lds
	s_waitcnt vmcnt(10)
	s_barrier
	s_setprio 1
	v_mfma_f32_16x16x32_bf16 v[44:47], v[184:187], v[146:149], v[44:47]
	v_mfma_f32_16x16x32_bf16 v[40:43], v[192:195], v[146:149], v[40:43]
	v_mfma_f32_16x16x32_bf16 v[36:39], v[184:187], v[160:163], v[36:39]
	v_mfma_f32_16x16x32_bf16 v[32:35], v[192:195], v[160:163], v[32:35]
	v_mfma_f32_16x16x32_bf16 v[12:15], v[184:187], v[168:171], v[12:15]
	v_mfma_f32_16x16x32_bf16 v[8:11], v[192:195], v[168:171], v[8:11]
	v_mfma_f32_16x16x32_bf16 v[4:7], v[184:187], v[176:179], v[4:7]
	v_mfma_f32_16x16x32_bf16 v[0:3], v[192:195], v[176:179], v[0:3]
	v_mfma_f32_16x16x32_bf16 v[44:47], v[188:191], v[156:159], v[44:47]
	v_mfma_f32_16x16x32_bf16 v[40:43], v[196:199], v[156:159], v[40:43]
	v_mfma_f32_16x16x32_bf16 v[36:39], v[188:191], v[164:167], v[36:39]
	v_mfma_f32_16x16x32_bf16 v[32:35], v[196:199], v[164:167], v[32:35]
	v_mfma_f32_16x16x32_bf16 v[12:15], v[188:191], v[172:175], v[12:15]
	v_mfma_f32_16x16x32_bf16 v[8:11], v[196:199], v[172:175], v[8:11]
	v_mfma_f32_16x16x32_bf16 v[4:7], v[188:191], v[180:183], v[4:7]
	v_mfma_f32_16x16x32_bf16 v[0:3], v[196:199], v[180:183], v[0:3]
	s_setprio 0
	s_add_i32 s51, s51, 2
	s_addk_i32 s49, 0x100
	s_addk_i32 s50, 0x100
	s_cmp_gt_u32 s51, 29
	s_barrier
	s_cbranch_scc0 .LBB0_1514
	s_getreg_b32 s10, hwreg(HW_REG_HW_ID, 0, 6)
	s_and_b32 s10, s10, 63
	s_lshl_b32 s10, s10, 2
	s_add_i32 s10, s10, 0
	s_add_i32 s10, s10, 0x20010
	v_mov_b32_e32 v64, s10
	ds_read_b32 v64, v64
	v_mbcnt_lo_u32_b32 v148, -1, 0
	v_mbcnt_hi_u32_b32 v148, -1, v148
	s_mov_b32 s50, s17
	v_lshrrev_b32_e32 v66, 1, v148
	v_and_b32_e32 v156, 24, v66
	s_waitcnt lgkmcnt(0)
	v_readfirstlane_b32 s10, v64
	s_nop 1
	v_lshl_or_b32 v146, s10, 6, v148
	s_lshl_b32 s10, s2, 8
	s_min_i32 s2, s46, 64
	s_ashr_i32 s2, s2, 3
	s_mul_hi_i32 s11, s2, 0xc000
	s_mul_i32 s2, s2, 0xc000
	s_add_u32 s2, s0, s2
	s_addc_u32 s47, s24, s11
	s_ashr_i32 s11, s10, 31
	s_lshl_b64 s[48:49], s[10:11], 2
	v_lshrrev_b32_e32 v64, 1, v146
	s_add_u32 s48, s2, s48
	v_and_b32_e32 v149, 0x60, v64
	s_addc_u32 s49, s47, s49
	v_lshlrev_b32_e32 v96, 2, v149
	v_lshl_add_u64 v[64:65], s[48:49], 0, v[96:97]
	v_lshlrev_b32_e32 v96, 2, v156
	v_lshl_add_u64 v[68:69], v[64:65], 0, v[96:97]
	v_ashrrev_i32_e32 v96, 2, v146
	s_lshl_b32 s48, s46, 8
	v_and_b32_e32 v146, 0xffffffc0, v96
	s_ashr_i32 s49, s48, 31
	v_ashrrev_i32_e32 v147, 31, v146
	v_lshl_add_u64 v[146:147], v[146:147], 0, s[48:49]
	v_and_or_b32 v146, v148, 15, v146
	s_cmp_gt_i32 s46, 63
	v_lshlrev_b64 v[146:147], 11, v[146:147]
	v_lshl_add_u64 v[146:147], v[146:147], 0, s[10:11]
	s_cselect_b32 s2, s44, s21
	s_cselect_b32 s10, s43, s20
	v_or3_b32 v146, v146, v149, v156
	v_mov_b32_e32 v148, s10
	v_mov_b32_e32 v149, s2
	v_lshl_add_u64 v[148:149], v[146:147], 2, v[148:149]
	global_load_dwordx4 v[72:75], v[68:69], off offset:16
	global_load_dwordx4 v[76:79], v[68:69], off
	global_load_dwordx4 v[64:67], v[68:69], off offset:528
	s_nop 0
	global_load_dwordx4 v[68:71], v[68:69], off offset:512
	s_nop 0
	global_load_dwordx4 v[156:159], v[148:149], off offset:16
	global_load_dwordx4 v[160:163], v[148:149], off
	global_load_dwordx4 v[164:167], v[148:149], off offset:528
	global_load_dwordx4 v[168:171], v[148:149], off offset:512
	s_mov_b64 s[10:11], 0x20000
	v_add_co_u32_e32 v180, vcc, s75, v148
	v_lshl_add_u64 v[176:177], v[148:149], 0, s[10:11]
	s_nop 0
	v_addc_co_u32_e32 v181, vcc, 0, v149, vcc
	global_load_dwordx4 v[172:175], v[180:181], off
	s_nop 0
	global_load_dwordx4 v[176:179], v[176:177], off offset:16
	s_mov_b64 s[10:11], 0x20200
	v_lshl_add_u64 v[184:185], v[148:149], 0, s[10:11]
	global_load_dwordx4 v[180:183], v[180:181], off offset:512
	s_nop 0
	global_load_dwordx4 v[184:187], v[184:185], off offset:16
	v_lshl_add_u64 v[146:147], v[146:147], 1, s[12:13]
	s_mov_b32 s2, 0x10000
	s_mov_b64 s[10:11], 0x40000
	s_mov_b32 s46, s15
	s_mov_b32 s49, s16
	s_waitcnt vmcnt(7)
	v_pk_fma_f32 v[158:159], v[140:141], v[74:75], v[158:159]
	s_waitcnt vmcnt(6)
	v_pk_fma_f32 v[144:145], v[144:145], v[78:79], v[162:163]
	v_pk_fma_f32 v[142:143], v[142:143], v[76:77], v[160:161]
	v_pk_fma_f32 v[140:141], v[138:139], v[72:73], v[156:157]
	v_cvt_pk_bf16_f32 v138, v142, v143
	v_cvt_pk_bf16_f32 v139, v144, v145
	v_cvt_pk_bf16_f32 v140, v140, v141
	v_cvt_pk_bf16_f32 v141, v158, v159
	global_store_dwordx4 v[146:147], v[138:141], off
	s_waitcnt vmcnt(5)
	v_pk_fma_f32 v[128:129], v[128:129], v[70:71], v[170:171]
	v_pk_fma_f32 v[126:127], v[126:127], v[68:69], v[168:169]
	v_pk_fma_f32 v[138:139], v[124:125], v[66:67], v[166:167]
	v_pk_fma_f32 v[124:125], v[122:123], v[64:65], v[164:165]
	v_cvt_pk_bf16_f32 v122, v126, v127
	v_cvt_pk_bf16_f32 v123, v128, v129
	v_cvt_pk_bf16_f32 v124, v124, v125
	v_cvt_pk_bf16_f32 v125, v138, v139
	global_store_dwordx4 v[146:147], v[122:125], off offset:256
	s_waitcnt vmcnt(4)
	v_pk_fma_f32 v[126:127], v[132:133], v[74:75], v[178:179]
	v_pk_fma_f32 v[128:129], v[130:131], v[72:73], v[176:177]
	v_pk_fma_f32 v[124:125], v[136:137], v[78:79], v[174:175]
	v_pk_fma_f32 v[122:123], v[134:135], v[76:77], v[172:173]
	s_waitcnt vmcnt(3)
	v_pk_fma_f32 v[120:121], v[120:121], v[70:71], v[182:183]
	v_cvt_pk_bf16_f32 v122, v122, v123
	v_cvt_pk_bf16_f32 v123, v124, v125
	v_cvt_pk_bf16_f32 v125, v126, v127
	v_add_co_u32_e32 v126, vcc, s2, v146
	v_cvt_pk_bf16_f32 v124, v128, v129
	s_nop 0
	v_addc_co_u32_e32 v127, vcc, 0, v147, vcc
	global_store_dwordx4 v[126:127], v[122:125], off
	v_pk_fma_f32 v[118:119], v[118:119], v[68:69], v[180:181]
	s_mov_b32 s2, 0x40000
	s_waitcnt vmcnt(3)
	v_pk_fma_f32 v[122:123], v[116:117], v[66:67], v[186:187]
	v_pk_fma_f32 v[116:117], v[114:115], v[64:65], v[184:185]
	v_cvt_pk_bf16_f32 v114, v118, v119
	v_cvt_pk_bf16_f32 v115, v120, v121
	v_cvt_pk_bf16_f32 v116, v116, v117
	v_cvt_pk_bf16_f32 v117, v122, v123
	v_add_co_u32_e32 v122, vcc, s2, v148
	global_store_dwordx4 v[126:127], v[114:117], off offset:256
	v_lshl_add_u64 v[118:119], v[148:149], 0, s[10:11]
	v_addc_co_u32_e32 v123, vcc, 0, v149, vcc
	global_load_dwordx4 v[114:117], v[122:123], off
	s_nop 0
	global_load_dwordx4 v[118:121], v[118:119], off offset:16
	s_mov_b64 s[10:11], 0x40200
	v_lshl_add_u64 v[126:127], v[148:149], 0, s[10:11]
	s_mov_b32 s2, 0x60000
	global_load_dwordx4 v[122:125], v[122:123], off offset:512
	s_nop 0
	global_load_dwordx4 v[126:129], v[126:127], off offset:16
	s_mov_b64 s[10:11], 0x60000
	v_add_co_u32_e32 v138, vcc, s2, v148
	v_lshl_add_u64 v[134:135], v[148:149], 0, s[10:11]
	s_nop 0
	v_addc_co_u32_e32 v139, vcc, 0, v149, vcc
	global_load_dwordx4 v[130:133], v[138:139], off
	s_nop 0
	global_load_dwordx4 v[134:137], v[134:135], off offset:16
	s_mov_b64 s[10:11], 0x60200
	v_lshl_add_u64 v[142:143], v[148:149], 0, s[10:11]
	global_load_dwordx4 v[138:141], v[138:139], off offset:512
	s_nop 0
	global_load_dwordx4 v[142:145], v[142:143], off offset:16
	s_mov_b32 s2, 0x30000
	s_mov_b64 s[10:11], 0x100000
	s_waitcnt vmcnt(7)
	v_pk_fma_f32 v[110:111], v[110:111], v[76:77], v[114:115]
	v_pk_fma_f32 v[112:113], v[112:113], v[78:79], v[116:117]
	s_waitcnt vmcnt(6)
	v_pk_fma_f32 v[114:115], v[108:109], v[74:75], v[120:121]
	v_pk_fma_f32 v[108:109], v[106:107], v[72:73], v[118:119]
	v_cvt_pk_bf16_f32 v106, v110, v111
	v_add_co_u32_e32 v110, vcc, s75, v146
	v_cvt_pk_bf16_f32 v107, v112, v113
	v_cvt_pk_bf16_f32 v108, v108, v109
	v_cvt_pk_bf16_f32 v109, v114, v115
	v_addc_co_u32_e32 v111, vcc, 0, v147, vcc
	global_store_dwordx4 v[110:111], v[106:109], off
	s_waitcnt vmcnt(6)
	v_pk_fma_f32 v[94:95], v[94:95], v[70:71], v[124:125]
	v_pk_fma_f32 v[92:93], v[92:93], v[68:69], v[122:123]
	s_waitcnt vmcnt(5)
	v_pk_fma_f32 v[106:107], v[90:91], v[66:67], v[128:129]
	v_pk_fma_f32 v[90:91], v[88:89], v[64:65], v[126:127]
	v_cvt_pk_bf16_f32 v88, v92, v93
	v_cvt_pk_bf16_f32 v89, v94, v95
	v_cvt_pk_bf16_f32 v90, v90, v91
	v_cvt_pk_bf16_f32 v91, v106, v107
	global_store_dwordx4 v[110:111], v[88:91], off offset:256
	s_waitcnt vmcnt(4)
	v_pk_fma_f32 v[92:93], v[100:101], v[74:75], v[136:137]
	v_pk_fma_f32 v[94:95], v[98:99], v[72:73], v[134:135]
	v_pk_fma_f32 v[90:91], v[104:105], v[78:79], v[132:133]
	v_pk_fma_f32 v[88:89], v[102:103], v[76:77], v[130:131]
	s_waitcnt vmcnt(3)
	v_pk_fma_f32 v[86:87], v[86:87], v[70:71], v[140:141]
	v_cvt_pk_bf16_f32 v88, v88, v89
	v_cvt_pk_bf16_f32 v89, v90, v91
	v_cvt_pk_bf16_f32 v91, v92, v93
	v_add_co_u32_e32 v92, vcc, s2, v146
	v_cvt_pk_bf16_f32 v90, v94, v95
	s_nop 0
	v_addc_co_u32_e32 v93, vcc, 0, v147, vcc
	global_store_dwordx4 v[92:93], v[88:91], off
	v_pk_fma_f32 v[84:85], v[84:85], v[68:69], v[138:139]
	s_mov_b32 s2, 0x100000
	s_waitcnt vmcnt(3)
	v_pk_fma_f32 v[88:89], v[82:83], v[66:67], v[144:145]
	v_pk_fma_f32 v[82:83], v[80:81], v[64:65], v[142:143]
	v_cvt_pk_bf16_f32 v80, v84, v85
	v_cvt_pk_bf16_f32 v81, v86, v87
	v_cvt_pk_bf16_f32 v82, v82, v83
	v_cvt_pk_bf16_f32 v83, v88, v89
	v_add_co_u32_e32 v88, vcc, s2, v148
	global_store_dwordx4 v[92:93], v[80:83], off offset:256
	s_nop 0
	v_addc_co_u32_e32 v89, vcc, 0, v149, vcc
	v_lshl_add_u64 v[80:81], v[148:149], 0, s[10:11]
	global_load_dwordx4 v[84:87], v[88:89], off
	s_nop 0
	global_load_dwordx4 v[80:83], v[80:81], off offset:16
	s_mov_b64 s[10:11], 0x100200
	v_lshl_add_u64 v[92:93], v[148:149], 0, s[10:11]
	s_mov_b32 s2, 0x120000
	global_load_dwordx4 v[88:91], v[88:89], off offset:512
	s_nop 0
	global_load_dwordx4 v[92:95], v[92:93], off offset:16
	s_mov_b64 s[10:11], 0x120000
	v_add_co_u32_e32 v106, vcc, s2, v148
	v_lshl_add_u64 v[102:103], v[148:149], 0, s[10:11]
	s_nop 0
	v_addc_co_u32_e32 v107, vcc, 0, v149, vcc
	global_load_dwordx4 v[98:101], v[106:107], off
	s_nop 0
	global_load_dwordx4 v[102:105], v[102:103], off offset:16
	s_mov_b64 s[10:11], 0x120200
	v_lshl_add_u64 v[110:111], v[148:149], 0, s[10:11]
	global_load_dwordx4 v[106:109], v[106:107], off offset:512
	s_nop 0
	global_load_dwordx4 v[110:113], v[110:111], off offset:16
	s_mov_b32 s2, 0x80000
	s_mov_b64 s[10:11], 0x140000
	s_waitcnt vmcnt(7)
	v_pk_fma_f32 v[60:61], v[60:61], v[76:77], v[84:85]
	v_pk_fma_f32 v[62:63], v[62:63], v[78:79], v[86:87]
	s_waitcnt vmcnt(6)
	v_pk_fma_f32 v[82:83], v[58:59], v[74:75], v[82:83]
	v_pk_fma_f32 v[58:59], v[56:57], v[72:73], v[80:81]
	v_cvt_pk_bf16_f32 v56, v60, v61
	v_add_co_u32_e32 v60, vcc, s2, v146
	v_cvt_pk_bf16_f32 v57, v62, v63
	v_cvt_pk_bf16_f32 v58, v58, v59
	v_cvt_pk_bf16_f32 v59, v82, v83
	v_addc_co_u32_e32 v61, vcc, 0, v147, vcc
	global_store_dwordx4 v[60:61], v[56:59], off
	s_waitcnt vmcnt(6)
	v_pk_fma_f32 v[46:47], v[46:47], v[70:71], v[90:91]
	v_pk_fma_f32 v[44:45], v[44:45], v[68:69], v[88:89]
	s_waitcnt vmcnt(5)
	v_pk_fma_f32 v[56:57], v[42:43], v[66:67], v[94:95]
	v_pk_fma_f32 v[42:43], v[40:41], v[64:65], v[92:93]
	v_cvt_pk_bf16_f32 v40, v44, v45
	v_cvt_pk_bf16_f32 v41, v46, v47
	v_cvt_pk_bf16_f32 v42, v42, v43
	v_cvt_pk_bf16_f32 v43, v56, v57
	global_store_dwordx4 v[60:61], v[40:43], off offset:256
	s_waitcnt vmcnt(4)
	v_pk_fma_f32 v[44:45], v[50:51], v[74:75], v[104:105]
	s_mov_b32 s2, 0x90000
	v_pk_fma_f32 v[42:43], v[54:55], v[78:79], v[100:101]
	v_pk_fma_f32 v[40:41], v[52:53], v[76:77], v[98:99]
	v_pk_fma_f32 v[46:47], v[48:49], v[72:73], v[102:103]
	v_cvt_pk_bf16_f32 v40, v40, v41
	v_cvt_pk_bf16_f32 v41, v42, v43
	v_cvt_pk_bf16_f32 v43, v44, v45
	v_add_co_u32_e32 v44, vcc, s2, v146
	v_cvt_pk_bf16_f32 v42, v46, v47
	s_nop 0
	v_addc_co_u32_e32 v45, vcc, 0, v147, vcc
	global_store_dwordx4 v[44:45], v[40:43], off
	s_waitcnt vmcnt(4)
	v_pk_fma_f32 v[38:39], v[38:39], v[70:71], v[108:109]
	v_pk_fma_f32 v[36:37], v[36:37], v[68:69], v[106:107]
	s_waitcnt vmcnt(3)
	v_pk_fma_f32 v[40:41], v[34:35], v[66:67], v[112:113]
	v_pk_fma_f32 v[34:35], v[32:33], v[64:65], v[110:111]
	s_mov_b32 s2, 0x140000
	v_cvt_pk_bf16_f32 v32, v36, v37
	v_cvt_pk_bf16_f32 v33, v38, v39
	v_cvt_pk_bf16_f32 v34, v34, v35
	v_cvt_pk_bf16_f32 v35, v40, v41
	v_add_co_u32_e32 v40, vcc, s2, v148
	global_store_dwordx4 v[44:45], v[32:35], off offset:256
	v_lshl_add_u64 v[36:37], v[148:149], 0, s[10:11]
	v_addc_co_u32_e32 v41, vcc, 0, v149, vcc
	global_load_dwordx4 v[32:35], v[40:41], off
	s_nop 0
	global_load_dwordx4 v[36:39], v[36:37], off offset:16
	s_mov_b64 s[10:11], 0x140200
	v_lshl_add_u64 v[44:45], v[148:149], 0, s[10:11]
	s_mov_b32 s2, 0x160000
	global_load_dwordx4 v[40:43], v[40:41], off offset:512
	s_nop 0
	global_load_dwordx4 v[44:47], v[44:45], off offset:16
	s_mov_b64 s[10:11], 0x160000
	v_add_co_u32_e32 v56, vcc, s2, v148
	v_lshl_add_u64 v[52:53], v[148:149], 0, s[10:11]
	s_nop 0
	v_addc_co_u32_e32 v57, vcc, 0, v149, vcc
	global_load_dwordx4 v[48:51], v[56:57], off
	s_nop 0
	global_load_dwordx4 v[52:55], v[52:53], off offset:16
	s_mov_b64 s[10:11], 0x160200
	v_lshl_add_u64 v[60:61], v[148:149], 0, s[10:11]
	global_load_dwordx4 v[56:59], v[56:57], off offset:512
	s_nop 0
	global_load_dwordx4 v[60:63], v[60:61], off offset:16
	s_mov_b32 s2, 0xa0000
	s_waitcnt vmcnt(7)
	v_pk_fma_f32 v[28:29], v[28:29], v[76:77], v[32:33]
	v_pk_fma_f32 v[30:31], v[30:31], v[78:79], v[34:35]
	s_waitcnt vmcnt(6)
	v_pk_fma_f32 v[32:33], v[26:27], v[74:75], v[38:39]
	v_pk_fma_f32 v[26:27], v[24:25], v[72:73], v[36:37]
	v_cvt_pk_bf16_f32 v24, v28, v29
	v_add_co_u32_e32 v28, vcc, s2, v146
	v_cvt_pk_bf16_f32 v25, v30, v31
	v_cvt_pk_bf16_f32 v26, v26, v27
	v_cvt_pk_bf16_f32 v27, v32, v33
	v_addc_co_u32_e32 v29, vcc, 0, v147, vcc
	global_store_dwordx4 v[28:29], v[24:27], off
	s_waitcnt vmcnt(6)
	v_pk_fma_f32 v[14:15], v[14:15], v[70:71], v[42:43]
	v_pk_fma_f32 v[12:13], v[12:13], v[68:69], v[40:41]
	s_waitcnt vmcnt(5)
	v_pk_fma_f32 v[24:25], v[10:11], v[66:67], v[46:47]
	v_pk_fma_f32 v[10:11], v[8:9], v[64:65], v[44:45]
	v_cvt_pk_bf16_f32 v8, v12, v13
	v_cvt_pk_bf16_f32 v9, v14, v15
	v_cvt_pk_bf16_f32 v10, v10, v11
	v_cvt_pk_bf16_f32 v11, v24, v25
	global_store_dwordx4 v[28:29], v[8:11], off offset:256
	s_waitcnt vmcnt(4)
	v_pk_fma_f32 v[12:13], v[18:19], v[74:75], v[54:55]
	s_mov_b32 s2, 0xb0000
	v_pk_fma_f32 v[10:11], v[22:23], v[78:79], v[50:51]
	v_pk_fma_f32 v[8:9], v[20:21], v[76:77], v[48:49]
	v_pk_fma_f32 v[14:15], v[16:17], v[72:73], v[52:53]
	v_cvt_pk_bf16_f32 v8, v8, v9
	v_cvt_pk_bf16_f32 v9, v10, v11
	v_cvt_pk_bf16_f32 v11, v12, v13
	v_add_co_u32_e32 v12, vcc, s2, v146
	v_cvt_pk_bf16_f32 v10, v14, v15
	s_nop 0
	v_addc_co_u32_e32 v13, vcc, 0, v147, vcc
	global_store_dwordx4 v[12:13], v[8:11], off
	s_waitcnt vmcnt(4)
	v_pk_fma_f32 v[6:7], v[6:7], v[70:71], v[58:59]
	v_pk_fma_f32 v[4:5], v[4:5], v[68:69], v[56:57]
	s_waitcnt vmcnt(3)
	v_pk_fma_f32 v[8:9], v[2:3], v[66:67], v[62:63]
	v_pk_fma_f32 v[2:3], v[0:1], v[64:65], v[60:61]
	v_cvt_pk_bf16_f32 v0, v4, v5
	v_cvt_pk_bf16_f32 v1, v6, v7
	v_cvt_pk_bf16_f32 v2, v2, v3
	v_cvt_pk_bf16_f32 v3, v8, v9
	s_and_b64 vcc, exec, s[4:5]
	s_mov_b32 s2, s14
	global_store_dwordx4 v[12:13], v[0:3], off offset:256
	s_cbranch_vccz .LBB0_1508
	s_branch .LBB0_1517

.LBB0_1639:
	ds_read_b128 v[134:137], v132
	ds_read_b128 v[138:141], v132 offset:1024
	ds_read_b128 v[142:145], v132 offset:2048
	ds_read_b128 v[146:149], v132 offset:3072
	s_add_i32 s10, s41, 0xfff80080
	s_cmp_eq_u32 s43, 28
	s_cselect_b32 s46, s39, s10
	s_cselect_b32 s44, s40, s42
	s_or_b32 s45, s46, 0x80
	s_mov_b32 m0, s35
	ds_read_b128 v[150:153], v133
	ds_read_b128 v[154:157], v133 offset:1024
	ds_read_b128 v[158:161], v133 offset:2048
	ds_read_b128 v[162:165], v133 offset:3072
	ds_read_b128 v[166:169], v133 offset:4096
	ds_read_b128 v[170:173], v133 offset:5120
	ds_read_b128 v[174:177], v133 offset:6144
	ds_read_b128 v[178:181], v133 offset:7168
	buffer_load_dwordx4 v130, s[72:75], s41 offen lds
	s_mov_b32 m0, s36
	s_nop 0
	buffer_load_dwordx4 v131, s[72:75], s41 offen lds
	s_waitcnt lgkmcnt(8)
	s_waitcnt vmcnt(10)
	s_barrier
	s_waitcnt lgkmcnt(0)
	s_setprio 1
	s_waitcnt lgkmcnt(7)
	v_mfma_f32_16x16x32_bf16 v[126:129], v[150:153], v[134:137], v[126:129]
	v_mfma_f32_16x16x32_bf16 v[114:117], v[150:153], v[142:145], v[114:117]
	s_waitcnt lgkmcnt(5)
	v_mfma_f32_16x16x32_bf16 v[122:125], v[158:161], v[134:137], v[122:125]
	v_mfma_f32_16x16x32_bf16 v[106:109], v[158:161], v[142:145], v[106:109]
	s_waitcnt lgkmcnt(3)
	v_mfma_f32_16x16x32_bf16 v[118:121], v[166:169], v[134:137], v[118:121]
	v_mfma_f32_16x16x32_bf16 v[102:105], v[166:169], v[142:145], v[102:105]
	s_waitcnt lgkmcnt(1)
	v_mfma_f32_16x16x32_bf16 v[110:113], v[174:177], v[134:137], v[110:113]
	v_mfma_f32_16x16x32_bf16 v[98:101], v[174:177], v[142:145], v[98:101]
	v_mfma_f32_16x16x32_bf16 v[126:129], v[154:157], v[138:141], v[126:129]
	v_mfma_f32_16x16x32_bf16 v[114:117], v[154:157], v[146:149], v[114:117]
	v_mfma_f32_16x16x32_bf16 v[122:125], v[162:165], v[138:141], v[122:125]
	v_mfma_f32_16x16x32_bf16 v[106:109], v[162:165], v[146:149], v[106:109]
	v_mfma_f32_16x16x32_bf16 v[118:121], v[170:173], v[138:141], v[118:121]
	v_mfma_f32_16x16x32_bf16 v[102:105], v[170:173], v[146:149], v[102:105]
	s_waitcnt lgkmcnt(0)
	v_mfma_f32_16x16x32_bf16 v[110:113], v[178:181], v[138:141], v[110:113]
	v_mfma_f32_16x16x32_bf16 v[98:101], v[178:181], v[146:149], v[98:101]
	s_setprio 0
	s_barrier
	s_mov_b32 s10, s74
	s_mov_b32 s11, s75
	s_mov_b32 m0, s19
	ds_read_b128 v[182:185], v132 offset:16384
	ds_read_b128 v[186:189], v132 offset:17408
	ds_read_b128 v[190:193], v132 offset:18432
	ds_read_b128 v[194:197], v132 offset:19456
	buffer_load_dwordx4 v130, s[8:11], s44 offen lds
	s_mov_b32 m0, s20
	s_nop 0
	buffer_load_dwordx4 v131, s[8:11], s44 offen lds
	s_waitcnt vmcnt(10)
	s_barrier
	s_waitcnt lgkmcnt(0)
	s_setprio 1
	s_waitcnt lgkmcnt(3)
	v_mfma_f32_16x16x32_bf16 v[92:95], v[150:153], v[182:185], v[92:95]
	s_waitcnt lgkmcnt(1)
	v_mfma_f32_16x16x32_bf16 v[64:67], v[150:153], v[190:193], v[64:67]
	v_mfma_f32_16x16x32_bf16 v[84:87], v[158:161], v[182:185], v[84:87]
	v_mfma_f32_16x16x32_bf16 v[48:51], v[158:161], v[190:193], v[48:51]
	v_mfma_f32_16x16x32_bf16 v[76:79], v[166:169], v[182:185], v[76:79]
	v_mfma_f32_16x16x32_bf16 v[40:43], v[166:169], v[190:193], v[40:43]
	v_mfma_f32_16x16x32_bf16 v[60:63], v[174:177], v[182:185], v[60:63]
	v_mfma_f32_16x16x32_bf16 v[32:35], v[174:177], v[190:193], v[32:35]
	v_mfma_f32_16x16x32_bf16 v[92:95], v[154:157], v[186:189], v[92:95]
	s_waitcnt lgkmcnt(0)
	v_mfma_f32_16x16x32_bf16 v[64:67], v[154:157], v[194:197], v[64:67]
	v_mfma_f32_16x16x32_bf16 v[84:87], v[162:165], v[186:189], v[84:87]
	v_mfma_f32_16x16x32_bf16 v[48:51], v[162:165], v[194:197], v[48:51]
	v_mfma_f32_16x16x32_bf16 v[76:79], v[170:173], v[186:189], v[76:79]
	v_mfma_f32_16x16x32_bf16 v[40:43], v[170:173], v[194:197], v[40:43]
	v_mfma_f32_16x16x32_bf16 v[60:63], v[178:181], v[186:189], v[60:63]
	v_mfma_f32_16x16x32_bf16 v[32:35], v[178:181], v[194:197], v[32:35]
	s_setprio 0
	s_mov_b32 m0, s2
	s_barrier
	ds_read_b128 v[150:153], v133 offset:16384
	ds_read_b128 v[154:157], v133 offset:17408
	ds_read_b128 v[158:161], v133 offset:18432
	ds_read_b128 v[162:165], v133 offset:19456
	ds_read_b128 v[166:169], v133 offset:20480
	ds_read_b128 v[170:173], v133 offset:21504
	ds_read_b128 v[174:177], v133 offset:22528
	ds_read_b128 v[178:181], v133 offset:23552
	buffer_load_dwordx4 v130, s[72:75], s46 offen lds
	s_mov_b32 m0, s21
	s_nop 0
	buffer_load_dwordx4 v131, s[72:75], s46 offen lds
	s_barrier
	s_waitcnt lgkmcnt(0)
	s_setprio 1
	s_waitcnt lgkmcnt(7)
	v_mfma_f32_16x16x32_bf16 v[88:91], v[150:153], v[134:137], v[88:91]
	v_mfma_f32_16x16x32_bf16 v[72:75], v[150:153], v[142:145], v[72:75]
	s_waitcnt lgkmcnt(5)
	v_mfma_f32_16x16x32_bf16 v[80:83], v[158:161], v[134:137], v[80:83]
	v_mfma_f32_16x16x32_bf16 v[56:59], v[158:161], v[142:145], v[56:59]
	s_waitcnt lgkmcnt(3)
	v_mfma_f32_16x16x32_bf16 v[68:71], v[166:169], v[134:137], v[68:71]
	v_mfma_f32_16x16x32_bf16 v[44:47], v[166:169], v[142:145], v[44:47]
	s_waitcnt lgkmcnt(1)
	v_mfma_f32_16x16x32_bf16 v[52:55], v[174:177], v[134:137], v[52:55]
	v_mfma_f32_16x16x32_bf16 v[36:39], v[174:177], v[142:145], v[36:39]
	v_mfma_f32_16x16x32_bf16 v[88:91], v[154:157], v[138:141], v[88:91]
	v_mfma_f32_16x16x32_bf16 v[72:75], v[154:157], v[146:149], v[72:75]
	v_mfma_f32_16x16x32_bf16 v[80:83], v[162:165], v[138:141], v[80:83]
	v_mfma_f32_16x16x32_bf16 v[56:59], v[162:165], v[146:149], v[56:59]
	v_mfma_f32_16x16x32_bf16 v[68:71], v[170:173], v[138:141], v[68:71]
	v_mfma_f32_16x16x32_bf16 v[44:47], v[170:173], v[146:149], v[44:47]
	s_waitcnt lgkmcnt(0)
	v_mfma_f32_16x16x32_bf16 v[52:55], v[178:181], v[138:141], v[52:55]
	v_mfma_f32_16x16x32_bf16 v[36:39], v[178:181], v[146:149], v[36:39]
	s_setprio 0
	s_barrier
	s_add_i32 s47, s44, 0x80000
	s_mov_b32 m0, s22
	s_nop 0
	buffer_load_dwordx4 v130, s[8:11], s47 offen lds
	s_mov_b32 m0, s23
	s_nop 0
	buffer_load_dwordx4 v131, s[8:11], s47 offen lds
	s_waitcnt vmcnt(10)
	s_barrier
	s_setprio 1
	v_mfma_f32_16x16x32_bf16 v[28:31], v[150:153], v[182:185], v[28:31]
	v_mfma_f32_16x16x32_bf16 v[16:19], v[150:153], v[190:193], v[16:19]
	v_mfma_f32_16x16x32_bf16 v[24:27], v[158:161], v[182:185], v[24:27]
	v_mfma_f32_16x16x32_bf16 v[8:11], v[158:161], v[190:193], v[8:11]
	v_mfma_f32_16x16x32_bf16 v[20:23], v[166:169], v[182:185], v[20:23]
	v_mfma_f32_16x16x32_bf16 v[4:7], v[166:169], v[190:193], v[4:7]
	v_mfma_f32_16x16x32_bf16 v[12:15], v[174:177], v[182:185], v[12:15]
	v_mfma_f32_16x16x32_bf16 v[0:3], v[174:177], v[190:193], v[0:3]
	v_mfma_f32_16x16x32_bf16 v[28:31], v[154:157], v[186:189], v[28:31]
	v_mfma_f32_16x16x32_bf16 v[16:19], v[154:157], v[194:197], v[16:19]
	v_mfma_f32_16x16x32_bf16 v[24:27], v[162:165], v[186:189], v[24:27]
	v_mfma_f32_16x16x32_bf16 v[8:11], v[162:165], v[194:197], v[8:11]
	v_mfma_f32_16x16x32_bf16 v[20:23], v[170:173], v[186:189], v[20:23]
	v_mfma_f32_16x16x32_bf16 v[4:7], v[170:173], v[194:197], v[4:7]
	v_mfma_f32_16x16x32_bf16 v[12:15], v[178:181], v[186:189], v[12:15]
	v_mfma_f32_16x16x32_bf16 v[0:3], v[178:181], v[194:197], v[0:3]
	s_setprio 0
	s_barrier
	ds_read_b128 v[134:137], v132 offset:32768
	ds_read_b128 v[138:141], v132 offset:33792
	ds_read_b128 v[142:145], v132 offset:34816
	ds_read_b128 v[146:149], v132 offset:35840
	s_add_i32 s46, s46, 0x80000
	s_mov_b32 m0, s24
	ds_read_b128 v[150:153], v133 offset:32768
	ds_read_b128 v[154:157], v133 offset:33792
	ds_read_b128 v[158:161], v133 offset:34816
	ds_read_b128 v[162:165], v133 offset:35840
	ds_read_b128 v[166:169], v133 offset:36864
	ds_read_b128 v[170:173], v133 offset:37888
	ds_read_b128 v[174:177], v133 offset:38912
	ds_read_b128 v[178:181], v133 offset:39936
	buffer_load_dwordx4 v130, s[72:75], s46 offen lds
	s_mov_b32 m0, s25
	s_nop 0
	buffer_load_dwordx4 v131, s[72:75], s46 offen lds
	s_waitcnt lgkmcnt(8)
	s_waitcnt vmcnt(10)
	s_barrier
	s_waitcnt lgkmcnt(0)
	s_setprio 1
	s_waitcnt lgkmcnt(7)
	v_mfma_f32_16x16x32_bf16 v[126:129], v[150:153], v[134:137], v[126:129]
	v_mfma_f32_16x16x32_bf16 v[114:117], v[150:153], v[142:145], v[114:117]
	s_waitcnt lgkmcnt(5)
	v_mfma_f32_16x16x32_bf16 v[122:125], v[158:161], v[134:137], v[122:125]
	v_mfma_f32_16x16x32_bf16 v[106:109], v[158:161], v[142:145], v[106:109]
	s_waitcnt lgkmcnt(3)
	v_mfma_f32_16x16x32_bf16 v[118:121], v[166:169], v[134:137], v[118:121]
	v_mfma_f32_16x16x32_bf16 v[102:105], v[166:169], v[142:145], v[102:105]
	s_waitcnt lgkmcnt(1)
	v_mfma_f32_16x16x32_bf16 v[110:113], v[174:177], v[134:137], v[110:113]
	v_mfma_f32_16x16x32_bf16 v[98:101], v[174:177], v[142:145], v[98:101]
	v_mfma_f32_16x16x32_bf16 v[126:129], v[154:157], v[138:141], v[126:129]
	v_mfma_f32_16x16x32_bf16 v[114:117], v[154:157], v[146:149], v[114:117]
	v_mfma_f32_16x16x32_bf16 v[122:125], v[162:165], v[138:141], v[122:125]
	v_mfma_f32_16x16x32_bf16 v[106:109], v[162:165], v[146:149], v[106:109]
	v_mfma_f32_16x16x32_bf16 v[118:121], v[170:173], v[138:141], v[118:121]
	v_mfma_f32_16x16x32_bf16 v[102:105], v[170:173], v[146:149], v[102:105]
	s_waitcnt lgkmcnt(0)
	v_mfma_f32_16x16x32_bf16 v[110:113], v[178:181], v[138:141], v[110:113]
	v_mfma_f32_16x16x32_bf16 v[98:101], v[178:181], v[146:149], v[98:101]
	s_setprio 0
	s_barrier
	s_or_b32 s46, s44, 0x80
	s_mov_b32 m0, s26
	ds_read_b128 v[182:185], v132 offset:49152
	ds_read_b128 v[186:189], v132 offset:50176
	ds_read_b128 v[190:193], v132 offset:51200
	ds_read_b128 v[194:197], v132 offset:52224
	buffer_load_dwordx4 v130, s[8:11], s46 offen lds
	s_mov_b32 m0, s27
	s_nop 0
	buffer_load_dwordx4 v131, s[8:11], s46 offen lds
	s_waitcnt vmcnt(10)
	s_barrier
	s_waitcnt lgkmcnt(0)
	s_setprio 1
	s_waitcnt lgkmcnt(3)
	v_mfma_f32_16x16x32_bf16 v[92:95], v[150:153], v[182:185], v[92:95]
	s_waitcnt lgkmcnt(1)
	v_mfma_f32_16x16x32_bf16 v[64:67], v[150:153], v[190:193], v[64:67]
	v_mfma_f32_16x16x32_bf16 v[84:87], v[158:161], v[182:185], v[84:87]
	v_mfma_f32_16x16x32_bf16 v[48:51], v[158:161], v[190:193], v[48:51]
	v_mfma_f32_16x16x32_bf16 v[76:79], v[166:169], v[182:185], v[76:79]
	v_mfma_f32_16x16x32_bf16 v[40:43], v[166:169], v[190:193], v[40:43]
	v_mfma_f32_16x16x32_bf16 v[60:63], v[174:177], v[182:185], v[60:63]
	v_mfma_f32_16x16x32_bf16 v[32:35], v[174:177], v[190:193], v[32:35]
	v_mfma_f32_16x16x32_bf16 v[92:95], v[154:157], v[186:189], v[92:95]
	s_waitcnt lgkmcnt(0)
	v_mfma_f32_16x16x32_bf16 v[64:67], v[154:157], v[194:197], v[64:67]
	v_mfma_f32_16x16x32_bf16 v[84:87], v[162:165], v[186:189], v[84:87]
	v_mfma_f32_16x16x32_bf16 v[48:51], v[162:165], v[194:197], v[48:51]
	v_mfma_f32_16x16x32_bf16 v[76:79], v[170:173], v[186:189], v[76:79]
	v_mfma_f32_16x16x32_bf16 v[40:43], v[170:173], v[194:197], v[40:43]
	v_mfma_f32_16x16x32_bf16 v[60:63], v[178:181], v[186:189], v[60:63]
	v_mfma_f32_16x16x32_bf16 v[32:35], v[178:181], v[194:197], v[32:35]
	s_setprio 0
	s_mov_b32 m0, s28
	s_barrier
	ds_read_b128 v[150:153], v133 offset:49152
	ds_read_b128 v[154:157], v133 offset:50176
	ds_read_b128 v[158:161], v133 offset:51200
	ds_read_b128 v[162:165], v133 offset:52224
	ds_read_b128 v[166:169], v133 offset:53248
	ds_read_b128 v[170:173], v133 offset:54272
	ds_read_b128 v[174:177], v133 offset:55296
	ds_read_b128 v[178:181], v133 offset:56320
	buffer_load_dwordx4 v130, s[72:75], s45 offen lds
	s_mov_b32 m0, s29
	s_nop 0
	buffer_load_dwordx4 v131, s[72:75], s45 offen lds
	s_barrier
	s_waitcnt lgkmcnt(0)
	s_setprio 1
	s_waitcnt lgkmcnt(7)
	v_mfma_f32_16x16x32_bf16 v[88:91], v[150:153], v[134:137], v[88:91]
	v_mfma_f32_16x16x32_bf16 v[72:75], v[150:153], v[142:145], v[72:75]
	s_waitcnt lgkmcnt(5)
	v_mfma_f32_16x16x32_bf16 v[80:83], v[158:161], v[134:137], v[80:83]
	v_mfma_f32_16x16x32_bf16 v[56:59], v[158:161], v[142:145], v[56:59]
	s_waitcnt lgkmcnt(3)
	v_mfma_f32_16x16x32_bf16 v[68:71], v[166:169], v[134:137], v[68:71]
	v_mfma_f32_16x16x32_bf16 v[44:47], v[166:169], v[142:145], v[44:47]
	s_waitcnt lgkmcnt(1)
	v_mfma_f32_16x16x32_bf16 v[52:55], v[174:177], v[134:137], v[52:55]
	v_mfma_f32_16x16x32_bf16 v[36:39], v[174:177], v[142:145], v[36:39]
	v_mfma_f32_16x16x32_bf16 v[88:91], v[154:157], v[138:141], v[88:91]
	v_mfma_f32_16x16x32_bf16 v[72:75], v[154:157], v[146:149], v[72:75]
	v_mfma_f32_16x16x32_bf16 v[80:83], v[162:165], v[138:141], v[80:83]
	v_mfma_f32_16x16x32_bf16 v[56:59], v[162:165], v[146:149], v[56:59]
	v_mfma_f32_16x16x32_bf16 v[68:71], v[170:173], v[138:141], v[68:71]
	v_mfma_f32_16x16x32_bf16 v[44:47], v[170:173], v[146:149], v[44:47]
	s_waitcnt lgkmcnt(0)
	v_mfma_f32_16x16x32_bf16 v[52:55], v[178:181], v[138:141], v[52:55]
	v_mfma_f32_16x16x32_bf16 v[36:39], v[178:181], v[146:149], v[36:39]
	s_setprio 0
	s_barrier
	s_add_i32 s44, s44, 0x80080
	s_mov_b32 m0, s30
	s_nop 0
	buffer_load_dwordx4 v130, s[8:11], s44 offen lds
	s_mov_b32 m0, s31
	s_nop 0
	buffer_load_dwordx4 v131, s[8:11], s44 offen lds
	s_waitcnt vmcnt(10)
	s_barrier
	s_setprio 1
	v_mfma_f32_16x16x32_bf16 v[28:31], v[150:153], v[182:185], v[28:31]
	v_mfma_f32_16x16x32_bf16 v[16:19], v[150:153], v[190:193], v[16:19]
	v_mfma_f32_16x16x32_bf16 v[24:27], v[158:161], v[182:185], v[24:27]
	v_mfma_f32_16x16x32_bf16 v[8:11], v[158:161], v[190:193], v[8:11]
	v_mfma_f32_16x16x32_bf16 v[20:23], v[166:169], v[182:185], v[20:23]
	v_mfma_f32_16x16x32_bf16 v[4:7], v[166:169], v[190:193], v[4:7]
	v_mfma_f32_16x16x32_bf16 v[12:15], v[174:177], v[182:185], v[12:15]
	v_mfma_f32_16x16x32_bf16 v[0:3], v[174:177], v[190:193], v[0:3]
	v_mfma_f32_16x16x32_bf16 v[28:31], v[154:157], v[186:189], v[28:31]
	v_mfma_f32_16x16x32_bf16 v[16:19], v[154:157], v[194:197], v[16:19]
	v_mfma_f32_16x16x32_bf16 v[24:27], v[162:165], v[186:189], v[24:27]
	v_mfma_f32_16x16x32_bf16 v[8:11], v[162:165], v[194:197], v[8:11]
	v_mfma_f32_16x16x32_bf16 v[20:23], v[170:173], v[186:189], v[20:23]
	v_mfma_f32_16x16x32_bf16 v[4:7], v[170:173], v[194:197], v[4:7]
	v_mfma_f32_16x16x32_bf16 v[12:15], v[178:181], v[186:189], v[12:15]
	v_mfma_f32_16x16x32_bf16 v[0:3], v[178:181], v[194:197], v[0:3]
	s_setprio 0
	s_add_i32 s43, s43, 2
	s_addk_i32 s41, 0x100
	s_addk_i32 s42, 0x100
	s_cmp_gt_u32 s43, 29
	s_barrier
	s_cbranch_scc0 .LBB0_1639
	s_getreg_b32 s10, hwreg(HW_REG_HW_ID, 0, 6)
	s_and_b32 s10, s10, 63
	s_lshl_b32 s10, s10, 2
	s_add_i32 s10, s10, 0
	s_add_i32 s10, s10, 0x20010
	v_mov_b32_e32 v96, s10
	ds_read_b32 v96, v96
	s_mul_i32 s10, s34, 0x120
	s_lshl_b32 s11, s37, 2
	v_mbcnt_lo_u32_b32 v136, -1, 0
	v_mbcnt_hi_u32_b32 v136, -1, v136
	s_add_i32 s11, s11, s10
	s_waitcnt lgkmcnt(0)
	v_readfirstlane_b32 s34, v96
	v_and_b32_e32 v137, 15, v136
	s_mov_b32 s10, 0x21000
	v_lshl_or_b32 v96, s34, 6, v136
	v_ashrrev_i32_e32 v134, 8, v96
	v_add_u32_e32 v134, s11, v134
	v_ashrrev_i32_e32 v135, 31, v134
	v_lshrrev_b32_e32 v96, 1, v96
	v_lshlrev_b64 v[134:135], 8, v[134:135]
	v_and_b32_e32 v96, 0x60, v96
	v_or3_b32 v134, v134, v96, v137
	v_lshlrev_b64 v[134:135], 8, v[134:135]
	v_lshl_add_u64 v[134:135], s[12:13], 0, v[134:135]
	v_and_b32_e32 v96, 48, v136
	v_lshl_add_u64 v[134:135], v[134:135], 0, v[96:97]
	global_store_dwordx4 v[134:135], v[126:129], off
	global_store_dwordx4 v[134:135], v[122:125], off offset:64
	global_store_dwordx4 v[134:135], v[118:121], off offset:128
	global_store_dwordx4 v[134:135], v[110:113], off offset:192
	s_mov_b32 s34, s14
	s_mov_b32 s37, s15
	v_add_co_u32_e32 v110, vcc, s75, v134
	s_mov_b32 s42, s17
	s_nop 0
	v_addc_co_u32_e32 v111, vcc, 0, v135, vcc
	v_add_co_u32_e32 v112, vcc, s10, v134
	s_mov_b64 s[10:11], 0x1000
	s_nop 0
	v_addc_co_u32_e32 v113, vcc, 0, v135, vcc
	global_store_dwordx4 v[112:113], v[88:91], off offset:-4096
	global_store_dwordx4 v[110:111], v[80:83], off offset:64
	global_store_dwordx4 v[110:111], v[68:71], off offset:128
	global_store_dwordx4 v[110:111], v[52:55], off offset:192
	s_mov_b32 s41, s16
	s_nop 0
	v_add_co_u32_e32 v54, vcc, s63, v134
	v_lshl_add_u64 v[52:53], v[134:135], 0, s[10:11]
	s_nop 0
	v_addc_co_u32_e32 v55, vcc, 0, v135, vcc
	s_mov_b64 s[10:11], 0x8000
	global_store_dwordx4 v[54:55], v[114:117], off
	global_store_dwordx4 v[52:53], v[106:109], off offset:64
	global_store_dwordx4 v[52:53], v[102:105], off offset:128
	global_store_dwordx4 v[52:53], v[98:101], off offset:192
	global_store_dwordx4 v[112:113], v[72:75], off
	global_store_dwordx4 v[112:113], v[56:59], off offset:64
	global_store_dwordx4 v[112:113], v[44:47], off offset:128
	global_store_dwordx4 v[112:113], v[36:39], off offset:192
	s_nop 1
	v_lshl_add_u64 v[36:37], v[134:135], 0, s[10:11]
	s_mov_b32 s10, 0x8000
	v_add_co_u32_e32 v38, vcc, s10, v134
	s_mov_b32 s10, 0x28000
	s_nop 0
	v_addc_co_u32_e32 v39, vcc, 0, v135, vcc
	global_store_dwordx4 v[38:39], v[92:95], off
	global_store_dwordx4 v[36:37], v[84:87], off offset:64
	global_store_dwordx4 v[36:37], v[76:79], off offset:128
	global_store_dwordx4 v[36:37], v[60:63], off offset:192
	v_add_co_u32_e32 v36, vcc, s10, v134
	s_mov_b64 s[10:11], 0x9000
	s_nop 0
	v_addc_co_u32_e32 v37, vcc, 0, v135, vcc
	global_store_dwordx4 v[36:37], v[28:31], off
	global_store_dwordx4 v[36:37], v[24:27], off offset:64
	global_store_dwordx4 v[36:37], v[20:23], off offset:128
	global_store_dwordx4 v[36:37], v[12:15], off offset:192
	s_nop 1
	v_add_co_u32_e32 v14, vcc, 0x9000, v134
	v_lshl_add_u64 v[12:13], v[134:135], 0, s[10:11]
	s_nop 0
	v_addc_co_u32_e32 v15, vcc, 0, v135, vcc
	global_store_dwordx4 v[14:15], v[64:67], off
	global_store_dwordx4 v[12:13], v[48:51], off offset:64
	global_store_dwordx4 v[12:13], v[40:43], off offset:128
	global_store_dwordx4 v[12:13], v[32:35], off offset:192
	v_add_co_u32_e32 v12, vcc, 0x29000, v134
	s_nop 1
	v_addc_co_u32_e32 v13, vcc, 0, v135, vcc
	s_and_b64 vcc, exec, s[4:5]
	global_store_dwordx4 v[12:13], v[16:19], off
	global_store_dwordx4 v[12:13], v[8:11], off offset:64
	global_store_dwordx4 v[12:13], v[4:7], off offset:128
	global_store_dwordx4 v[12:13], v[0:3], off offset:192
	s_cbranch_vccz .LBB0_1633
	s_branch .LBB0_1642
